# C5 with every s_setprio removed from the 12 GEMM K-loops
# speedup vs baseline: 1.0054x; 1.0054x over previous
; #define PG8_STAGE(bufoff, gbase, voff) do { _Pragma("unroll") for (int _i = 0; _i < 2; ++_i) \
;         __builtin_amdgcn_global_load_lds((const __attribute__((address_space(1))) unsigned*)((const __attribute__((address_space(1))) char*)(gbase) + (unsigned)lnd_v((int)(voff)[_i])), (LAS unsigned*)(lds + (bufoff) + ldsw + _i * 8192), 16, 0, 0); } while (0)
; #define PG8_LDA(dst, b, h) do { _Pragma("unroll") for (int m = 0; m < 4; ++m) _Pragma("unroll") for (int k = 0; k < 2; ++k) dst[m][k] = *(const LAS bf16x8*)(lds + PG8_SA(b, h) + aoff + m * 2048 + k * 1024); } while (0)
; #define PG8_LDB(dst, b, h) do { _Pragma("unroll") for (int n = 0; n < 2; ++n) _Pragma("unroll") for (int k = 0; k < 2; ++k) dst[n][k] = *(const LAS bf16x8*)(lds + PG8_SB(b, h) + boff + n * 2048 + k * 1024); } while (0)
; #define PG8_MMA(ai, bj, At, Bt) do { __builtin_amdgcn_s_setprio(1); _Pragma("unroll") for (int m = 0; m < 4; ++m) _Pragma("unroll") for (int n = 0; n < 2; ++n) _Pragma("unroll") for (int k = 0; k < 2; ++k) \
;         acc[ai][bj][m][n] = __builtin_amdgcn_mfma_f32_16x16x32_bf16(Bt[n][k], At[m][k], acc[ai][bj][m][n], 0, 0, 0); __builtin_amdgcn_s_setprio(0); } while (0)
; #define PG8_WAIT_V(n) asm volatile("s_waitcnt vmcnt(" #n ")" ::: "memory")
; #define PG8_WAIT_L(n) asm volatile("s_waitcnt lgkmcnt(" #n ")" ::: "memory")
; #define PG8_BAR __builtin_amdgcn_s_barrier()
; #define PG8_SCHED __builtin_amdgcn_sched_barrier(0)
; template <class Desc, class Epi>
; __device__ __forceinline__ void gemm_phase(const int wv_, LAS unsigned char* lds, const Desc& d, const Epi& E) {
;     ...
;             const char* a1 = cA + (size_t)(t + 1) * kstep;
;             const char* a2 = last ? nA : cA + (size_t)(t + 2) * kstep; const char* b2 = last ? nB : cB + (size_t)(t + 2) * kstep;
;             const char* a3 = a2 + kstep; const char* b3 = b2 + kstep;
;             PG8_LDB(B0, 0, 0); PG8_LDB(B1, 0, 1); PG8_SCHED; PG8_LDA(At, 0, 0); PG8_STAGE(PG8_SA(1, 1), a1, voffA1);
;             PG8_WAIT_V(8); PG8_WAIT_L(0); PG8_BAR; PG8_MMA(0, 0, At, B0); PG8_MMA(0, 1, At, B1); PG8_BAR; PG8_SCHED;
;             PG8_LDA(At, 0, 1); PG8_STAGE(PG8_SB(0, 0), b2, voffB); PG8_STAGE(PG8_SB(0, 1), b2 + hstepB, voffB); PG8_STAGE(PG8_SA(0, 0), a2, sA0);
;             PG8_WAIT_V(8); PG8_WAIT_L(0); PG8_BAR; PG8_MMA(1, 0, At, B0); PG8_MMA(1, 1, At, B1); PG8_BAR; PG8_SCHED;
.LBB0_662:
	ds_read_b128 v[154:157], v148
	ds_read_b128 v[158:161], v148 offset:1024
	ds_read_b128 v[162:165], v148 offset:2048
	ds_read_b128 v[166:169], v148 offset:3072
	ds_read_b128 v[170:173], v149
	ds_read_b128 v[174:177], v149 offset:1024
	ds_read_b128 v[178:181], v149 offset:2048
	ds_read_b128 v[182:185], v149 offset:3072
	s_add_u32 s2, s0, 0x80
	s_addc_u32 s3, s1, 0
	s_cmp_eq_u32 s60, 12
	s_cselect_b32 s3, s17, s3
	s_cselect_b32 s2, s16, s2
	s_cselect_b32 s27, s23, s59
	s_cselect_b32 s26, s22, s58
	v_mov_b32_e32 v128, v133
	s_mov_b32 m0, s42
	ds_read_b128 v[186:189], v150
	ds_read_b128 v[190:193], v150 offset:1024
	ds_read_b128 v[194:197], v150 offset:2048
	ds_read_b128 v[198:201], v150 offset:3072
	ds_read_b128 v[202:205], v150 offset:4096
	ds_read_b128 v[206:209], v150 offset:5120
	ds_read_b128 v[210:213], v150 offset:6144
	ds_read_b128 v[214:217], v150 offset:7168
	s_nop 0
	global_load_lds_dwordx4 v128, s[0:1]
	v_mov_b32_e32 v128, v136
	s_mov_b32 m0, s43
	s_nop 0
	global_load_lds_dwordx4 v128, s[0:1]
	s_waitcnt vmcnt(8)
	s_waitcnt lgkmcnt(0)
	s_barrier
	s_waitcnt lgkmcnt(0)
	v_mfma_f32_16x16x32_bf16 v[124:127], v[154:157], v[186:189], v[124:127]
	v_mfma_f32_16x16x32_bf16 v[120:123], v[162:165], v[186:189], v[120:123]
	v_mfma_f32_16x16x32_bf16 v[108:111], v[154:157], v[194:197], v[108:111]
	v_mfma_f32_16x16x32_bf16 v[104:107], v[162:165], v[194:197], v[104:107]
	v_mfma_f32_16x16x32_bf16 v[92:95], v[154:157], v[202:205], v[92:95]
	v_mfma_f32_16x16x32_bf16 v[88:91], v[162:165], v[202:205], v[88:91]
	v_mfma_f32_16x16x32_bf16 v[76:79], v[154:157], v[210:213], v[76:79]
	v_mfma_f32_16x16x32_bf16 v[72:75], v[162:165], v[210:213], v[72:75]
	v_mfma_f32_16x16x32_bf16 v[124:127], v[158:161], v[190:193], v[124:127]
	v_mfma_f32_16x16x32_bf16 v[120:123], v[166:169], v[190:193], v[120:123]
	v_mfma_f32_16x16x32_bf16 v[108:111], v[158:161], v[198:201], v[108:111]
	v_mfma_f32_16x16x32_bf16 v[104:107], v[166:169], v[198:201], v[104:107]
	v_mfma_f32_16x16x32_bf16 v[92:95], v[158:161], v[206:209], v[92:95]
	v_mfma_f32_16x16x32_bf16 v[88:91], v[166:169], v[206:209], v[88:91]
	v_mfma_f32_16x16x32_bf16 v[76:79], v[158:161], v[214:217], v[76:79]
	v_mfma_f32_16x16x32_bf16 v[72:75], v[166:169], v[214:217], v[72:75]
	v_mfma_f32_16x16x32_bf16 v[116:119], v[170:173], v[186:189], v[116:119]
	v_mfma_f32_16x16x32_bf16 v[112:115], v[178:181], v[186:189], v[112:115]
	v_mfma_f32_16x16x32_bf16 v[100:103], v[170:173], v[194:197], v[100:103]
	v_mfma_f32_16x16x32_bf16 v[96:99], v[178:181], v[194:197], v[96:99]
	v_mfma_f32_16x16x32_bf16 v[84:87], v[170:173], v[202:205], v[84:87]
	v_mfma_f32_16x16x32_bf16 v[80:83], v[178:181], v[202:205], v[80:83]
	v_mfma_f32_16x16x32_bf16 v[68:71], v[170:173], v[210:213], v[68:71]
	v_mfma_f32_16x16x32_bf16 v[64:67], v[178:181], v[210:213], v[64:67]
	v_mfma_f32_16x16x32_bf16 v[116:119], v[174:177], v[190:193], v[116:119]
	v_mfma_f32_16x16x32_bf16 v[112:115], v[182:185], v[190:193], v[112:115]
	v_mfma_f32_16x16x32_bf16 v[100:103], v[174:177], v[198:201], v[100:103]
	v_mfma_f32_16x16x32_bf16 v[96:99], v[182:185], v[198:201], v[96:99]
	v_mfma_f32_16x16x32_bf16 v[84:87], v[174:177], v[206:209], v[84:87]
	v_mfma_f32_16x16x32_bf16 v[80:83], v[182:185], v[206:209], v[80:83]
	v_mfma_f32_16x16x32_bf16 v[68:71], v[174:177], v[214:217], v[68:71]
	v_mfma_f32_16x16x32_bf16 v[64:67], v[182:185], v[214:217], v[64:67]
	s_barrier
	v_mov_b32_e32 v128, v134
	s_mov_b32 m0, s44
	ds_read_b128 v[186:189], v150 offset:16384
	ds_read_b128 v[190:193], v150 offset:17408
	ds_read_b128 v[194:197], v150 offset:18432
	ds_read_b128 v[198:201], v150 offset:19456
	ds_read_b128 v[202:205], v150 offset:20480
	ds_read_b128 v[206:209], v150 offset:21504
	ds_read_b128 v[210:213], v150 offset:22528
	ds_read_b128 v[214:217], v150 offset:23552
	s_add_u32 s62, s26, 0x40000
	global_load_lds_dwordx4 v128, s[26:27]
	v_mov_b32_e32 v128, v137
	s_mov_b32 m0, s45
	s_addc_u32 s63, s27, 0
	global_load_lds_dwordx4 v128, s[26:27]
	v_mov_b32_e32 v128, v134
	s_mov_b32 m0, s46
	s_nop 0
	global_load_lds_dwordx4 v128, s[62:63]
	v_mov_b32_e32 v128, v137
	s_mov_b32 m0, s47
	s_nop 0
	global_load_lds_dwordx4 v128, s[62:63]
	v_mov_b32_e32 v128, v132
	s_mov_b32 m0, s36
	s_nop 0
	global_load_lds_dwordx4 v128, s[2:3]
	v_mov_b32_e32 v128, v135
	s_mov_b32 m0, s37
	s_nop 0
	global_load_lds_dwordx4 v128, s[2:3]
	s_waitcnt vmcnt(8)
	s_waitcnt lgkmcnt(0)
	s_barrier
	s_waitcnt lgkmcnt(0)
	v_mfma_f32_16x16x32_bf16 v[60:63], v[154:157], v[186:189], v[60:63]
	v_mfma_f32_16x16x32_bf16 v[56:59], v[162:165], v[186:189], v[56:59]
	v_mfma_f32_16x16x32_bf16 v[44:47], v[154:157], v[194:197], v[44:47]
	v_mfma_f32_16x16x32_bf16 v[32:35], v[162:165], v[194:197], v[32:35]
	v_mfma_f32_16x16x32_bf16 v[16:19], v[154:157], v[202:205], v[16:19]
	v_mfma_f32_16x16x32_bf16 v[8:11], v[162:165], v[202:205], v[8:11]
	v_mfma_f32_16x16x32_bf16 v[4:7], v[154:157], v[210:213], v[4:7]
	v_mfma_f32_16x16x32_bf16 v[0:3], v[162:165], v[210:213], v[0:3]
	v_mfma_f32_16x16x32_bf16 v[60:63], v[158:161], v[190:193], v[60:63]
	v_mfma_f32_16x16x32_bf16 v[56:59], v[166:169], v[190:193], v[56:59]
	v_mfma_f32_16x16x32_bf16 v[44:47], v[158:161], v[198:201], v[44:47]
	v_mfma_f32_16x16x32_bf16 v[32:35], v[166:169], v[198:201], v[32:35]
	v_mfma_f32_16x16x32_bf16 v[16:19], v[158:161], v[206:209], v[16:19]
	v_mfma_f32_16x16x32_bf16 v[8:11], v[166:169], v[206:209], v[8:11]
	v_mfma_f32_16x16x32_bf16 v[4:7], v[158:161], v[214:217], v[4:7]
	v_mfma_f32_16x16x32_bf16 v[0:3], v[166:169], v[214:217], v[0:3]
	v_mfma_f32_16x16x32_bf16 v[52:55], v[170:173], v[186:189], v[52:55]
	v_mfma_f32_16x16x32_bf16 v[48:51], v[178:181], v[186:189], v[48:51]
	v_mfma_f32_16x16x32_bf16 v[28:31], v[170:173], v[194:197], v[28:31]
	v_mfma_f32_16x16x32_bf16 v[12:15], v[178:181], v[194:197], v[12:15]
	v_mfma_f32_16x16x32_bf16 v[36:39], v[170:173], v[202:205], v[36:39]
	v_mfma_f32_16x16x32_bf16 v[40:43], v[178:181], v[202:205], v[40:43]
	v_mfma_f32_16x16x32_bf16 v[20:23], v[170:173], v[210:213], v[20:23]
	v_mfma_f32_16x16x32_bf16 v[24:27], v[178:181], v[210:213], v[24:27]
	v_mfma_f32_16x16x32_bf16 v[52:55], v[174:177], v[190:193], v[52:55]
	v_mfma_f32_16x16x32_bf16 v[48:51], v[182:185], v[190:193], v[48:51]
	v_mfma_f32_16x16x32_bf16 v[28:31], v[174:177], v[198:201], v[28:31]
	v_mfma_f32_16x16x32_bf16 v[12:15], v[182:185], v[198:201], v[12:15]
	v_mfma_f32_16x16x32_bf16 v[36:39], v[174:177], v[206:209], v[36:39]
	v_mfma_f32_16x16x32_bf16 v[40:43], v[182:185], v[206:209], v[40:43]
	v_mfma_f32_16x16x32_bf16 v[20:23], v[174:177], v[214:217], v[20:23]
	v_mfma_f32_16x16x32_bf16 v[24:27], v[182:185], v[214:217], v[24:27]
	s_barrier
; #define PG8_STAGE(bufoff, gbase, voff) do { _Pragma("unroll") for (int _i = 0; _i < 2; ++_i) \
;         __builtin_amdgcn_global_load_lds((const __attribute__((address_space(1))) unsigned*)((const __attribute__((address_space(1))) char*)(gbase) + (unsigned)lnd_v((int)(voff)[_i])), (LAS unsigned*)(lds + (bufoff) + ldsw + _i * 8192), 16, 0, 0); } while (0)
; #define PG8_LDA(dst, b, h) do { _Pragma("unroll") for (int m = 0; m < 4; ++m) _Pragma("unroll") for (int k = 0; k < 2; ++k) dst[m][k] = *(const LAS bf16x8*)(lds + PG8_SA(b, h) + aoff + m * 2048 + k * 1024); } while (0)
; #define PG8_LDB(dst, b, h) do { _Pragma("unroll") for (int n = 0; n < 2; ++n) _Pragma("unroll") for (int k = 0; k < 2; ++k) dst[n][k] = *(const LAS bf16x8*)(lds + PG8_SB(b, h) + boff + n * 2048 + k * 1024); } while (0)
; #define PG8_MMA(ai, bj, At, Bt) do { __builtin_amdgcn_s_setprio(1); _Pragma("unroll") for (int m = 0; m < 4; ++m) _Pragma("unroll") for (int n = 0; n < 2; ++n) _Pragma("unroll") for (int k = 0; k < 2; ++k) \
;         acc[ai][bj][m][n] = __builtin_amdgcn_mfma_f32_16x16x32_bf16(Bt[n][k], At[m][k], acc[ai][bj][m][n], 0, 0, 0); __builtin_amdgcn_s_setprio(0); } while (0)
; #define PG8_WAIT_V(n) asm volatile("s_waitcnt vmcnt(" #n ")" ::: "memory")
; #define PG8_WAIT_L(n) asm volatile("s_waitcnt lgkmcnt(" #n ")" ::: "memory")
; #define PG8_BAR __builtin_amdgcn_s_barrier()
; #define PG8_SCHED __builtin_amdgcn_sched_barrier(0)
; template <class Desc, class Epi>
; __device__ __forceinline__ void gemm_phase(const int wv_, LAS unsigned char* lds, const Desc& d, const Epi& E) {
;     ...
;             PG8_LDB(B0, 1, 0); PG8_LDB(B1, 1, 1); PG8_SCHED; PG8_LDA(At, 1, 0); PG8_STAGE(PG8_SA(0, 1), a2, sA1);
;             PG8_WAIT_V(8); PG8_WAIT_L(0); PG8_BAR; PG8_MMA(0, 0, At, B0); PG8_MMA(0, 1, At, B1); PG8_BAR; PG8_SCHED;
	ds_read_b128 v[154:157], v151
	ds_read_b128 v[158:161], v151 offset:1024
	ds_read_b128 v[162:165], v151 offset:2048
	ds_read_b128 v[166:169], v151 offset:3072
	ds_read_b128 v[170:173], v152
	ds_read_b128 v[174:177], v152 offset:1024
	ds_read_b128 v[178:181], v152 offset:2048
	ds_read_b128 v[182:185], v152 offset:3072
	v_mov_b32_e32 v128, v133
	s_mov_b32 m0, s38
	ds_read_b128 v[186:189], v150 offset:32768
	ds_read_b128 v[190:193], v150 offset:33792
	ds_read_b128 v[194:197], v150 offset:34816
	ds_read_b128 v[198:201], v150 offset:35840
	ds_read_b128 v[202:205], v150 offset:36864
	ds_read_b128 v[206:209], v150 offset:37888
	ds_read_b128 v[210:213], v150 offset:38912
	ds_read_b128 v[214:217], v150 offset:39936
	s_nop 0
	global_load_lds_dwordx4 v128, s[2:3]
	v_mov_b32_e32 v128, v136
	s_mov_b32 m0, s39
	s_nop 0
	global_load_lds_dwordx4 v128, s[2:3]
	s_waitcnt vmcnt(8)
	s_waitcnt lgkmcnt(0)
	s_barrier
	s_waitcnt lgkmcnt(0)
	v_mfma_f32_16x16x32_bf16 v[124:127], v[154:157], v[186:189], v[124:127]
	v_mfma_f32_16x16x32_bf16 v[120:123], v[162:165], v[186:189], v[120:123]
	v_mfma_f32_16x16x32_bf16 v[108:111], v[154:157], v[194:197], v[108:111]
	v_mfma_f32_16x16x32_bf16 v[104:107], v[162:165], v[194:197], v[104:107]
	v_mfma_f32_16x16x32_bf16 v[92:95], v[154:157], v[202:205], v[92:95]
	v_mfma_f32_16x16x32_bf16 v[88:91], v[162:165], v[202:205], v[88:91]
	v_mfma_f32_16x16x32_bf16 v[76:79], v[154:157], v[210:213], v[76:79]
	v_mfma_f32_16x16x32_bf16 v[72:75], v[162:165], v[210:213], v[72:75]
	v_mfma_f32_16x16x32_bf16 v[124:127], v[158:161], v[190:193], v[124:127]
	v_mfma_f32_16x16x32_bf16 v[120:123], v[166:169], v[190:193], v[120:123]
	v_mfma_f32_16x16x32_bf16 v[108:111], v[158:161], v[198:201], v[108:111]
	v_mfma_f32_16x16x32_bf16 v[104:107], v[166:169], v[198:201], v[104:107]
	v_mfma_f32_16x16x32_bf16 v[92:95], v[158:161], v[206:209], v[92:95]
	v_mfma_f32_16x16x32_bf16 v[88:91], v[166:169], v[206:209], v[88:91]
	v_mfma_f32_16x16x32_bf16 v[76:79], v[158:161], v[214:217], v[76:79]
	v_mfma_f32_16x16x32_bf16 v[72:75], v[166:169], v[214:217], v[72:75]
	v_mfma_f32_16x16x32_bf16 v[116:119], v[170:173], v[186:189], v[116:119]
	v_mfma_f32_16x16x32_bf16 v[112:115], v[178:181], v[186:189], v[112:115]
	v_mfma_f32_16x16x32_bf16 v[100:103], v[170:173], v[194:197], v[100:103]
	v_mfma_f32_16x16x32_bf16 v[96:99], v[178:181], v[194:197], v[96:99]
	v_mfma_f32_16x16x32_bf16 v[84:87], v[170:173], v[202:205], v[84:87]
	v_mfma_f32_16x16x32_bf16 v[80:83], v[178:181], v[202:205], v[80:83]
	v_mfma_f32_16x16x32_bf16 v[68:71], v[170:173], v[210:213], v[68:71]
	v_mfma_f32_16x16x32_bf16 v[64:67], v[178:181], v[210:213], v[64:67]
	v_mfma_f32_16x16x32_bf16 v[116:119], v[174:177], v[190:193], v[116:119]
	v_mfma_f32_16x16x32_bf16 v[112:115], v[182:185], v[190:193], v[112:115]
	v_mfma_f32_16x16x32_bf16 v[100:103], v[174:177], v[198:201], v[100:103]
	v_mfma_f32_16x16x32_bf16 v[96:99], v[182:185], v[198:201], v[96:99]
	v_mfma_f32_16x16x32_bf16 v[84:87], v[174:177], v[206:209], v[84:87]
	v_mfma_f32_16x16x32_bf16 v[80:83], v[182:185], v[206:209], v[80:83]
	v_mfma_f32_16x16x32_bf16 v[68:71], v[174:177], v[214:217], v[68:71]
	v_mfma_f32_16x16x32_bf16 v[64:67], v[182:185], v[214:217], v[64:67]
	s_barrier
; #define PG8_STAGE(bufoff, gbase, voff) do { _Pragma("unroll") for (int _i = 0; _i < 2; ++_i) \
;         __builtin_amdgcn_global_load_lds((const __attribute__((address_space(1))) unsigned*)((const __attribute__((address_space(1))) char*)(gbase) + (unsigned)lnd_v((int)(voff)[_i])), (LAS unsigned*)(lds + (bufoff) + ldsw + _i * 8192), 16, 0, 0); } while (0)
; #define PG8_LDA(dst, b, h) do { _Pragma("unroll") for (int m = 0; m < 4; ++m) _Pragma("unroll") for (int k = 0; k < 2; ++k) dst[m][k] = *(const LAS bf16x8*)(lds + PG8_SA(b, h) + aoff + m * 2048 + k * 1024); } while (0)
; #define PG8_MMA(ai, bj, At, Bt) do { __builtin_amdgcn_s_setprio(1); _Pragma("unroll") for (int m = 0; m < 4; ++m) _Pragma("unroll") for (int n = 0; n < 2; ++n) _Pragma("unroll") for (int k = 0; k < 2; ++k) \
;         acc[ai][bj][m][n] = __builtin_amdgcn_mfma_f32_16x16x32_bf16(Bt[n][k], At[m][k], acc[ai][bj][m][n], 0, 0, 0); __builtin_amdgcn_s_setprio(0); } while (0)
; #define PG8_WAIT_V(n) asm volatile("s_waitcnt vmcnt(" #n ")" ::: "memory")
; #define PG8_WAIT_L(n) asm volatile("s_waitcnt lgkmcnt(" #n ")" ::: "memory")
; #define PG8_BAR __builtin_amdgcn_s_barrier()
; #define PG8_SCHED __builtin_amdgcn_sched_barrier(0)
; template <class Desc, class Epi>
; __device__ __forceinline__ void gemm_phase(const int wv_, LAS unsigned char* lds, const Desc& d, const Epi& E) {
;     ...
;             PG8_LDA(At, 1, 1); PG8_STAGE(PG8_SB(1, 0), b3, voffB); PG8_STAGE(PG8_SB(1, 1), b3 + hstepB, voffB); PG8_STAGE(PG8_SA(1, 0), a3, sA0);
;             PG8_WAIT_V(8); PG8_WAIT_L(0); PG8_BAR; PG8_MMA(1, 0, At, B0); PG8_MMA(1, 1, At, B1); PG8_BAR; PG8_SCHED;
;         }
;         if (wr == 0) PG8_BAR;
	v_mov_b32_e32 v128, v134
	ds_read_b128 v[186:189], v150 offset:49152
	ds_read_b128 v[190:193], v150 offset:50176
	ds_read_b128 v[194:197], v150 offset:51200
	ds_read_b128 v[198:201], v150 offset:52224
	ds_read_b128 v[202:205], v150 offset:53248
	ds_read_b128 v[206:209], v150 offset:54272
	ds_read_b128 v[210:213], v150 offset:55296
	ds_read_b128 v[214:217], v150 offset:56320
	s_mov_b32 m0, s48
	v_lshl_add_u64 v[130:131], s[26:27], 0, v[128:129]
	v_lshl_add_u64 v[130:131], v[130:131], 0, s[8:9]
	v_mov_b32_e32 v128, v137
	global_load_lds_dwordx4 v[130:131], off
	s_mov_b32 m0, s49
	v_lshl_add_u64 v[130:131], s[26:27], 0, v[128:129]
	v_lshl_add_u64 v[130:131], v[130:131], 0, s[8:9]
	s_add_u32 s26, s26, 0x40080
	v_mov_b32_e32 v128, v134
	global_load_lds_dwordx4 v[130:131], off
	s_addc_u32 s27, s27, 0
	s_mov_b32 m0, s50
	s_nop 0
	global_load_lds_dwordx4 v128, s[26:27]
	v_mov_b32_e32 v128, v137
	s_mov_b32 m0, s51
	s_nop 0
	global_load_lds_dwordx4 v128, s[26:27]
	v_mov_b32_e32 v128, v132
	s_mov_b32 m0, s40
	v_lshl_add_u64 v[130:131], s[2:3], 0, v[128:129]
	v_lshl_add_u64 v[130:131], v[130:131], 0, s[8:9]
	v_mov_b32_e32 v128, v135
	global_load_lds_dwordx4 v[130:131], off
	s_mov_b32 m0, s41
	v_lshl_add_u64 v[130:131], s[2:3], 0, v[128:129]
	v_lshl_add_u64 v[130:131], v[130:131], 0, s[8:9]
	global_load_lds_dwordx4 v[130:131], off
	s_waitcnt vmcnt(8)
	s_waitcnt lgkmcnt(0)
	s_barrier
	s_waitcnt lgkmcnt(0)
	v_mfma_f32_16x16x32_bf16 v[60:63], v[154:157], v[186:189], v[60:63]
	v_mfma_f32_16x16x32_bf16 v[56:59], v[162:165], v[186:189], v[56:59]
	v_mfma_f32_16x16x32_bf16 v[44:47], v[154:157], v[194:197], v[44:47]
	v_mfma_f32_16x16x32_bf16 v[32:35], v[162:165], v[194:197], v[32:35]
	v_mfma_f32_16x16x32_bf16 v[16:19], v[154:157], v[202:205], v[16:19]
	v_mfma_f32_16x16x32_bf16 v[8:11], v[162:165], v[202:205], v[8:11]
	v_mfma_f32_16x16x32_bf16 v[4:7], v[154:157], v[210:213], v[4:7]
	v_mfma_f32_16x16x32_bf16 v[0:3], v[162:165], v[210:213], v[0:3]
	v_mfma_f32_16x16x32_bf16 v[60:63], v[158:161], v[190:193], v[60:63]
	v_mfma_f32_16x16x32_bf16 v[56:59], v[166:169], v[190:193], v[56:59]
	v_mfma_f32_16x16x32_bf16 v[44:47], v[158:161], v[198:201], v[44:47]
	v_mfma_f32_16x16x32_bf16 v[32:35], v[166:169], v[198:201], v[32:35]
	v_mfma_f32_16x16x32_bf16 v[16:19], v[158:161], v[206:209], v[16:19]
	v_mfma_f32_16x16x32_bf16 v[8:11], v[166:169], v[206:209], v[8:11]
	v_mfma_f32_16x16x32_bf16 v[4:7], v[158:161], v[214:217], v[4:7]
	v_mfma_f32_16x16x32_bf16 v[0:3], v[166:169], v[214:217], v[0:3]
	v_mfma_f32_16x16x32_bf16 v[52:55], v[170:173], v[186:189], v[52:55]
	v_mfma_f32_16x16x32_bf16 v[48:51], v[178:181], v[186:189], v[48:51]
	v_mfma_f32_16x16x32_bf16 v[28:31], v[170:173], v[194:197], v[28:31]
	v_mfma_f32_16x16x32_bf16 v[12:15], v[178:181], v[194:197], v[12:15]
	v_mfma_f32_16x16x32_bf16 v[36:39], v[170:173], v[202:205], v[36:39]
	v_mfma_f32_16x16x32_bf16 v[40:43], v[178:181], v[202:205], v[40:43]
	v_mfma_f32_16x16x32_bf16 v[20:23], v[170:173], v[210:213], v[20:23]
	v_mfma_f32_16x16x32_bf16 v[24:27], v[178:181], v[210:213], v[24:27]
	v_mfma_f32_16x16x32_bf16 v[52:55], v[174:177], v[190:193], v[52:55]
	v_mfma_f32_16x16x32_bf16 v[48:51], v[182:185], v[190:193], v[48:51]
	v_mfma_f32_16x16x32_bf16 v[28:31], v[174:177], v[198:201], v[28:31]
	v_mfma_f32_16x16x32_bf16 v[12:15], v[182:185], v[198:201], v[12:15]
	v_mfma_f32_16x16x32_bf16 v[36:39], v[174:177], v[206:209], v[36:39]
	v_mfma_f32_16x16x32_bf16 v[40:43], v[182:185], v[206:209], v[40:43]
	v_mfma_f32_16x16x32_bf16 v[20:23], v[174:177], v[214:217], v[20:23]
	v_mfma_f32_16x16x32_bf16 v[24:27], v[182:185], v[214:217], v[24:27]
	s_barrier
	s_add_i32 s60, s60, 2
	s_add_u32 s0, s0, 0x100
	s_addc_u32 s1, s1, 0
	s_add_u32 s58, s58, 0x100
	s_addc_u32 s59, s59, 0
	s_cmp_gt_u32 s60, 13
	s_cbranch_scc0 .LBB0_662
	s_and_b64 vcc, exec, s[14:15]
	s_cbranch_vccz .LBB0_665
	s_barrier

; #define PG8_STAGE(bufoff, gbase, voff) do { _Pragma("unroll") for (int _i = 0; _i < 2; ++_i) \
;         __builtin_amdgcn_global_load_lds((const __attribute__((address_space(1))) unsigned*)((const __attribute__((address_space(1))) char*)(gbase) + (unsigned)lnd_v((int)(voff)[_i])), (LAS unsigned*)(lds + (bufoff) + ldsw + _i * 8192), 16, 0, 0); } while (0)
; #define PG8_LDA(dst, b, h) do { _Pragma("unroll") for (int m = 0; m < 4; ++m) _Pragma("unroll") for (int k = 0; k < 2; ++k) dst[m][k] = *(const LAS bf16x8*)(lds + PG8_SA(b, h) + aoff + m * 2048 + k * 1024); } while (0)
; #define PG8_LDB(dst, b, h) do { _Pragma("unroll") for (int n = 0; n < 2; ++n) _Pragma("unroll") for (int k = 0; k < 2; ++k) dst[n][k] = *(const LAS bf16x8*)(lds + PG8_SB(b, h) + boff + n * 2048 + k * 1024); } while (0)
; #define PG8_WAIT_V(n) asm volatile("s_waitcnt vmcnt(" #n ")" ::: "memory")
; #define PG8_WAIT_L(n) asm volatile("s_waitcnt lgkmcnt(" #n ")" ::: "memory")
; #define PG8_BAR __builtin_amdgcn_s_barrier()
; template <class Desc, class Epi>
; __device__ __forceinline__ void gemm_phase(const int wv_, LAS unsigned char* lds, const Desc& d, const Epi& E) {
;     ...
;         for (int t = 0; t < nt; t += 2) {
;             const bool last = (t == nt - 2);
;             unsigned sA0[2], sA1[2];
;             if constexpr (Desc::GATHER) { sA0[0] = last ? voffAn[0] : voffA[0]; sA0[1] = last ? voffAn[1] : voffA[1]; sA1[0] = last ? voffAn1[0] : voffA1[0]; sA1[1] = last ? voffAn1[1] : voffA1[1]; }
;             else { sA0[0] = voffA[0]; sA0[1] = voffA[1]; sA1[0] = voffA1[0]; sA1[1] = voffA1[1]; }
;             const char* a1 = cA + (size_t)(t + 1) * kstep;
;             const char* a2 = last ? nA : cA + (size_t)(t + 2) * kstep; const char* b2 = last ? nB : cB + (size_t)(t + 2) * kstep;
;             const char* a3 = a2 + kstep; const char* b3 = b2 + kstep;
;             PG8_LDB(B0, 0, 0); PG8_LDB(B1, 0, 1); PG8_SCHED; PG8_LDA(At, 0, 0); PG8_STAGE(PG8_SA(1, 1), a1, voffA1);
;             PG8_WAIT_V(8); PG8_WAIT_L(0); PG8_BAR; PG8_MMA(0, 0, At, B0); PG8_MMA(0, 1, At, B1); PG8_BAR; PG8_SCHED;
;             PG8_LDA(At, 0, 1); PG8_STAGE(PG8_SB(0, 0), b2, voffB); PG8_STAGE(PG8_SB(0, 1), b2 + hstepB, voffB); PG8_STAGE(PG8_SA(0, 0), a2, sA0);
;             PG8_WAIT_V(8); PG8_WAIT_L(0); PG8_BAR; PG8_MMA(1, 0, At, B0); PG8_MMA(1, 1, At, B1); PG8_BAR; PG8_SCHED;
.LBB0_747:
	s_add_u32 s4, s2, 0x80
	s_addc_u32 s5, s3, 0
	s_add_i32 s63, 0, 0x10000
	s_cmp_eq_u32 s45, 12
	s_cselect_b32 s5, s47, s5
	s_cselect_b32 s4, s46, s4
	v_add_u32_e32 v96, s63, v139
	s_cselect_b32 s21, s49, s43
	s_cselect_b32 s20, s48, s29
	s_add_i32 s66, 0, 0x14000
	ds_read_b128 v[150:153], v96
	ds_read_b128 v[154:157], v96 offset:1024
	ds_read_b128 v[158:161], v96 offset:2048
	ds_read_b128 v[162:165], v96 offset:3072
	v_add_u32_e32 v96, s66, v139
	ds_read_b128 v[166:169], v96
	ds_read_b128 v[170:173], v96 offset:1024
	ds_read_b128 v[174:177], v96 offset:2048
	ds_read_b128 v[178:181], v96 offset:3072
	v_mov_b32_e32 v96, v133
	ds_read_b128 v[182:185], v149
	ds_read_b128 v[186:189], v149 offset:1024
	ds_read_b128 v[190:193], v149 offset:2048
	ds_read_b128 v[194:197], v149 offset:3072
	ds_read_b128 v[198:201], v149 offset:4096
	ds_read_b128 v[202:205], v149 offset:5120
	ds_read_b128 v[206:209], v149 offset:6144
	ds_read_b128 v[210:213], v149 offset:7168
	s_add_i32 m0, s55, 0xc000
	s_nop 0
	global_load_lds_dwordx4 v96, s[2:3]
	v_mov_b32_e32 v96, v136
	s_add_i32 m0, s55, 0xe000
	s_nop 0
	global_load_lds_dwordx4 v96, s[2:3]
	s_waitcnt vmcnt(8)
	s_waitcnt lgkmcnt(0)
	s_barrier
	s_waitcnt lgkmcnt(0)
	v_mfma_f32_16x16x32_bf16 v[126:129], v[150:153], v[182:185], v[126:129]
	v_mfma_f32_16x16x32_bf16 v[122:125], v[158:161], v[182:185], v[122:125]
	v_mfma_f32_16x16x32_bf16 v[110:113], v[150:153], v[190:193], v[110:113]
	v_mfma_f32_16x16x32_bf16 v[106:109], v[158:161], v[190:193], v[106:109]
	v_mfma_f32_16x16x32_bf16 v[92:95], v[150:153], v[198:201], v[92:95]
	v_mfma_f32_16x16x32_bf16 v[88:91], v[158:161], v[198:201], v[88:91]
	v_mfma_f32_16x16x32_bf16 v[76:79], v[150:153], v[206:209], v[76:79]
	v_mfma_f32_16x16x32_bf16 v[72:75], v[158:161], v[206:209], v[72:75]
	v_mfma_f32_16x16x32_bf16 v[126:129], v[154:157], v[186:189], v[126:129]
	v_mfma_f32_16x16x32_bf16 v[122:125], v[162:165], v[186:189], v[122:125]
	v_mfma_f32_16x16x32_bf16 v[110:113], v[154:157], v[194:197], v[110:113]
	v_mfma_f32_16x16x32_bf16 v[106:109], v[162:165], v[194:197], v[106:109]
	v_mfma_f32_16x16x32_bf16 v[92:95], v[154:157], v[202:205], v[92:95]
	v_mfma_f32_16x16x32_bf16 v[88:91], v[162:165], v[202:205], v[88:91]
	v_mfma_f32_16x16x32_bf16 v[76:79], v[154:157], v[210:213], v[76:79]
	v_mfma_f32_16x16x32_bf16 v[72:75], v[162:165], v[210:213], v[72:75]
	v_mfma_f32_16x16x32_bf16 v[118:121], v[166:169], v[182:185], v[118:121]
	v_mfma_f32_16x16x32_bf16 v[114:117], v[174:177], v[182:185], v[114:117]
	v_mfma_f32_16x16x32_bf16 v[102:105], v[166:169], v[190:193], v[102:105]
	v_mfma_f32_16x16x32_bf16 v[98:101], v[174:177], v[190:193], v[98:101]
	v_mfma_f32_16x16x32_bf16 v[84:87], v[166:169], v[198:201], v[84:87]
	v_mfma_f32_16x16x32_bf16 v[80:83], v[174:177], v[198:201], v[80:83]
	v_mfma_f32_16x16x32_bf16 v[68:71], v[166:169], v[206:209], v[68:71]
	v_mfma_f32_16x16x32_bf16 v[64:67], v[174:177], v[206:209], v[64:67]
	v_mfma_f32_16x16x32_bf16 v[118:121], v[170:173], v[186:189], v[118:121]
	v_mfma_f32_16x16x32_bf16 v[114:117], v[178:181], v[186:189], v[114:117]
	v_mfma_f32_16x16x32_bf16 v[102:105], v[170:173], v[194:197], v[102:105]
	v_mfma_f32_16x16x32_bf16 v[98:101], v[178:181], v[194:197], v[98:101]
	v_mfma_f32_16x16x32_bf16 v[84:87], v[170:173], v[202:205], v[84:87]
	v_mfma_f32_16x16x32_bf16 v[80:83], v[178:181], v[202:205], v[80:83]
	v_mfma_f32_16x16x32_bf16 v[68:71], v[170:173], v[210:213], v[68:71]
	v_mfma_f32_16x16x32_bf16 v[64:67], v[178:181], v[210:213], v[64:67]
	s_barrier
	v_mov_b32_e32 v96, v134
	s_add_i32 s63, s63, s54
	ds_read_b128 v[182:185], v149 offset:16384
	ds_read_b128 v[186:189], v149 offset:17408
	ds_read_b128 v[190:193], v149 offset:18432
	ds_read_b128 v[194:197], v149 offset:19456
	ds_read_b128 v[198:201], v149 offset:20480
	ds_read_b128 v[202:205], v149 offset:21504
	ds_read_b128 v[206:209], v149 offset:22528
	ds_read_b128 v[210:213], v149 offset:23552
	s_mov_b32 m0, s63
	s_nop 0
	global_load_lds_dwordx4 v96, s[20:21]
	v_mov_b32_e32 v96, v137
	s_add_i32 m0, s63, 0x2000
	s_add_u32 s64, s20, 0x40000
	global_load_lds_dwordx4 v96, s[20:21]
	s_addc_u32 s65, s21, 0
	v_mov_b32_e32 v96, v134
	s_add_i32 s63, s66, s54
	s_mov_b32 m0, s63
	s_nop 0
	global_load_lds_dwordx4 v96, s[64:65]
	v_mov_b32_e32 v96, v137
	s_add_i32 m0, s63, 0x2000
	s_nop 0
	global_load_lds_dwordx4 v96, s[64:65]
	v_mov_b32_e32 v96, v132
	s_mov_b32 m0, s55
	s_nop 0
	global_load_lds_dwordx4 v96, s[4:5]
	v_mov_b32_e32 v96, v135
	s_mov_b32 m0, s56
	s_nop 0
	global_load_lds_dwordx4 v96, s[4:5]
	s_waitcnt vmcnt(8)
	s_waitcnt lgkmcnt(0)
	s_barrier
; #define PG8_STAGE(bufoff, gbase, voff) do { _Pragma("unroll") for (int _i = 0; _i < 2; ++_i) \
;         __builtin_amdgcn_global_load_lds((const __attribute__((address_space(1))) unsigned*)((const __attribute__((address_space(1))) char*)(gbase) + (unsigned)lnd_v((int)(voff)[_i])), (LAS unsigned*)(lds + (bufoff) + ldsw + _i * 8192), 16, 0, 0); } while (0)
; #define PG8_LDA(dst, b, h) do { _Pragma("unroll") for (int m = 0; m < 4; ++m) _Pragma("unroll") for (int k = 0; k < 2; ++k) dst[m][k] = *(const LAS bf16x8*)(lds + PG8_SA(b, h) + aoff + m * 2048 + k * 1024); } while (0)
; #define PG8_LDB(dst, b, h) do { _Pragma("unroll") for (int n = 0; n < 2; ++n) _Pragma("unroll") for (int k = 0; k < 2; ++k) dst[n][k] = *(const LAS bf16x8*)(lds + PG8_SB(b, h) + boff + n * 2048 + k * 1024); } while (0)
; #define PG8_MMA(ai, bj, At, Bt) do { __builtin_amdgcn_s_setprio(1); _Pragma("unroll") for (int m = 0; m < 4; ++m) _Pragma("unroll") for (int n = 0; n < 2; ++n) _Pragma("unroll") for (int k = 0; k < 2; ++k) \
;         acc[ai][bj][m][n] = __builtin_amdgcn_mfma_f32_16x16x32_bf16(Bt[n][k], At[m][k], acc[ai][bj][m][n], 0, 0, 0); __builtin_amdgcn_s_setprio(0); } while (0)
; #define PG8_WAIT_V(n) asm volatile("s_waitcnt vmcnt(" #n ")" ::: "memory")
; #define PG8_WAIT_L(n) asm volatile("s_waitcnt lgkmcnt(" #n ")" ::: "memory")
; #define PG8_BAR __builtin_amdgcn_s_barrier()
; #define PG8_SCHED __builtin_amdgcn_sched_barrier(0)
; template <class Desc, class Epi>
; __device__ __forceinline__ void gemm_phase(const int wv_, LAS unsigned char* lds, const Desc& d, const Epi& E) {
;     ...
;             PG8_WAIT_V(8); PG8_WAIT_L(0); PG8_BAR; PG8_MMA(1, 0, At, B0); PG8_MMA(1, 1, At, B1); PG8_BAR; PG8_SCHED;
;             PG8_LDB(B0, 1, 0); PG8_LDB(B1, 1, 1); PG8_SCHED; PG8_LDA(At, 1, 0); PG8_STAGE(PG8_SA(0, 1), a2, sA1);
;             PG8_WAIT_V(8); PG8_WAIT_L(0); PG8_BAR; PG8_MMA(0, 0, At, B0); PG8_MMA(0, 1, At, B1); PG8_BAR; PG8_SCHED;
	s_waitcnt lgkmcnt(0)
	v_mfma_f32_16x16x32_bf16 v[60:63], v[150:153], v[182:185], v[60:63]
	v_mfma_f32_16x16x32_bf16 v[56:59], v[158:161], v[182:185], v[56:59]
	v_mfma_f32_16x16x32_bf16 v[44:47], v[150:153], v[190:193], v[44:47]
	v_mfma_f32_16x16x32_bf16 v[32:35], v[158:161], v[190:193], v[32:35]
	v_mfma_f32_16x16x32_bf16 v[16:19], v[150:153], v[198:201], v[16:19]
	v_mfma_f32_16x16x32_bf16 v[8:11], v[158:161], v[198:201], v[8:11]
	v_mfma_f32_16x16x32_bf16 v[4:7], v[150:153], v[206:209], v[4:7]
	v_mfma_f32_16x16x32_bf16 v[0:3], v[158:161], v[206:209], v[0:3]
	v_mfma_f32_16x16x32_bf16 v[60:63], v[154:157], v[186:189], v[60:63]
	v_mfma_f32_16x16x32_bf16 v[56:59], v[162:165], v[186:189], v[56:59]
	v_mfma_f32_16x16x32_bf16 v[44:47], v[154:157], v[194:197], v[44:47]
	v_mfma_f32_16x16x32_bf16 v[32:35], v[162:165], v[194:197], v[32:35]
	v_mfma_f32_16x16x32_bf16 v[16:19], v[154:157], v[202:205], v[16:19]
	v_mfma_f32_16x16x32_bf16 v[8:11], v[162:165], v[202:205], v[8:11]
	v_mfma_f32_16x16x32_bf16 v[4:7], v[154:157], v[210:213], v[4:7]
	v_mfma_f32_16x16x32_bf16 v[0:3], v[162:165], v[210:213], v[0:3]
	v_mfma_f32_16x16x32_bf16 v[52:55], v[166:169], v[182:185], v[52:55]
	v_mfma_f32_16x16x32_bf16 v[48:51], v[174:177], v[182:185], v[48:51]
	v_mfma_f32_16x16x32_bf16 v[28:31], v[166:169], v[190:193], v[28:31]
	v_mfma_f32_16x16x32_bf16 v[12:15], v[174:177], v[190:193], v[12:15]
	v_mfma_f32_16x16x32_bf16 v[36:39], v[166:169], v[198:201], v[36:39]
	v_mfma_f32_16x16x32_bf16 v[40:43], v[174:177], v[198:201], v[40:43]
	v_mfma_f32_16x16x32_bf16 v[20:23], v[166:169], v[206:209], v[20:23]
	v_mfma_f32_16x16x32_bf16 v[24:27], v[174:177], v[206:209], v[24:27]
	v_mfma_f32_16x16x32_bf16 v[52:55], v[170:173], v[186:189], v[52:55]
	v_mfma_f32_16x16x32_bf16 v[48:51], v[178:181], v[186:189], v[48:51]
	v_mfma_f32_16x16x32_bf16 v[28:31], v[170:173], v[194:197], v[28:31]
	v_mfma_f32_16x16x32_bf16 v[12:15], v[178:181], v[194:197], v[12:15]
	v_mfma_f32_16x16x32_bf16 v[36:39], v[170:173], v[202:205], v[36:39]
	v_mfma_f32_16x16x32_bf16 v[40:43], v[178:181], v[202:205], v[40:43]
	v_mfma_f32_16x16x32_bf16 v[20:23], v[170:173], v[210:213], v[20:23]
	v_mfma_f32_16x16x32_bf16 v[24:27], v[178:181], v[210:213], v[24:27]
	s_barrier
	s_add_i32 s63, 0, 0x18000
	v_add_u32_e32 v96, s63, v139
	s_add_i32 s64, 0, 0x1c000
	ds_read_b128 v[150:153], v96
	ds_read_b128 v[154:157], v96 offset:1024
	ds_read_b128 v[158:161], v96 offset:2048
	ds_read_b128 v[162:165], v96 offset:3072
	v_add_u32_e32 v96, s64, v139
	ds_read_b128 v[166:169], v96
	ds_read_b128 v[170:173], v96 offset:1024
	ds_read_b128 v[174:177], v96 offset:2048
	ds_read_b128 v[178:181], v96 offset:3072
	v_mov_b32_e32 v96, v133
	s_mov_b32 m0, s57
	ds_read_b128 v[182:185], v149 offset:32768
	ds_read_b128 v[186:189], v149 offset:33792
	ds_read_b128 v[190:193], v149 offset:34816
	ds_read_b128 v[194:197], v149 offset:35840
	ds_read_b128 v[198:201], v149 offset:36864
	ds_read_b128 v[202:205], v149 offset:37888
	ds_read_b128 v[206:209], v149 offset:38912
	ds_read_b128 v[210:213], v149 offset:39936
	s_nop 0
	global_load_lds_dwordx4 v96, s[4:5]
	v_mov_b32_e32 v96, v136
	s_mov_b32 m0, s58
	s_nop 0
	global_load_lds_dwordx4 v96, s[4:5]
	s_waitcnt vmcnt(8)
	s_waitcnt lgkmcnt(0)
	s_barrier
	s_waitcnt lgkmcnt(0)
	v_mfma_f32_16x16x32_bf16 v[126:129], v[150:153], v[182:185], v[126:129]
	v_mfma_f32_16x16x32_bf16 v[122:125], v[158:161], v[182:185], v[122:125]
	v_mfma_f32_16x16x32_bf16 v[110:113], v[150:153], v[190:193], v[110:113]
	v_mfma_f32_16x16x32_bf16 v[106:109], v[158:161], v[190:193], v[106:109]
	v_mfma_f32_16x16x32_bf16 v[92:95], v[150:153], v[198:201], v[92:95]
	v_mfma_f32_16x16x32_bf16 v[88:91], v[158:161], v[198:201], v[88:91]
	v_mfma_f32_16x16x32_bf16 v[76:79], v[150:153], v[206:209], v[76:79]
	v_mfma_f32_16x16x32_bf16 v[72:75], v[158:161], v[206:209], v[72:75]
	v_mfma_f32_16x16x32_bf16 v[126:129], v[154:157], v[186:189], v[126:129]
	v_mfma_f32_16x16x32_bf16 v[122:125], v[162:165], v[186:189], v[122:125]
	v_mfma_f32_16x16x32_bf16 v[110:113], v[154:157], v[194:197], v[110:113]
	v_mfma_f32_16x16x32_bf16 v[106:109], v[162:165], v[194:197], v[106:109]
	v_mfma_f32_16x16x32_bf16 v[92:95], v[154:157], v[202:205], v[92:95]
	v_mfma_f32_16x16x32_bf16 v[88:91], v[162:165], v[202:205], v[88:91]
	v_mfma_f32_16x16x32_bf16 v[76:79], v[154:157], v[210:213], v[76:79]
	v_mfma_f32_16x16x32_bf16 v[72:75], v[162:165], v[210:213], v[72:75]
	v_mfma_f32_16x16x32_bf16 v[118:121], v[166:169], v[182:185], v[118:121]
	v_mfma_f32_16x16x32_bf16 v[114:117], v[174:177], v[182:185], v[114:117]
	v_mfma_f32_16x16x32_bf16 v[102:105], v[166:169], v[190:193], v[102:105]
	v_mfma_f32_16x16x32_bf16 v[98:101], v[174:177], v[190:193], v[98:101]
	v_mfma_f32_16x16x32_bf16 v[84:87], v[166:169], v[198:201], v[84:87]
	v_mfma_f32_16x16x32_bf16 v[80:83], v[174:177], v[198:201], v[80:83]
	v_mfma_f32_16x16x32_bf16 v[68:71], v[166:169], v[206:209], v[68:71]
	v_mfma_f32_16x16x32_bf16 v[64:67], v[174:177], v[206:209], v[64:67]
	v_mfma_f32_16x16x32_bf16 v[118:121], v[170:173], v[186:189], v[118:121]
	v_mfma_f32_16x16x32_bf16 v[114:117], v[178:181], v[186:189], v[114:117]
	v_mfma_f32_16x16x32_bf16 v[102:105], v[170:173], v[194:197], v[102:105]
	v_mfma_f32_16x16x32_bf16 v[98:101], v[178:181], v[194:197], v[98:101]
	v_mfma_f32_16x16x32_bf16 v[84:87], v[170:173], v[202:205], v[84:87]
	v_mfma_f32_16x16x32_bf16 v[80:83], v[178:181], v[202:205], v[80:83]
	v_mfma_f32_16x16x32_bf16 v[68:71], v[170:173], v[210:213], v[68:71]
	v_mfma_f32_16x16x32_bf16 v[64:67], v[178:181], v[210:213], v[64:67]
	s_barrier
; #define PG8_STAGE(bufoff, gbase, voff) do { _Pragma("unroll") for (int _i = 0; _i < 2; ++_i) \
;         __builtin_amdgcn_global_load_lds((const __attribute__((address_space(1))) unsigned*)((const __attribute__((address_space(1))) char*)(gbase) + (unsigned)lnd_v((int)(voff)[_i])), (LAS unsigned*)(lds + (bufoff) + ldsw + _i * 8192), 16, 0, 0); } while (0)
; #define PG8_LDA(dst, b, h) do { _Pragma("unroll") for (int m = 0; m < 4; ++m) _Pragma("unroll") for (int k = 0; k < 2; ++k) dst[m][k] = *(const LAS bf16x8*)(lds + PG8_SA(b, h) + aoff + m * 2048 + k * 1024); } while (0)
; #define PG8_MMA(ai, bj, At, Bt) do { __builtin_amdgcn_s_setprio(1); _Pragma("unroll") for (int m = 0; m < 4; ++m) _Pragma("unroll") for (int n = 0; n < 2; ++n) _Pragma("unroll") for (int k = 0; k < 2; ++k) \
;         acc[ai][bj][m][n] = __builtin_amdgcn_mfma_f32_16x16x32_bf16(Bt[n][k], At[m][k], acc[ai][bj][m][n], 0, 0, 0); __builtin_amdgcn_s_setprio(0); } while (0)
; #define PG8_WAIT_V(n) asm volatile("s_waitcnt vmcnt(" #n ")" ::: "memory")
; #define PG8_WAIT_L(n) asm volatile("s_waitcnt lgkmcnt(" #n ")" ::: "memory")
; #define PG8_BAR __builtin_amdgcn_s_barrier()
; #define PG8_SCHED __builtin_amdgcn_sched_barrier(0)
; template <class Desc, class Epi>
; __device__ __forceinline__ void gemm_phase(const int wv_, LAS unsigned char* lds, const Desc& d, const Epi& E) {
;     ...
;             PG8_LDA(At, 1, 1); PG8_STAGE(PG8_SB(1, 0), b3, voffB); PG8_STAGE(PG8_SB(1, 1), b3 + hstepB, voffB); PG8_STAGE(PG8_SA(1, 0), a3, sA0);
;             PG8_WAIT_V(8); PG8_WAIT_L(0); PG8_BAR; PG8_MMA(1, 0, At, B0); PG8_MMA(1, 1, At, B1); PG8_BAR; PG8_SCHED;
;         }
;         if (wr == 0) PG8_BAR;
	v_mov_b32_e32 v96, v134
	ds_read_b128 v[182:185], v149 offset:49152
	ds_read_b128 v[186:189], v149 offset:50176
	ds_read_b128 v[190:193], v149 offset:51200
	ds_read_b128 v[194:197], v149 offset:52224
	ds_read_b128 v[198:201], v149 offset:53248
	ds_read_b128 v[202:205], v149 offset:54272
	ds_read_b128 v[206:209], v149 offset:55296
	ds_read_b128 v[210:213], v149 offset:56320
	s_add_i32 s63, s63, s54
	v_lshl_add_u64 v[130:131], s[20:21], 0, v[96:97]
	v_lshl_add_u64 v[130:131], v[130:131], 0, s[30:31]
	s_mov_b32 m0, s63
	v_mov_b32_e32 v96, v137
	global_load_lds_dwordx4 v[130:131], off
	s_add_i32 m0, s63, 0x2000
	s_nop 0
	v_lshl_add_u64 v[130:131], s[20:21], 0, v[96:97]
	s_add_u32 s20, s20, 0x40080
	v_lshl_add_u64 v[130:131], v[130:131], 0, s[30:31]
	s_addc_u32 s21, s21, 0
	v_mov_b32_e32 v96, v134
	s_add_i32 s63, s64, s54
	global_load_lds_dwordx4 v[130:131], off
	s_mov_b32 m0, s63
	s_nop 0
	global_load_lds_dwordx4 v96, s[20:21]
	v_mov_b32_e32 v96, v137
	s_add_i32 m0, s63, 0x2000
	s_nop 0
	global_load_lds_dwordx4 v96, s[20:21]
	v_mov_b32_e32 v96, v132
	s_mov_b32 m0, s59
	v_lshl_add_u64 v[130:131], s[4:5], 0, v[96:97]
	v_lshl_add_u64 v[130:131], v[130:131], 0, s[30:31]
	v_mov_b32_e32 v96, v135
	global_load_lds_dwordx4 v[130:131], off
	s_mov_b32 m0, s60
	v_lshl_add_u64 v[130:131], s[4:5], 0, v[96:97]
	v_lshl_add_u64 v[130:131], v[130:131], 0, s[30:31]
	global_load_lds_dwordx4 v[130:131], off
	s_waitcnt vmcnt(8)
	s_waitcnt lgkmcnt(0)
	s_barrier
	s_waitcnt lgkmcnt(0)
	v_mfma_f32_16x16x32_bf16 v[60:63], v[150:153], v[182:185], v[60:63]
	v_mfma_f32_16x16x32_bf16 v[56:59], v[158:161], v[182:185], v[56:59]
	v_mfma_f32_16x16x32_bf16 v[44:47], v[150:153], v[190:193], v[44:47]
	v_mfma_f32_16x16x32_bf16 v[32:35], v[158:161], v[190:193], v[32:35]
	v_mfma_f32_16x16x32_bf16 v[16:19], v[150:153], v[198:201], v[16:19]
	v_mfma_f32_16x16x32_bf16 v[8:11], v[158:161], v[198:201], v[8:11]
	v_mfma_f32_16x16x32_bf16 v[4:7], v[150:153], v[206:209], v[4:7]
	v_mfma_f32_16x16x32_bf16 v[0:3], v[158:161], v[206:209], v[0:3]
	v_mfma_f32_16x16x32_bf16 v[60:63], v[154:157], v[186:189], v[60:63]
	v_mfma_f32_16x16x32_bf16 v[56:59], v[162:165], v[186:189], v[56:59]
	v_mfma_f32_16x16x32_bf16 v[44:47], v[154:157], v[194:197], v[44:47]
	v_mfma_f32_16x16x32_bf16 v[32:35], v[162:165], v[194:197], v[32:35]
	v_mfma_f32_16x16x32_bf16 v[16:19], v[154:157], v[202:205], v[16:19]
	v_mfma_f32_16x16x32_bf16 v[8:11], v[162:165], v[202:205], v[8:11]
	v_mfma_f32_16x16x32_bf16 v[4:7], v[154:157], v[210:213], v[4:7]
	v_mfma_f32_16x16x32_bf16 v[0:3], v[162:165], v[210:213], v[0:3]
	v_mfma_f32_16x16x32_bf16 v[52:55], v[166:169], v[182:185], v[52:55]
	v_mfma_f32_16x16x32_bf16 v[48:51], v[174:177], v[182:185], v[48:51]
	v_mfma_f32_16x16x32_bf16 v[28:31], v[166:169], v[190:193], v[28:31]
	v_mfma_f32_16x16x32_bf16 v[12:15], v[174:177], v[190:193], v[12:15]
	v_mfma_f32_16x16x32_bf16 v[36:39], v[166:169], v[198:201], v[36:39]
	v_mfma_f32_16x16x32_bf16 v[40:43], v[174:177], v[198:201], v[40:43]
	v_mfma_f32_16x16x32_bf16 v[20:23], v[166:169], v[206:209], v[20:23]
	v_mfma_f32_16x16x32_bf16 v[24:27], v[174:177], v[206:209], v[24:27]
	v_mfma_f32_16x16x32_bf16 v[52:55], v[170:173], v[186:189], v[52:55]
	v_mfma_f32_16x16x32_bf16 v[48:51], v[178:181], v[186:189], v[48:51]
	v_mfma_f32_16x16x32_bf16 v[28:31], v[170:173], v[194:197], v[28:31]
	v_mfma_f32_16x16x32_bf16 v[12:15], v[178:181], v[194:197], v[12:15]
	v_mfma_f32_16x16x32_bf16 v[36:39], v[170:173], v[202:205], v[36:39]
	v_mfma_f32_16x16x32_bf16 v[40:43], v[178:181], v[202:205], v[40:43]
	v_mfma_f32_16x16x32_bf16 v[20:23], v[170:173], v[210:213], v[20:23]
	v_mfma_f32_16x16x32_bf16 v[24:27], v[178:181], v[210:213], v[24:27]
	s_barrier
	s_add_i32 s45, s45, 2
	s_add_u32 s2, s2, 0x100
	s_addc_u32 s3, s3, 0
	s_add_u32 s29, s29, 0x100
	s_addc_u32 s43, s43, 0
	s_cmp_gt_u32 s45, 13
	s_cbranch_scc0 .LBB0_747
	s_and_b64 vcc, exec, s[40:41]
	s_cbranch_vccz .LBB0_750
	s_barrier

; #define PG8_STAGE(bufoff, gbase, voff) do { _Pragma("unroll") for (int _i = 0; _i < 2; ++_i) \
;         __builtin_amdgcn_global_load_lds((const __attribute__((address_space(1))) unsigned*)((const __attribute__((address_space(1))) char*)(gbase) + (unsigned)lnd_v((int)(voff)[_i])), (LAS unsigned*)(lds + (bufoff) + ldsw + _i * 8192), 16, 0, 0); } while (0)
; #define PG8_LDA(dst, b, h) do { _Pragma("unroll") for (int m = 0; m < 4; ++m) _Pragma("unroll") for (int k = 0; k < 2; ++k) dst[m][k] = *(const LAS bf16x8*)(lds + PG8_SA(b, h) + aoff + m * 2048 + k * 1024); } while (0)
; #define PG8_LDB(dst, b, h) do { _Pragma("unroll") for (int n = 0; n < 2; ++n) _Pragma("unroll") for (int k = 0; k < 2; ++k) dst[n][k] = *(const LAS bf16x8*)(lds + PG8_SB(b, h) + boff + n * 2048 + k * 1024); } while (0)
; #define PG8_WAIT_V(n) asm volatile("s_waitcnt vmcnt(" #n ")" ::: "memory")
; #define PG8_BAR __builtin_amdgcn_s_barrier()
; template <class Desc, class Epi>
; __device__ __forceinline__ void gemm_phase(const int wv_, LAS unsigned char* lds, const Desc& d, const Epi& E) {
;     ...
;         const char* nA = has_next ? (const char*)nxt.a : cA; const char* nB = has_next ? (const char*)nxt.b : cB;
;         for (int t = 0; t < nt; t += 2) {
;             const bool last = (t == nt - 2);
;             unsigned sA0[2], sA1[2];
;             if constexpr (Desc::GATHER) { sA0[0] = last ? voffAn[0] : voffA[0]; sA0[1] = last ? voffAn[1] : voffA[1]; sA1[0] = last ? voffAn1[0] : voffA1[0]; sA1[1] = last ? voffAn1[1] : voffA1[1]; }
;             else { sA0[0] = voffA[0]; sA0[1] = voffA[1]; sA1[0] = voffA1[0]; sA1[1] = voffA1[1]; }
;             const char* a1 = cA + (size_t)(t + 1) * kstep;
;             const char* a2 = last ? nA : cA + (size_t)(t + 2) * kstep; const char* b2 = last ? nB : cB + (size_t)(t + 2) * kstep;
;             const char* a3 = a2 + kstep; const char* b3 = b2 + kstep;
;             PG8_LDB(B0, 0, 0); PG8_LDB(B1, 0, 1); PG8_SCHED; PG8_LDA(At, 0, 0); PG8_STAGE(PG8_SA(1, 1), a1, voffA1);
;             PG8_WAIT_V(8); PG8_WAIT_L(0); PG8_BAR; PG8_MMA(0, 0, At, B0); PG8_MMA(0, 1, At, B1); PG8_BAR; PG8_SCHED;
;             PG8_LDA(At, 0, 1); PG8_STAGE(PG8_SB(0, 0), b2, voffB); PG8_STAGE(PG8_SB(0, 1), b2 + hstepB, voffB); PG8_STAGE(PG8_SA(0, 0), a2, sA0);
;             PG8_WAIT_V(8); PG8_WAIT_L(0); PG8_BAR; PG8_MMA(1, 0, At, B0); PG8_MMA(1, 1, At, B1); PG8_BAR; PG8_SCHED;
.LBB0_890:
	s_add_u32 s60, s58, s22
	s_addc_u32 s61, s59, 0
	s_add_u32 s23, s60, 0x100
	s_addc_u32 s24, s61, 0
	s_and_b64 s[4:5], s[20:21], exec
	s_cselect_b32 s4, s50, s23
	s_cselect_b32 s5, s51, s24
	s_add_u32 s22, s56, s22
	s_addc_u32 s23, s57, 0
	s_add_u32 s22, s22, 0x100
	s_addc_u32 s23, s23, 0
	s_add_i32 s82, 0, 0x10000
	s_and_b64 s[20:21], s[20:21], exec
	s_cselect_b32 s21, s53, s23
	s_cselect_b32 s20, s52, s22
	s_add_i32 s23, 0, 0x14000
	v_add_u32_e32 v96, s82, v210
	s_add_i32 s84, s82, s68
	ds_read_b128 v[130:133], v96
	ds_read_b128 v[134:137], v96 offset:1024
	ds_read_b128 v[138:141], v96 offset:2048
	ds_read_b128 v[142:145], v96 offset:3072
	v_add_u32_e32 v96, s23, v210
	s_add_i32 m0, s69, 0xc000
	s_add_i32 s85, s69, 0xe000
	s_add_i32 s80, s84, 0x2000
	ds_read_b128 v[146:149], v96
	ds_read_b128 v[150:153], v96 offset:1024
	ds_read_b128 v[154:157], v96 offset:2048
	ds_read_b128 v[158:161], v96 offset:3072
	s_add_u32 s24, s20, 0x10000
	s_addc_u32 s25, s21, 0
	s_add_i32 s78, 0, 0x18000
	s_add_i32 s81, s23, s68
	s_add_i32 s47, s78, s68
	s_add_i32 s79, s81, 0x2000
	s_add_i32 s49, 0, 0x1c000
	s_add_i32 s29, s47, 0x2000
	s_add_u32 s22, s20, 0x10080
	s_addc_u32 s23, s21, 0
	s_add_i32 s83, s49, s68
	s_add_i32 s82, s83, 0x2000
	v_mov_b32_e32 v96, v204
	ds_read_b128 v[162:165], v222
	ds_read_b128 v[166:169], v222 offset:1024
	ds_read_b128 v[170:173], v222 offset:2048
	ds_read_b128 v[174:177], v222 offset:3072
	ds_read_b128 v[178:181], v222 offset:4096
	ds_read_b128 v[182:185], v222 offset:5120
	ds_read_b128 v[188:191], v222 offset:6144
	ds_read_b128 v[192:195], v222 offset:7168
	s_nop 0
	v_lshl_add_u64 v[196:197], s[60:61], 0, v[96:97]
	v_lshl_add_u64 v[196:197], v[196:197], 0, s[30:31]
	v_mov_b32_e32 v96, v207
	global_load_lds_dwordx4 v[196:197], off
	s_mov_b32 m0, s85
	v_lshl_add_u64 v[196:197], s[60:61], 0, v[96:97]
	v_lshl_add_u64 v[196:197], v[196:197], 0, s[30:31]
	global_load_lds_dwordx4 v[196:197], off
	s_waitcnt vmcnt(8)
	s_waitcnt lgkmcnt(0)
	s_barrier
	s_waitcnt lgkmcnt(0)
	v_mfma_f32_16x16x32_bf16 v[126:129], v[130:133], v[162:165], v[126:129]
	v_mfma_f32_16x16x32_bf16 v[122:125], v[138:141], v[162:165], v[122:125]
	v_mfma_f32_16x16x32_bf16 v[118:121], v[130:133], v[170:173], v[118:121]
	v_mfma_f32_16x16x32_bf16 v[114:117], v[138:141], v[170:173], v[114:117]
	v_mfma_f32_16x16x32_bf16 v[110:113], v[130:133], v[178:181], v[110:113]
	v_mfma_f32_16x16x32_bf16 v[106:109], v[138:141], v[178:181], v[106:109]
	v_mfma_f32_16x16x32_bf16 v[102:105], v[130:133], v[188:191], v[102:105]
	v_mfma_f32_16x16x32_bf16 v[98:101], v[138:141], v[188:191], v[98:101]
	v_mfma_f32_16x16x32_bf16 v[126:129], v[134:137], v[166:169], v[126:129]
	v_mfma_f32_16x16x32_bf16 v[122:125], v[142:145], v[166:169], v[122:125]
	v_mfma_f32_16x16x32_bf16 v[118:121], v[134:137], v[174:177], v[118:121]
	v_mfma_f32_16x16x32_bf16 v[114:117], v[142:145], v[174:177], v[114:117]
	v_mfma_f32_16x16x32_bf16 v[110:113], v[134:137], v[182:185], v[110:113]
	v_mfma_f32_16x16x32_bf16 v[106:109], v[142:145], v[182:185], v[106:109]
	v_mfma_f32_16x16x32_bf16 v[102:105], v[134:137], v[192:195], v[102:105]
	v_mfma_f32_16x16x32_bf16 v[98:101], v[142:145], v[192:195], v[98:101]
	v_mfma_f32_16x16x32_bf16 v[60:63], v[146:149], v[162:165], v[60:63]
	v_mfma_f32_16x16x32_bf16 v[56:59], v[154:157], v[162:165], v[56:59]
	v_mfma_f32_16x16x32_bf16 v[52:55], v[146:149], v[170:173], v[52:55]
	v_mfma_f32_16x16x32_bf16 v[48:51], v[154:157], v[170:173], v[48:51]
	v_mfma_f32_16x16x32_bf16 v[44:47], v[146:149], v[178:181], v[44:47]
	v_mfma_f32_16x16x32_bf16 v[40:43], v[154:157], v[178:181], v[40:43]
	v_mfma_f32_16x16x32_bf16 v[36:39], v[146:149], v[188:191], v[36:39]
	v_mfma_f32_16x16x32_bf16 v[32:35], v[154:157], v[188:191], v[32:35]
	v_mfma_f32_16x16x32_bf16 v[60:63], v[150:153], v[166:169], v[60:63]
	v_mfma_f32_16x16x32_bf16 v[56:59], v[158:161], v[166:169], v[56:59]
	v_mfma_f32_16x16x32_bf16 v[52:55], v[150:153], v[174:177], v[52:55]
	v_mfma_f32_16x16x32_bf16 v[48:51], v[158:161], v[174:177], v[48:51]
	v_mfma_f32_16x16x32_bf16 v[44:47], v[150:153], v[182:185], v[44:47]
	v_mfma_f32_16x16x32_bf16 v[40:43], v[158:161], v[182:185], v[40:43]
	v_mfma_f32_16x16x32_bf16 v[36:39], v[150:153], v[192:195], v[36:39]
	v_mfma_f32_16x16x32_bf16 v[32:35], v[158:161], v[192:195], v[32:35]
	s_barrier
	v_mov_b32_e32 v96, v205
	s_mov_b32 m0, s84
	ds_read_b128 v[162:165], v222 offset:16384
	ds_read_b128 v[166:169], v222 offset:17408
	ds_read_b128 v[170:173], v222 offset:18432
	ds_read_b128 v[174:177], v222 offset:19456
	ds_read_b128 v[178:181], v222 offset:20480
	ds_read_b128 v[182:185], v222 offset:21504
	ds_read_b128 v[188:191], v222 offset:22528
	ds_read_b128 v[192:195], v222 offset:23552
	s_nop 0
	global_load_lds_dwordx4 v96, s[20:21]
	v_mov_b32_e32 v96, v208
	s_mov_b32 m0, s80
	s_nop 0
	global_load_lds_dwordx4 v96, s[20:21]
	v_mov_b32_e32 v96, v205
	s_mov_b32 m0, s81
	s_nop 0
	global_load_lds_dwordx4 v96, s[24:25]
	v_mov_b32_e32 v96, v208
	s_mov_b32 m0, s79
	s_nop 0
	global_load_lds_dwordx4 v96, s[24:25]
	v_mov_b32_e32 v96, v187
	s_mov_b32 m0, s69
	s_nop 0
	global_load_lds_dwordx4 v96, s[4:5]
	v_mov_b32_e32 v96, v206
	s_mov_b32 m0, s70
	s_nop 0
	global_load_lds_dwordx4 v96, s[4:5]
	s_waitcnt vmcnt(8)
	s_waitcnt lgkmcnt(0)
	s_barrier
; #define PG8_STAGE(bufoff, gbase, voff) do { _Pragma("unroll") for (int _i = 0; _i < 2; ++_i) \
;         __builtin_amdgcn_global_load_lds((const __attribute__((address_space(1))) unsigned*)((const __attribute__((address_space(1))) char*)(gbase) + (unsigned)lnd_v((int)(voff)[_i])), (LAS unsigned*)(lds + (bufoff) + ldsw + _i * 8192), 16, 0, 0); } while (0)
; #define PG8_LDA(dst, b, h) do { _Pragma("unroll") for (int m = 0; m < 4; ++m) _Pragma("unroll") for (int k = 0; k < 2; ++k) dst[m][k] = *(const LAS bf16x8*)(lds + PG8_SA(b, h) + aoff + m * 2048 + k * 1024); } while (0)
; #define PG8_LDB(dst, b, h) do { _Pragma("unroll") for (int n = 0; n < 2; ++n) _Pragma("unroll") for (int k = 0; k < 2; ++k) dst[n][k] = *(const LAS bf16x8*)(lds + PG8_SB(b, h) + boff + n * 2048 + k * 1024); } while (0)
; #define PG8_MMA(ai, bj, At, Bt) do { __builtin_amdgcn_s_setprio(1); _Pragma("unroll") for (int m = 0; m < 4; ++m) _Pragma("unroll") for (int n = 0; n < 2; ++n) _Pragma("unroll") for (int k = 0; k < 2; ++k) \
;         acc[ai][bj][m][n] = __builtin_amdgcn_mfma_f32_16x16x32_bf16(Bt[n][k], At[m][k], acc[ai][bj][m][n], 0, 0, 0); __builtin_amdgcn_s_setprio(0); } while (0)
; #define PG8_WAIT_V(n) asm volatile("s_waitcnt vmcnt(" #n ")" ::: "memory")
; #define PG8_WAIT_L(n) asm volatile("s_waitcnt lgkmcnt(" #n ")" ::: "memory")
; #define PG8_BAR __builtin_amdgcn_s_barrier()
; #define PG8_SCHED __builtin_amdgcn_sched_barrier(0)
; template <class Desc, class Epi>
; __device__ __forceinline__ void gemm_phase(const int wv_, LAS unsigned char* lds, const Desc& d, const Epi& E) {
;     ...
;             PG8_WAIT_V(8); PG8_WAIT_L(0); PG8_BAR; PG8_MMA(1, 0, At, B0); PG8_MMA(1, 1, At, B1); PG8_BAR; PG8_SCHED;
;             PG8_LDB(B0, 1, 0); PG8_LDB(B1, 1, 1); PG8_SCHED; PG8_LDA(At, 1, 0); PG8_STAGE(PG8_SA(0, 1), a2, sA1);
;             PG8_WAIT_V(8); PG8_WAIT_L(0); PG8_BAR; PG8_MMA(0, 0, At, B0); PG8_MMA(0, 1, At, B1); PG8_BAR; PG8_SCHED;
	s_waitcnt lgkmcnt(0)
	v_mfma_f32_16x16x32_bf16 v[92:95], v[130:133], v[162:165], v[92:95]
	v_mfma_f32_16x16x32_bf16 v[88:91], v[138:141], v[162:165], v[88:91]
	v_mfma_f32_16x16x32_bf16 v[84:87], v[130:133], v[170:173], v[84:87]
	v_mfma_f32_16x16x32_bf16 v[80:83], v[138:141], v[170:173], v[80:83]
	v_mfma_f32_16x16x32_bf16 v[76:79], v[130:133], v[178:181], v[76:79]
	v_mfma_f32_16x16x32_bf16 v[72:75], v[138:141], v[178:181], v[72:75]
	v_mfma_f32_16x16x32_bf16 v[68:71], v[130:133], v[188:191], v[68:71]
	v_mfma_f32_16x16x32_bf16 v[64:67], v[138:141], v[188:191], v[64:67]
	v_mfma_f32_16x16x32_bf16 v[92:95], v[134:137], v[166:169], v[92:95]
	v_mfma_f32_16x16x32_bf16 v[88:91], v[142:145], v[166:169], v[88:91]
	v_mfma_f32_16x16x32_bf16 v[84:87], v[134:137], v[174:177], v[84:87]
	v_mfma_f32_16x16x32_bf16 v[80:83], v[142:145], v[174:177], v[80:83]
	v_mfma_f32_16x16x32_bf16 v[76:79], v[134:137], v[182:185], v[76:79]
	v_mfma_f32_16x16x32_bf16 v[72:75], v[142:145], v[182:185], v[72:75]
	v_mfma_f32_16x16x32_bf16 v[68:71], v[134:137], v[192:195], v[68:71]
	v_mfma_f32_16x16x32_bf16 v[64:67], v[142:145], v[192:195], v[64:67]
	v_mfma_f32_16x16x32_bf16 v[28:31], v[146:149], v[162:165], v[28:31]
	v_mfma_f32_16x16x32_bf16 v[24:27], v[154:157], v[162:165], v[24:27]
	v_mfma_f32_16x16x32_bf16 v[12:15], v[146:149], v[170:173], v[12:15]
	v_mfma_f32_16x16x32_bf16 v[8:11], v[154:157], v[170:173], v[8:11]
	v_mfma_f32_16x16x32_bf16 v[20:23], v[146:149], v[178:181], v[20:23]
	v_mfma_f32_16x16x32_bf16 v[16:19], v[154:157], v[178:181], v[16:19]
	v_mfma_f32_16x16x32_bf16 v[4:7], v[146:149], v[188:191], v[4:7]
	v_mfma_f32_16x16x32_bf16 v[0:3], v[154:157], v[188:191], v[0:3]
	v_mfma_f32_16x16x32_bf16 v[28:31], v[150:153], v[166:169], v[28:31]
	v_mfma_f32_16x16x32_bf16 v[24:27], v[158:161], v[166:169], v[24:27]
	v_mfma_f32_16x16x32_bf16 v[12:15], v[150:153], v[174:177], v[12:15]
	v_mfma_f32_16x16x32_bf16 v[8:11], v[158:161], v[174:177], v[8:11]
	v_mfma_f32_16x16x32_bf16 v[20:23], v[150:153], v[182:185], v[20:23]
	v_mfma_f32_16x16x32_bf16 v[16:19], v[158:161], v[182:185], v[16:19]
	v_mfma_f32_16x16x32_bf16 v[4:7], v[150:153], v[192:195], v[4:7]
	v_mfma_f32_16x16x32_bf16 v[0:3], v[158:161], v[192:195], v[0:3]
	s_barrier
	v_add_u32_e32 v96, s78, v210
	ds_read_b128 v[130:133], v96
	ds_read_b128 v[134:137], v96 offset:1024
	ds_read_b128 v[138:141], v96 offset:2048
	ds_read_b128 v[142:145], v96 offset:3072
	v_add_u32_e32 v96, s49, v210
	ds_read_b128 v[146:149], v96
	ds_read_b128 v[150:153], v96 offset:1024
	ds_read_b128 v[154:157], v96 offset:2048
	ds_read_b128 v[158:161], v96 offset:3072
	v_mov_b32_e32 v96, v204
	s_mov_b32 m0, s71
	ds_read_b128 v[162:165], v222 offset:32768
	ds_read_b128 v[166:169], v222 offset:33792
	ds_read_b128 v[170:173], v222 offset:34816
	ds_read_b128 v[174:177], v222 offset:35840
	ds_read_b128 v[178:181], v222 offset:36864
	ds_read_b128 v[182:185], v222 offset:37888
	ds_read_b128 v[188:191], v222 offset:38912
	ds_read_b128 v[192:195], v222 offset:39936
	s_nop 0
	global_load_lds_dwordx4 v96, s[4:5]
	v_mov_b32_e32 v96, v207
	s_mov_b32 m0, s72
	s_nop 0
	global_load_lds_dwordx4 v96, s[4:5]
	s_waitcnt vmcnt(8)
	s_waitcnt lgkmcnt(0)
	s_barrier
	s_waitcnt lgkmcnt(0)
	v_mfma_f32_16x16x32_bf16 v[126:129], v[130:133], v[162:165], v[126:129]
	v_mfma_f32_16x16x32_bf16 v[122:125], v[138:141], v[162:165], v[122:125]
	v_mfma_f32_16x16x32_bf16 v[118:121], v[130:133], v[170:173], v[118:121]
	v_mfma_f32_16x16x32_bf16 v[114:117], v[138:141], v[170:173], v[114:117]
	v_mfma_f32_16x16x32_bf16 v[110:113], v[130:133], v[178:181], v[110:113]
	v_mfma_f32_16x16x32_bf16 v[106:109], v[138:141], v[178:181], v[106:109]
	v_mfma_f32_16x16x32_bf16 v[102:105], v[130:133], v[188:191], v[102:105]
	v_mfma_f32_16x16x32_bf16 v[98:101], v[138:141], v[188:191], v[98:101]
	v_mfma_f32_16x16x32_bf16 v[126:129], v[134:137], v[166:169], v[126:129]
	v_mfma_f32_16x16x32_bf16 v[122:125], v[142:145], v[166:169], v[122:125]
	v_mfma_f32_16x16x32_bf16 v[118:121], v[134:137], v[174:177], v[118:121]
	v_mfma_f32_16x16x32_bf16 v[114:117], v[142:145], v[174:177], v[114:117]
	v_mfma_f32_16x16x32_bf16 v[110:113], v[134:137], v[182:185], v[110:113]
	v_mfma_f32_16x16x32_bf16 v[106:109], v[142:145], v[182:185], v[106:109]
	v_mfma_f32_16x16x32_bf16 v[102:105], v[134:137], v[192:195], v[102:105]
	v_mfma_f32_16x16x32_bf16 v[98:101], v[142:145], v[192:195], v[98:101]
	v_mfma_f32_16x16x32_bf16 v[60:63], v[146:149], v[162:165], v[60:63]
	v_mfma_f32_16x16x32_bf16 v[56:59], v[154:157], v[162:165], v[56:59]
	v_mfma_f32_16x16x32_bf16 v[52:55], v[146:149], v[170:173], v[52:55]
	v_mfma_f32_16x16x32_bf16 v[48:51], v[154:157], v[170:173], v[48:51]
	v_mfma_f32_16x16x32_bf16 v[44:47], v[146:149], v[178:181], v[44:47]
	v_mfma_f32_16x16x32_bf16 v[40:43], v[154:157], v[178:181], v[40:43]
	v_mfma_f32_16x16x32_bf16 v[36:39], v[146:149], v[188:191], v[36:39]
	v_mfma_f32_16x16x32_bf16 v[32:35], v[154:157], v[188:191], v[32:35]
	v_mfma_f32_16x16x32_bf16 v[60:63], v[150:153], v[166:169], v[60:63]
	v_mfma_f32_16x16x32_bf16 v[56:59], v[158:161], v[166:169], v[56:59]
	v_mfma_f32_16x16x32_bf16 v[52:55], v[150:153], v[174:177], v[52:55]
	v_mfma_f32_16x16x32_bf16 v[48:51], v[158:161], v[174:177], v[48:51]
	v_mfma_f32_16x16x32_bf16 v[44:47], v[150:153], v[182:185], v[44:47]
	v_mfma_f32_16x16x32_bf16 v[40:43], v[158:161], v[182:185], v[40:43]
	v_mfma_f32_16x16x32_bf16 v[36:39], v[150:153], v[192:195], v[36:39]
	v_mfma_f32_16x16x32_bf16 v[32:35], v[158:161], v[192:195], v[32:35]
	s_barrier
; #define PG8_STAGE(bufoff, gbase, voff) do { _Pragma("unroll") for (int _i = 0; _i < 2; ++_i) \
;         __builtin_amdgcn_global_load_lds((const __attribute__((address_space(1))) unsigned*)((const __attribute__((address_space(1))) char*)(gbase) + (unsigned)lnd_v((int)(voff)[_i])), (LAS unsigned*)(lds + (bufoff) + ldsw + _i * 8192), 16, 0, 0); } while (0)
; #define PG8_LDA(dst, b, h) do { _Pragma("unroll") for (int m = 0; m < 4; ++m) _Pragma("unroll") for (int k = 0; k < 2; ++k) dst[m][k] = *(const LAS bf16x8*)(lds + PG8_SA(b, h) + aoff + m * 2048 + k * 1024); } while (0)
; #define PG8_MMA(ai, bj, At, Bt) do { __builtin_amdgcn_s_setprio(1); _Pragma("unroll") for (int m = 0; m < 4; ++m) _Pragma("unroll") for (int n = 0; n < 2; ++n) _Pragma("unroll") for (int k = 0; k < 2; ++k) \
;         acc[ai][bj][m][n] = __builtin_amdgcn_mfma_f32_16x16x32_bf16(Bt[n][k], At[m][k], acc[ai][bj][m][n], 0, 0, 0); __builtin_amdgcn_s_setprio(0); } while (0)
; #define PG8_WAIT_V(n) asm volatile("s_waitcnt vmcnt(" #n ")" ::: "memory")
; #define PG8_WAIT_L(n) asm volatile("s_waitcnt lgkmcnt(" #n ")" ::: "memory")
; #define PG8_BAR __builtin_amdgcn_s_barrier()
; #define PG8_SCHED __builtin_amdgcn_sched_barrier(0)
; template <class Desc, class Epi>
; __device__ __forceinline__ void gemm_phase(const int wv_, LAS unsigned char* lds, const Desc& d, const Epi& E) {
;     ...
;             PG8_LDA(At, 1, 1); PG8_STAGE(PG8_SB(1, 0), b3, voffB); PG8_STAGE(PG8_SB(1, 1), b3 + hstepB, voffB); PG8_STAGE(PG8_SA(1, 0), a3, sA0);
;             PG8_WAIT_V(8); PG8_WAIT_L(0); PG8_BAR; PG8_MMA(1, 0, At, B0); PG8_MMA(1, 1, At, B1); PG8_BAR; PG8_SCHED;
;         }
;         if (wr == 0) PG8_BAR;
	v_mov_b32_e32 v96, v205
	ds_read_b128 v[162:165], v222 offset:49152
	ds_read_b128 v[166:169], v222 offset:50176
	ds_read_b128 v[170:173], v222 offset:51200
	ds_read_b128 v[174:177], v222 offset:52224
	ds_read_b128 v[178:181], v222 offset:53248
	ds_read_b128 v[182:185], v222 offset:54272
	ds_read_b128 v[188:191], v222 offset:55296
	ds_read_b128 v[192:195], v222 offset:56320
	s_mov_b32 m0, s47
	v_lshl_add_u64 v[196:197], s[20:21], 0, v[96:97]
	v_lshl_add_u64 v[196:197], v[196:197], 0, s[30:31]
	v_mov_b32_e32 v96, v208
	global_load_lds_dwordx4 v[196:197], off
	s_mov_b32 m0, s29
	v_lshl_add_u64 v[196:197], s[20:21], 0, v[96:97]
	v_lshl_add_u64 v[196:197], v[196:197], 0, s[30:31]
	v_mov_b32_e32 v96, v205
	global_load_lds_dwordx4 v[196:197], off
	s_mov_b32 m0, s83
	s_nop 0
	global_load_lds_dwordx4 v96, s[22:23]
	v_mov_b32_e32 v96, v208
	s_mov_b32 m0, s82
	s_nop 0
	global_load_lds_dwordx4 v96, s[22:23]
	v_mov_b32_e32 v96, v187
	s_mov_b32 m0, s74
	v_lshl_add_u64 v[196:197], s[4:5], 0, v[96:97]
	v_lshl_add_u64 v[196:197], v[196:197], 0, s[30:31]
	v_mov_b32_e32 v96, v206
	global_load_lds_dwordx4 v[196:197], off
	s_mov_b32 m0, s75
	v_lshl_add_u64 v[196:197], s[4:5], 0, v[96:97]
	v_lshl_add_u64 v[196:197], v[196:197], 0, s[30:31]
	global_load_lds_dwordx4 v[196:197], off
	s_waitcnt vmcnt(8)
	s_waitcnt lgkmcnt(0)
	s_barrier
	s_waitcnt lgkmcnt(0)
	v_mfma_f32_16x16x32_bf16 v[92:95], v[130:133], v[162:165], v[92:95]
	v_mfma_f32_16x16x32_bf16 v[88:91], v[138:141], v[162:165], v[88:91]
	v_mfma_f32_16x16x32_bf16 v[84:87], v[130:133], v[170:173], v[84:87]
	v_mfma_f32_16x16x32_bf16 v[80:83], v[138:141], v[170:173], v[80:83]
	v_mfma_f32_16x16x32_bf16 v[76:79], v[130:133], v[178:181], v[76:79]
	v_mfma_f32_16x16x32_bf16 v[72:75], v[138:141], v[178:181], v[72:75]
	v_mfma_f32_16x16x32_bf16 v[68:71], v[130:133], v[188:191], v[68:71]
	v_mfma_f32_16x16x32_bf16 v[64:67], v[138:141], v[188:191], v[64:67]
	v_mfma_f32_16x16x32_bf16 v[92:95], v[134:137], v[166:169], v[92:95]
	v_mfma_f32_16x16x32_bf16 v[88:91], v[142:145], v[166:169], v[88:91]
	v_mfma_f32_16x16x32_bf16 v[84:87], v[134:137], v[174:177], v[84:87]
	v_mfma_f32_16x16x32_bf16 v[80:83], v[142:145], v[174:177], v[80:83]
	v_mfma_f32_16x16x32_bf16 v[76:79], v[134:137], v[182:185], v[76:79]
	v_mfma_f32_16x16x32_bf16 v[72:75], v[142:145], v[182:185], v[72:75]
	v_mfma_f32_16x16x32_bf16 v[68:71], v[134:137], v[192:195], v[68:71]
	v_mfma_f32_16x16x32_bf16 v[64:67], v[142:145], v[192:195], v[64:67]
	v_mfma_f32_16x16x32_bf16 v[28:31], v[146:149], v[162:165], v[28:31]
	v_mfma_f32_16x16x32_bf16 v[24:27], v[154:157], v[162:165], v[24:27]
	v_mfma_f32_16x16x32_bf16 v[12:15], v[146:149], v[170:173], v[12:15]
	v_mfma_f32_16x16x32_bf16 v[8:11], v[154:157], v[170:173], v[8:11]
	v_mfma_f32_16x16x32_bf16 v[20:23], v[146:149], v[178:181], v[20:23]
	v_mfma_f32_16x16x32_bf16 v[16:19], v[154:157], v[178:181], v[16:19]
	v_mfma_f32_16x16x32_bf16 v[4:7], v[146:149], v[188:191], v[4:7]
	v_mfma_f32_16x16x32_bf16 v[0:3], v[154:157], v[188:191], v[0:3]
	v_mfma_f32_16x16x32_bf16 v[28:31], v[150:153], v[166:169], v[28:31]
	v_mfma_f32_16x16x32_bf16 v[24:27], v[158:161], v[166:169], v[24:27]
	v_mfma_f32_16x16x32_bf16 v[12:15], v[150:153], v[174:177], v[12:15]
	v_mfma_f32_16x16x32_bf16 v[8:11], v[158:161], v[174:177], v[8:11]
	v_mfma_f32_16x16x32_bf16 v[20:23], v[150:153], v[182:185], v[20:23]
	v_mfma_f32_16x16x32_bf16 v[16:19], v[158:161], v[182:185], v[16:19]
	v_mfma_f32_16x16x32_bf16 v[4:7], v[150:153], v[192:195], v[4:7]
	v_mfma_f32_16x16x32_bf16 v[0:3], v[158:161], v[192:195], v[0:3]
	s_barrier
	s_movk_i32 s22, 0x100
	s_andn2_b64 vcc, exec, s[2:3]
	s_mov_b64 s[20:21], -1
	s_mov_b64 s[2:3], 0
	s_cbranch_vccz .LBB0_890
	s_and_b64 vcc, exec, s[44:45]
	s_cbranch_vccz .LBB0_893
	s_barrier

; #define PG8_STAGE(bufoff, gbase, voff) do { _Pragma("unroll") for (int _i = 0; _i < 2; ++_i) \
;         __builtin_amdgcn_global_load_lds((const __attribute__((address_space(1))) unsigned*)((const __attribute__((address_space(1))) char*)(gbase) + (unsigned)lnd_v((int)(voff)[_i])), (LAS unsigned*)(lds + (bufoff) + ldsw + _i * 8192), 16, 0, 0); } while (0)
; #define PG8_LDA(dst, b, h) do { _Pragma("unroll") for (int m = 0; m < 4; ++m) _Pragma("unroll") for (int k = 0; k < 2; ++k) dst[m][k] = *(const LAS bf16x8*)(lds + PG8_SA(b, h) + aoff + m * 2048 + k * 1024); } while (0)
; #define PG8_LDB(dst, b, h) do { _Pragma("unroll") for (int n = 0; n < 2; ++n) _Pragma("unroll") for (int k = 0; k < 2; ++k) dst[n][k] = *(const LAS bf16x8*)(lds + PG8_SB(b, h) + boff + n * 2048 + k * 1024); } while (0)
; #define PG8_WAIT_V(n) asm volatile("s_waitcnt vmcnt(" #n ")" ::: "memory")
; #define PG8_BAR __builtin_amdgcn_s_barrier()
; template <class Desc, class Epi>
; __device__ __forceinline__ void gemm_phase(const int wv_, LAS unsigned char* lds, const Desc& d, const Epi& E) {
;     ...
;         const char* nA = has_next ? (const char*)nxt.a : cA; const char* nB = has_next ? (const char*)nxt.b : cB;
;         for (int t = 0; t < nt; t += 2) {
;             const bool last = (t == nt - 2);
;             unsigned sA0[2], sA1[2];
;             if constexpr (Desc::GATHER) { sA0[0] = last ? voffAn[0] : voffA[0]; sA0[1] = last ? voffAn[1] : voffA[1]; sA1[0] = last ? voffAn1[0] : voffA1[0]; sA1[1] = last ? voffAn1[1] : voffA1[1]; }
;             else { sA0[0] = voffA[0]; sA0[1] = voffA[1]; sA1[0] = voffA1[0]; sA1[1] = voffA1[1]; }
;             const char* a1 = cA + (size_t)(t + 1) * kstep;
;             const char* a2 = last ? nA : cA + (size_t)(t + 2) * kstep; const char* b2 = last ? nB : cB + (size_t)(t + 2) * kstep;
;             const char* a3 = a2 + kstep; const char* b3 = b2 + kstep;
;             PG8_LDB(B0, 0, 0); PG8_LDB(B1, 0, 1); PG8_SCHED; PG8_LDA(At, 0, 0); PG8_STAGE(PG8_SA(1, 1), a1, voffA1);
;             PG8_WAIT_V(8); PG8_WAIT_L(0); PG8_BAR; PG8_MMA(0, 0, At, B0); PG8_MMA(0, 1, At, B1); PG8_BAR; PG8_SCHED;
;             PG8_LDA(At, 0, 1); PG8_STAGE(PG8_SB(0, 0), b2, voffB); PG8_STAGE(PG8_SB(0, 1), b2 + hstepB, voffB); PG8_STAGE(PG8_SA(0, 0), a2, sA0);
;             PG8_WAIT_V(8); PG8_WAIT_L(0); PG8_BAR; PG8_MMA(1, 0, At, B0); PG8_MMA(1, 1, At, B1); PG8_BAR; PG8_SCHED;
.LBB0_917:
	s_add_u32 s54, s52, s22
	s_addc_u32 s55, s53, 0
	s_add_u32 s23, s54, 0x100
	s_addc_u32 s24, s55, 0
	s_and_b64 s[4:5], s[20:21], exec
	s_cselect_b32 s4, s44, s23
	s_cselect_b32 s5, s45, s24
	s_add_u32 s22, s50, s22
	s_addc_u32 s23, s51, 0
	s_add_u32 s22, s22, 0x100
	s_addc_u32 s23, s23, 0
	s_add_i32 s80, 0, 0x10000
	s_and_b64 s[20:21], s[20:21], exec
	s_cselect_b32 s21, s47, s23
	s_cselect_b32 s20, s46, s22
	s_add_i32 s23, 0, 0x14000
	v_add_u32_e32 v96, s80, v139
	s_add_i32 s82, s80, s60
	ds_read_b128 v[150:153], v96
	ds_read_b128 v[154:157], v96 offset:1024
	ds_read_b128 v[158:161], v96 offset:2048
	ds_read_b128 v[162:165], v96 offset:3072
	v_add_u32_e32 v96, s23, v139
	s_add_i32 m0, s61, 0xc000
	s_add_i32 s83, s61, 0xe000
	s_add_i32 s78, s82, 0x2000
	ds_read_b128 v[166:169], v96
	ds_read_b128 v[170:173], v96 offset:1024
	ds_read_b128 v[174:177], v96 offset:2048
	ds_read_b128 v[178:181], v96 offset:3072
	s_add_u32 s24, s20, 0x40000
	s_addc_u32 s25, s21, 0
	s_add_i32 s76, 0, 0x18000
	s_add_i32 s79, s23, s60
	s_add_i32 s74, s76, s60
	s_add_i32 s77, s79, 0x2000
	s_add_i32 s75, 0, 0x1c000
	s_add_i32 s29, s74, 0x2000
	s_add_u32 s22, s20, 0x40080
	s_addc_u32 s23, s21, 0
	s_add_i32 s81, s75, s60
	s_add_i32 s80, s81, 0x2000
	v_mov_b32_e32 v96, v133
	ds_read_b128 v[182:185], v149
	ds_read_b128 v[186:189], v149 offset:1024
	ds_read_b128 v[190:193], v149 offset:2048
	ds_read_b128 v[194:197], v149 offset:3072
	ds_read_b128 v[198:201], v149 offset:4096
	ds_read_b128 v[202:205], v149 offset:5120
	ds_read_b128 v[206:209], v149 offset:6144
	ds_read_b128 v[210:213], v149 offset:7168
	s_nop 0
	v_lshl_add_u64 v[130:131], s[54:55], 0, v[96:97]
	v_lshl_add_u64 v[130:131], v[130:131], 0, s[30:31]
	v_mov_b32_e32 v96, v136
	global_load_lds_dwordx4 v[130:131], off
	s_mov_b32 m0, s83
	v_lshl_add_u64 v[130:131], s[54:55], 0, v[96:97]
	v_lshl_add_u64 v[130:131], v[130:131], 0, s[30:31]
	global_load_lds_dwordx4 v[130:131], off
	s_waitcnt vmcnt(8)
	s_waitcnt lgkmcnt(0)
	s_barrier
	s_waitcnt lgkmcnt(0)
	v_mfma_f32_16x16x32_bf16 v[126:129], v[150:153], v[182:185], v[126:129]
	v_mfma_f32_16x16x32_bf16 v[122:125], v[158:161], v[182:185], v[122:125]
	v_mfma_f32_16x16x32_bf16 v[110:113], v[150:153], v[190:193], v[110:113]
	v_mfma_f32_16x16x32_bf16 v[106:109], v[158:161], v[190:193], v[106:109]
	v_mfma_f32_16x16x32_bf16 v[92:95], v[150:153], v[198:201], v[92:95]
	v_mfma_f32_16x16x32_bf16 v[88:91], v[158:161], v[198:201], v[88:91]
	v_mfma_f32_16x16x32_bf16 v[76:79], v[150:153], v[206:209], v[76:79]
	v_mfma_f32_16x16x32_bf16 v[72:75], v[158:161], v[206:209], v[72:75]
	v_mfma_f32_16x16x32_bf16 v[126:129], v[154:157], v[186:189], v[126:129]
	v_mfma_f32_16x16x32_bf16 v[122:125], v[162:165], v[186:189], v[122:125]
	v_mfma_f32_16x16x32_bf16 v[110:113], v[154:157], v[194:197], v[110:113]
	v_mfma_f32_16x16x32_bf16 v[106:109], v[162:165], v[194:197], v[106:109]
	v_mfma_f32_16x16x32_bf16 v[92:95], v[154:157], v[202:205], v[92:95]
	v_mfma_f32_16x16x32_bf16 v[88:91], v[162:165], v[202:205], v[88:91]
	v_mfma_f32_16x16x32_bf16 v[76:79], v[154:157], v[210:213], v[76:79]
	v_mfma_f32_16x16x32_bf16 v[72:75], v[162:165], v[210:213], v[72:75]
	v_mfma_f32_16x16x32_bf16 v[118:121], v[166:169], v[182:185], v[118:121]
	v_mfma_f32_16x16x32_bf16 v[114:117], v[174:177], v[182:185], v[114:117]
	v_mfma_f32_16x16x32_bf16 v[102:105], v[166:169], v[190:193], v[102:105]
	v_mfma_f32_16x16x32_bf16 v[98:101], v[174:177], v[190:193], v[98:101]
	v_mfma_f32_16x16x32_bf16 v[84:87], v[166:169], v[198:201], v[84:87]
	v_mfma_f32_16x16x32_bf16 v[80:83], v[174:177], v[198:201], v[80:83]
	v_mfma_f32_16x16x32_bf16 v[68:71], v[166:169], v[206:209], v[68:71]
	v_mfma_f32_16x16x32_bf16 v[64:67], v[174:177], v[206:209], v[64:67]
	v_mfma_f32_16x16x32_bf16 v[118:121], v[170:173], v[186:189], v[118:121]
	v_mfma_f32_16x16x32_bf16 v[114:117], v[178:181], v[186:189], v[114:117]
	v_mfma_f32_16x16x32_bf16 v[102:105], v[170:173], v[194:197], v[102:105]
	v_mfma_f32_16x16x32_bf16 v[98:101], v[178:181], v[194:197], v[98:101]
	v_mfma_f32_16x16x32_bf16 v[84:87], v[170:173], v[202:205], v[84:87]
	v_mfma_f32_16x16x32_bf16 v[80:83], v[178:181], v[202:205], v[80:83]
	v_mfma_f32_16x16x32_bf16 v[68:71], v[170:173], v[210:213], v[68:71]
	v_mfma_f32_16x16x32_bf16 v[64:67], v[178:181], v[210:213], v[64:67]
	s_barrier
	v_mov_b32_e32 v96, v134
	s_mov_b32 m0, s82
	ds_read_b128 v[182:185], v149 offset:16384
	ds_read_b128 v[186:189], v149 offset:17408
	ds_read_b128 v[190:193], v149 offset:18432
	ds_read_b128 v[194:197], v149 offset:19456
	ds_read_b128 v[198:201], v149 offset:20480
	ds_read_b128 v[202:205], v149 offset:21504
	ds_read_b128 v[206:209], v149 offset:22528
	ds_read_b128 v[210:213], v149 offset:23552
	s_nop 0
	global_load_lds_dwordx4 v96, s[20:21]
	v_mov_b32_e32 v96, v137
	s_mov_b32 m0, s78
	s_nop 0
	global_load_lds_dwordx4 v96, s[20:21]
	v_mov_b32_e32 v96, v134
	s_mov_b32 m0, s79
	s_nop 0
	global_load_lds_dwordx4 v96, s[24:25]
	v_mov_b32_e32 v96, v137
	s_mov_b32 m0, s77
	s_nop 0
	global_load_lds_dwordx4 v96, s[24:25]
	v_mov_b32_e32 v96, v132
	s_mov_b32 m0, s61
	s_nop 0
	global_load_lds_dwordx4 v96, s[4:5]
	v_mov_b32_e32 v96, v135
	s_mov_b32 m0, s63
	s_nop 0
	global_load_lds_dwordx4 v96, s[4:5]
	s_waitcnt vmcnt(8)
	s_waitcnt lgkmcnt(0)
	s_barrier
; #define PG8_STAGE(bufoff, gbase, voff) do { _Pragma("unroll") for (int _i = 0; _i < 2; ++_i) \
;         __builtin_amdgcn_global_load_lds((const __attribute__((address_space(1))) unsigned*)((const __attribute__((address_space(1))) char*)(gbase) + (unsigned)lnd_v((int)(voff)[_i])), (LAS unsigned*)(lds + (bufoff) + ldsw + _i * 8192), 16, 0, 0); } while (0)
; #define PG8_LDA(dst, b, h) do { _Pragma("unroll") for (int m = 0; m < 4; ++m) _Pragma("unroll") for (int k = 0; k < 2; ++k) dst[m][k] = *(const LAS bf16x8*)(lds + PG8_SA(b, h) + aoff + m * 2048 + k * 1024); } while (0)
; #define PG8_LDB(dst, b, h) do { _Pragma("unroll") for (int n = 0; n < 2; ++n) _Pragma("unroll") for (int k = 0; k < 2; ++k) dst[n][k] = *(const LAS bf16x8*)(lds + PG8_SB(b, h) + boff + n * 2048 + k * 1024); } while (0)
; #define PG8_MMA(ai, bj, At, Bt) do { __builtin_amdgcn_s_setprio(1); _Pragma("unroll") for (int m = 0; m < 4; ++m) _Pragma("unroll") for (int n = 0; n < 2; ++n) _Pragma("unroll") for (int k = 0; k < 2; ++k) \
;         acc[ai][bj][m][n] = __builtin_amdgcn_mfma_f32_16x16x32_bf16(Bt[n][k], At[m][k], acc[ai][bj][m][n], 0, 0, 0); __builtin_amdgcn_s_setprio(0); } while (0)
; #define PG8_WAIT_V(n) asm volatile("s_waitcnt vmcnt(" #n ")" ::: "memory")
; #define PG8_WAIT_L(n) asm volatile("s_waitcnt lgkmcnt(" #n ")" ::: "memory")
; #define PG8_BAR __builtin_amdgcn_s_barrier()
; #define PG8_SCHED __builtin_amdgcn_sched_barrier(0)
; template <class Desc, class Epi>
; __device__ __forceinline__ void gemm_phase(const int wv_, LAS unsigned char* lds, const Desc& d, const Epi& E) {
;     ...
;             PG8_WAIT_V(8); PG8_WAIT_L(0); PG8_BAR; PG8_MMA(1, 0, At, B0); PG8_MMA(1, 1, At, B1); PG8_BAR; PG8_SCHED;
;             PG8_LDB(B0, 1, 0); PG8_LDB(B1, 1, 1); PG8_SCHED; PG8_LDA(At, 1, 0); PG8_STAGE(PG8_SA(0, 1), a2, sA1);
;             PG8_WAIT_V(8); PG8_WAIT_L(0); PG8_BAR; PG8_MMA(0, 0, At, B0); PG8_MMA(0, 1, At, B1); PG8_BAR; PG8_SCHED;
	s_waitcnt lgkmcnt(0)
	v_mfma_f32_16x16x32_bf16 v[60:63], v[150:153], v[182:185], v[60:63]
	v_mfma_f32_16x16x32_bf16 v[56:59], v[158:161], v[182:185], v[56:59]
	v_mfma_f32_16x16x32_bf16 v[44:47], v[150:153], v[190:193], v[44:47]
	v_mfma_f32_16x16x32_bf16 v[32:35], v[158:161], v[190:193], v[32:35]
	v_mfma_f32_16x16x32_bf16 v[16:19], v[150:153], v[198:201], v[16:19]
	v_mfma_f32_16x16x32_bf16 v[8:11], v[158:161], v[198:201], v[8:11]
	v_mfma_f32_16x16x32_bf16 v[4:7], v[150:153], v[206:209], v[4:7]
	v_mfma_f32_16x16x32_bf16 v[0:3], v[158:161], v[206:209], v[0:3]
	v_mfma_f32_16x16x32_bf16 v[60:63], v[154:157], v[186:189], v[60:63]
	v_mfma_f32_16x16x32_bf16 v[56:59], v[162:165], v[186:189], v[56:59]
	v_mfma_f32_16x16x32_bf16 v[44:47], v[154:157], v[194:197], v[44:47]
	v_mfma_f32_16x16x32_bf16 v[32:35], v[162:165], v[194:197], v[32:35]
	v_mfma_f32_16x16x32_bf16 v[16:19], v[154:157], v[202:205], v[16:19]
	v_mfma_f32_16x16x32_bf16 v[8:11], v[162:165], v[202:205], v[8:11]
	v_mfma_f32_16x16x32_bf16 v[4:7], v[154:157], v[210:213], v[4:7]
	v_mfma_f32_16x16x32_bf16 v[0:3], v[162:165], v[210:213], v[0:3]
	v_mfma_f32_16x16x32_bf16 v[52:55], v[166:169], v[182:185], v[52:55]
	v_mfma_f32_16x16x32_bf16 v[48:51], v[174:177], v[182:185], v[48:51]
	v_mfma_f32_16x16x32_bf16 v[28:31], v[166:169], v[190:193], v[28:31]
	v_mfma_f32_16x16x32_bf16 v[12:15], v[174:177], v[190:193], v[12:15]
	v_mfma_f32_16x16x32_bf16 v[36:39], v[166:169], v[198:201], v[36:39]
	v_mfma_f32_16x16x32_bf16 v[40:43], v[174:177], v[198:201], v[40:43]
	v_mfma_f32_16x16x32_bf16 v[20:23], v[166:169], v[206:209], v[20:23]
	v_mfma_f32_16x16x32_bf16 v[24:27], v[174:177], v[206:209], v[24:27]
	v_mfma_f32_16x16x32_bf16 v[52:55], v[170:173], v[186:189], v[52:55]
	v_mfma_f32_16x16x32_bf16 v[48:51], v[178:181], v[186:189], v[48:51]
	v_mfma_f32_16x16x32_bf16 v[28:31], v[170:173], v[194:197], v[28:31]
	v_mfma_f32_16x16x32_bf16 v[12:15], v[178:181], v[194:197], v[12:15]
	v_mfma_f32_16x16x32_bf16 v[36:39], v[170:173], v[202:205], v[36:39]
	v_mfma_f32_16x16x32_bf16 v[40:43], v[178:181], v[202:205], v[40:43]
	v_mfma_f32_16x16x32_bf16 v[20:23], v[170:173], v[210:213], v[20:23]
	v_mfma_f32_16x16x32_bf16 v[24:27], v[178:181], v[210:213], v[24:27]
	s_barrier
	v_add_u32_e32 v96, s76, v139
	ds_read_b128 v[150:153], v96
	ds_read_b128 v[154:157], v96 offset:1024
	ds_read_b128 v[158:161], v96 offset:2048
	ds_read_b128 v[162:165], v96 offset:3072
	v_add_u32_e32 v96, s75, v139
	ds_read_b128 v[166:169], v96
	ds_read_b128 v[170:173], v96 offset:1024
	ds_read_b128 v[174:177], v96 offset:2048
	ds_read_b128 v[178:181], v96 offset:3072
	v_mov_b32_e32 v96, v133
	s_mov_b32 m0, s64
	ds_read_b128 v[182:185], v149 offset:32768
	ds_read_b128 v[186:189], v149 offset:33792
	ds_read_b128 v[190:193], v149 offset:34816
	ds_read_b128 v[194:197], v149 offset:35840
	ds_read_b128 v[198:201], v149 offset:36864
	ds_read_b128 v[202:205], v149 offset:37888
	ds_read_b128 v[206:209], v149 offset:38912
	ds_read_b128 v[210:213], v149 offset:39936
	s_nop 0
	global_load_lds_dwordx4 v96, s[4:5]
	v_mov_b32_e32 v96, v136
	s_mov_b32 m0, s65
	s_nop 0
	global_load_lds_dwordx4 v96, s[4:5]
	s_waitcnt vmcnt(8)
	s_waitcnt lgkmcnt(0)
	s_barrier
	s_waitcnt lgkmcnt(0)
	v_mfma_f32_16x16x32_bf16 v[126:129], v[150:153], v[182:185], v[126:129]
	v_mfma_f32_16x16x32_bf16 v[122:125], v[158:161], v[182:185], v[122:125]
	v_mfma_f32_16x16x32_bf16 v[110:113], v[150:153], v[190:193], v[110:113]
	v_mfma_f32_16x16x32_bf16 v[106:109], v[158:161], v[190:193], v[106:109]
	v_mfma_f32_16x16x32_bf16 v[92:95], v[150:153], v[198:201], v[92:95]
	v_mfma_f32_16x16x32_bf16 v[88:91], v[158:161], v[198:201], v[88:91]
	v_mfma_f32_16x16x32_bf16 v[76:79], v[150:153], v[206:209], v[76:79]
	v_mfma_f32_16x16x32_bf16 v[72:75], v[158:161], v[206:209], v[72:75]
	v_mfma_f32_16x16x32_bf16 v[126:129], v[154:157], v[186:189], v[126:129]
	v_mfma_f32_16x16x32_bf16 v[122:125], v[162:165], v[186:189], v[122:125]
	v_mfma_f32_16x16x32_bf16 v[110:113], v[154:157], v[194:197], v[110:113]
	v_mfma_f32_16x16x32_bf16 v[106:109], v[162:165], v[194:197], v[106:109]
	v_mfma_f32_16x16x32_bf16 v[92:95], v[154:157], v[202:205], v[92:95]
	v_mfma_f32_16x16x32_bf16 v[88:91], v[162:165], v[202:205], v[88:91]
	v_mfma_f32_16x16x32_bf16 v[76:79], v[154:157], v[210:213], v[76:79]
	v_mfma_f32_16x16x32_bf16 v[72:75], v[162:165], v[210:213], v[72:75]
	v_mfma_f32_16x16x32_bf16 v[118:121], v[166:169], v[182:185], v[118:121]
	v_mfma_f32_16x16x32_bf16 v[114:117], v[174:177], v[182:185], v[114:117]
	v_mfma_f32_16x16x32_bf16 v[102:105], v[166:169], v[190:193], v[102:105]
	v_mfma_f32_16x16x32_bf16 v[98:101], v[174:177], v[190:193], v[98:101]
	v_mfma_f32_16x16x32_bf16 v[84:87], v[166:169], v[198:201], v[84:87]
	v_mfma_f32_16x16x32_bf16 v[80:83], v[174:177], v[198:201], v[80:83]
	v_mfma_f32_16x16x32_bf16 v[68:71], v[166:169], v[206:209], v[68:71]
	v_mfma_f32_16x16x32_bf16 v[64:67], v[174:177], v[206:209], v[64:67]
	v_mfma_f32_16x16x32_bf16 v[118:121], v[170:173], v[186:189], v[118:121]
	v_mfma_f32_16x16x32_bf16 v[114:117], v[178:181], v[186:189], v[114:117]
	v_mfma_f32_16x16x32_bf16 v[102:105], v[170:173], v[194:197], v[102:105]
	v_mfma_f32_16x16x32_bf16 v[98:101], v[178:181], v[194:197], v[98:101]
	v_mfma_f32_16x16x32_bf16 v[84:87], v[170:173], v[202:205], v[84:87]
	v_mfma_f32_16x16x32_bf16 v[80:83], v[178:181], v[202:205], v[80:83]
	v_mfma_f32_16x16x32_bf16 v[68:71], v[170:173], v[210:213], v[68:71]
	v_mfma_f32_16x16x32_bf16 v[64:67], v[178:181], v[210:213], v[64:67]
	s_barrier
; #define PG8_STAGE(bufoff, gbase, voff) do { _Pragma("unroll") for (int _i = 0; _i < 2; ++_i) \
;         __builtin_amdgcn_global_load_lds((const __attribute__((address_space(1))) unsigned*)((const __attribute__((address_space(1))) char*)(gbase) + (unsigned)lnd_v((int)(voff)[_i])), (LAS unsigned*)(lds + (bufoff) + ldsw + _i * 8192), 16, 0, 0); } while (0)
; #define PG8_LDA(dst, b, h) do { _Pragma("unroll") for (int m = 0; m < 4; ++m) _Pragma("unroll") for (int k = 0; k < 2; ++k) dst[m][k] = *(const LAS bf16x8*)(lds + PG8_SA(b, h) + aoff + m * 2048 + k * 1024); } while (0)
; #define PG8_MMA(ai, bj, At, Bt) do { __builtin_amdgcn_s_setprio(1); _Pragma("unroll") for (int m = 0; m < 4; ++m) _Pragma("unroll") for (int n = 0; n < 2; ++n) _Pragma("unroll") for (int k = 0; k < 2; ++k) \
;         acc[ai][bj][m][n] = __builtin_amdgcn_mfma_f32_16x16x32_bf16(Bt[n][k], At[m][k], acc[ai][bj][m][n], 0, 0, 0); __builtin_amdgcn_s_setprio(0); } while (0)
; #define PG8_WAIT_V(n) asm volatile("s_waitcnt vmcnt(" #n ")" ::: "memory")
; #define PG8_WAIT_L(n) asm volatile("s_waitcnt lgkmcnt(" #n ")" ::: "memory")
; #define PG8_BAR __builtin_amdgcn_s_barrier()
; #define PG8_SCHED __builtin_amdgcn_sched_barrier(0)
; template <class Desc, class Epi>
; __device__ __forceinline__ void gemm_phase(const int wv_, LAS unsigned char* lds, const Desc& d, const Epi& E) {
;     ...
;             PG8_LDA(At, 1, 1); PG8_STAGE(PG8_SB(1, 0), b3, voffB); PG8_STAGE(PG8_SB(1, 1), b3 + hstepB, voffB); PG8_STAGE(PG8_SA(1, 0), a3, sA0);
;             PG8_WAIT_V(8); PG8_WAIT_L(0); PG8_BAR; PG8_MMA(1, 0, At, B0); PG8_MMA(1, 1, At, B1); PG8_BAR; PG8_SCHED;
;         }
;         if (wr == 0) PG8_BAR;
	v_mov_b32_e32 v96, v134
	ds_read_b128 v[182:185], v149 offset:49152
	ds_read_b128 v[186:189], v149 offset:50176
	ds_read_b128 v[190:193], v149 offset:51200
	ds_read_b128 v[194:197], v149 offset:52224
	ds_read_b128 v[198:201], v149 offset:53248
	ds_read_b128 v[202:205], v149 offset:54272
	ds_read_b128 v[206:209], v149 offset:55296
	ds_read_b128 v[210:213], v149 offset:56320
	s_mov_b32 m0, s74
	v_lshl_add_u64 v[130:131], s[20:21], 0, v[96:97]
	v_lshl_add_u64 v[130:131], v[130:131], 0, s[30:31]
	v_mov_b32_e32 v96, v137
	global_load_lds_dwordx4 v[130:131], off
	s_mov_b32 m0, s29
	v_lshl_add_u64 v[130:131], s[20:21], 0, v[96:97]
	v_lshl_add_u64 v[130:131], v[130:131], 0, s[30:31]
	v_mov_b32_e32 v96, v134
	global_load_lds_dwordx4 v[130:131], off
	s_mov_b32 m0, s81
	s_nop 0
	global_load_lds_dwordx4 v96, s[22:23]
	v_mov_b32_e32 v96, v137
	s_mov_b32 m0, s80
	s_nop 0
	global_load_lds_dwordx4 v96, s[22:23]
	v_mov_b32_e32 v96, v132
	s_mov_b32 m0, s68
	v_lshl_add_u64 v[130:131], s[4:5], 0, v[96:97]
	v_lshl_add_u64 v[130:131], v[130:131], 0, s[30:31]
	v_mov_b32_e32 v96, v135
	global_load_lds_dwordx4 v[130:131], off
	s_mov_b32 m0, s69
	v_lshl_add_u64 v[130:131], s[4:5], 0, v[96:97]
	v_lshl_add_u64 v[130:131], v[130:131], 0, s[30:31]
	global_load_lds_dwordx4 v[130:131], off
	s_waitcnt vmcnt(8)
	s_waitcnt lgkmcnt(0)
	s_barrier
	s_waitcnt lgkmcnt(0)
	v_mfma_f32_16x16x32_bf16 v[60:63], v[150:153], v[182:185], v[60:63]
	v_mfma_f32_16x16x32_bf16 v[56:59], v[158:161], v[182:185], v[56:59]
	v_mfma_f32_16x16x32_bf16 v[44:47], v[150:153], v[190:193], v[44:47]
	v_mfma_f32_16x16x32_bf16 v[32:35], v[158:161], v[190:193], v[32:35]
	v_mfma_f32_16x16x32_bf16 v[16:19], v[150:153], v[198:201], v[16:19]
	v_mfma_f32_16x16x32_bf16 v[8:11], v[158:161], v[198:201], v[8:11]
	v_mfma_f32_16x16x32_bf16 v[4:7], v[150:153], v[206:209], v[4:7]
	v_mfma_f32_16x16x32_bf16 v[0:3], v[158:161], v[206:209], v[0:3]
	v_mfma_f32_16x16x32_bf16 v[60:63], v[154:157], v[186:189], v[60:63]
	v_mfma_f32_16x16x32_bf16 v[56:59], v[162:165], v[186:189], v[56:59]
	v_mfma_f32_16x16x32_bf16 v[44:47], v[154:157], v[194:197], v[44:47]
	v_mfma_f32_16x16x32_bf16 v[32:35], v[162:165], v[194:197], v[32:35]
	v_mfma_f32_16x16x32_bf16 v[16:19], v[154:157], v[202:205], v[16:19]
	v_mfma_f32_16x16x32_bf16 v[8:11], v[162:165], v[202:205], v[8:11]
	v_mfma_f32_16x16x32_bf16 v[4:7], v[154:157], v[210:213], v[4:7]
	v_mfma_f32_16x16x32_bf16 v[0:3], v[162:165], v[210:213], v[0:3]
	v_mfma_f32_16x16x32_bf16 v[52:55], v[166:169], v[182:185], v[52:55]
	v_mfma_f32_16x16x32_bf16 v[48:51], v[174:177], v[182:185], v[48:51]
	v_mfma_f32_16x16x32_bf16 v[28:31], v[166:169], v[190:193], v[28:31]
	v_mfma_f32_16x16x32_bf16 v[12:15], v[174:177], v[190:193], v[12:15]
	v_mfma_f32_16x16x32_bf16 v[36:39], v[166:169], v[198:201], v[36:39]
	v_mfma_f32_16x16x32_bf16 v[40:43], v[174:177], v[198:201], v[40:43]
	v_mfma_f32_16x16x32_bf16 v[20:23], v[166:169], v[206:209], v[20:23]
	v_mfma_f32_16x16x32_bf16 v[24:27], v[174:177], v[206:209], v[24:27]
	v_mfma_f32_16x16x32_bf16 v[52:55], v[170:173], v[186:189], v[52:55]
	v_mfma_f32_16x16x32_bf16 v[48:51], v[178:181], v[186:189], v[48:51]
	v_mfma_f32_16x16x32_bf16 v[28:31], v[170:173], v[194:197], v[28:31]
	v_mfma_f32_16x16x32_bf16 v[12:15], v[178:181], v[194:197], v[12:15]
	v_mfma_f32_16x16x32_bf16 v[36:39], v[170:173], v[202:205], v[36:39]
	v_mfma_f32_16x16x32_bf16 v[40:43], v[178:181], v[202:205], v[40:43]
	v_mfma_f32_16x16x32_bf16 v[20:23], v[170:173], v[210:213], v[20:23]
	v_mfma_f32_16x16x32_bf16 v[24:27], v[178:181], v[210:213], v[24:27]
	s_barrier
	s_movk_i32 s22, 0x100
	s_andn2_b64 vcc, exec, s[2:3]
	s_mov_b64 s[20:21], -1
	s_mov_b64 s[2:3], 0
	s_cbranch_vccz .LBB0_917
	s_and_b64 vcc, exec, s[42:43]
	s_cbranch_vccz .LBB0_920
	s_barrier

; #define PG8_STAGE(bufoff, gbase, voff) do { _Pragma("unroll") for (int _i = 0; _i < 2; ++_i) \
;         __builtin_amdgcn_global_load_lds((const __attribute__((address_space(1))) unsigned*)((const __attribute__((address_space(1))) char*)(gbase) + (unsigned)lnd_v((int)(voff)[_i])), (LAS unsigned*)(lds + (bufoff) + ldsw + _i * 8192), 16, 0, 0); } while (0)
; #define PG8_LDA(dst, b, h) do { _Pragma("unroll") for (int m = 0; m < 4; ++m) _Pragma("unroll") for (int k = 0; k < 2; ++k) dst[m][k] = *(const LAS bf16x8*)(lds + PG8_SA(b, h) + aoff + m * 2048 + k * 1024); } while (0)
; #define PG8_LDB(dst, b, h) do { _Pragma("unroll") for (int n = 0; n < 2; ++n) _Pragma("unroll") for (int k = 0; k < 2; ++k) dst[n][k] = *(const LAS bf16x8*)(lds + PG8_SB(b, h) + boff + n * 2048 + k * 1024); } while (0)
; #define PG8_WAIT_V(n) asm volatile("s_waitcnt vmcnt(" #n ")" ::: "memory")
; #define PG8_BAR __builtin_amdgcn_s_barrier()
; template <class Desc, class Epi>
; __device__ __forceinline__ void gemm_phase(const int wv_, LAS unsigned char* lds, const Desc& d, const Epi& E) {
;     ...
;         const char* nA = has_next ? (const char*)nxt.a : cA; const char* nB = has_next ? (const char*)nxt.b : cB;
;         for (int t = 0; t < nt; t += 2) {
;             const bool last = (t == nt - 2);
;             unsigned sA0[2], sA1[2];
;             if constexpr (Desc::GATHER) { sA0[0] = last ? voffAn[0] : voffA[0]; sA0[1] = last ? voffAn[1] : voffA[1]; sA1[0] = last ? voffAn1[0] : voffA1[0]; sA1[1] = last ? voffAn1[1] : voffA1[1]; }
;             else { sA0[0] = voffA[0]; sA0[1] = voffA[1]; sA1[0] = voffA1[0]; sA1[1] = voffA1[1]; }
;             const char* a1 = cA + (size_t)(t + 1) * kstep;
;             const char* a2 = last ? nA : cA + (size_t)(t + 2) * kstep; const char* b2 = last ? nB : cB + (size_t)(t + 2) * kstep;
;             const char* a3 = a2 + kstep; const char* b3 = b2 + kstep;
;             PG8_LDB(B0, 0, 0); PG8_LDB(B1, 0, 1); PG8_SCHED; PG8_LDA(At, 0, 0); PG8_STAGE(PG8_SA(1, 1), a1, voffA1);
;             PG8_WAIT_V(8); PG8_WAIT_L(0); PG8_BAR; PG8_MMA(0, 0, At, B0); PG8_MMA(0, 1, At, B1); PG8_BAR; PG8_SCHED;
;             PG8_LDA(At, 0, 1); PG8_STAGE(PG8_SB(0, 0), b2, voffB); PG8_STAGE(PG8_SB(0, 1), b2 + hstepB, voffB); PG8_STAGE(PG8_SA(0, 0), a2, sA0);
;             PG8_WAIT_V(8); PG8_WAIT_L(0); PG8_BAR; PG8_MMA(1, 0, At, B0); PG8_MMA(1, 1, At, B1); PG8_BAR; PG8_SCHED;
.LBB0_937:
	s_add_u32 s52, s50, s22
	s_addc_u32 s53, s51, 0
	s_add_u32 s23, s52, 0x100
	s_addc_u32 s24, s53, 0
	s_and_b64 s[4:5], s[20:21], exec
	s_cselect_b32 s4, s42, s23
	s_cselect_b32 s5, s43, s24
	s_add_u32 s22, s48, s22
	s_addc_u32 s23, s49, 0
	s_add_u32 s22, s22, 0x100
	s_addc_u32 s23, s23, 0
	s_add_i32 s77, 0, 0x10000
	s_and_b64 s[20:21], s[20:21], exec
	s_cselect_b32 s21, s45, s23
	s_cselect_b32 s20, s44, s22
	s_add_i32 s23, 0, 0x14000
	v_add_u32_e32 v96, s77, v139
	s_add_i32 s79, s77, s59
	ds_read_b128 v[150:153], v96
	ds_read_b128 v[154:157], v96 offset:1024
	ds_read_b128 v[158:161], v96 offset:2048
	ds_read_b128 v[162:165], v96 offset:3072
	v_add_u32_e32 v96, s23, v139
	s_add_i32 m0, s60, 0xc000
	s_add_i32 s80, s60, 0xe000
	s_add_i32 s75, s79, 0x2000
	ds_read_b128 v[166:169], v96
	ds_read_b128 v[170:173], v96 offset:1024
	ds_read_b128 v[174:177], v96 offset:2048
	ds_read_b128 v[178:181], v96 offset:3072
	s_add_u32 s24, s20, 0x40000
	s_addc_u32 s25, s21, 0
	s_add_i32 s73, 0, 0x18000
	s_add_i32 s76, s23, s59
	s_add_i32 s71, s73, s59
	s_add_i32 s74, s76, 0x2000
	s_add_i32 s72, 0, 0x1c000
	s_add_i32 s29, s71, 0x2000
	s_add_u32 s22, s20, 0x40080
	s_addc_u32 s23, s21, 0
	s_add_i32 s78, s72, s59
	s_add_i32 s77, s78, 0x2000
	v_mov_b32_e32 v96, v133
	ds_read_b128 v[182:185], v149
	ds_read_b128 v[186:189], v149 offset:1024
	ds_read_b128 v[190:193], v149 offset:2048
	ds_read_b128 v[194:197], v149 offset:3072
	ds_read_b128 v[198:201], v149 offset:4096
	ds_read_b128 v[202:205], v149 offset:5120
	ds_read_b128 v[206:209], v149 offset:6144
	ds_read_b128 v[210:213], v149 offset:7168
	s_nop 0
	v_lshl_add_u64 v[130:131], s[52:53], 0, v[96:97]
	v_lshl_add_u64 v[130:131], v[130:131], 0, s[30:31]
	v_mov_b32_e32 v96, v136
	global_load_lds_dwordx4 v[130:131], off
	s_mov_b32 m0, s80
	v_lshl_add_u64 v[130:131], s[52:53], 0, v[96:97]
	v_lshl_add_u64 v[130:131], v[130:131], 0, s[30:31]
	global_load_lds_dwordx4 v[130:131], off
	s_waitcnt vmcnt(8)
	s_waitcnt lgkmcnt(0)
	s_barrier
	s_waitcnt lgkmcnt(0)
	v_mfma_f32_16x16x32_bf16 v[126:129], v[150:153], v[182:185], v[126:129]
	v_mfma_f32_16x16x32_bf16 v[122:125], v[158:161], v[182:185], v[122:125]
	v_mfma_f32_16x16x32_bf16 v[110:113], v[150:153], v[190:193], v[110:113]
	v_mfma_f32_16x16x32_bf16 v[106:109], v[158:161], v[190:193], v[106:109]
	v_mfma_f32_16x16x32_bf16 v[92:95], v[150:153], v[198:201], v[92:95]
	v_mfma_f32_16x16x32_bf16 v[88:91], v[158:161], v[198:201], v[88:91]
	v_mfma_f32_16x16x32_bf16 v[76:79], v[150:153], v[206:209], v[76:79]
	v_mfma_f32_16x16x32_bf16 v[72:75], v[158:161], v[206:209], v[72:75]
	v_mfma_f32_16x16x32_bf16 v[126:129], v[154:157], v[186:189], v[126:129]
	v_mfma_f32_16x16x32_bf16 v[122:125], v[162:165], v[186:189], v[122:125]
	v_mfma_f32_16x16x32_bf16 v[110:113], v[154:157], v[194:197], v[110:113]
	v_mfma_f32_16x16x32_bf16 v[106:109], v[162:165], v[194:197], v[106:109]
	v_mfma_f32_16x16x32_bf16 v[92:95], v[154:157], v[202:205], v[92:95]
	v_mfma_f32_16x16x32_bf16 v[88:91], v[162:165], v[202:205], v[88:91]
	v_mfma_f32_16x16x32_bf16 v[76:79], v[154:157], v[210:213], v[76:79]
	v_mfma_f32_16x16x32_bf16 v[72:75], v[162:165], v[210:213], v[72:75]
	v_mfma_f32_16x16x32_bf16 v[118:121], v[166:169], v[182:185], v[118:121]
	v_mfma_f32_16x16x32_bf16 v[114:117], v[174:177], v[182:185], v[114:117]
	v_mfma_f32_16x16x32_bf16 v[102:105], v[166:169], v[190:193], v[102:105]
	v_mfma_f32_16x16x32_bf16 v[98:101], v[174:177], v[190:193], v[98:101]
	v_mfma_f32_16x16x32_bf16 v[84:87], v[166:169], v[198:201], v[84:87]
	v_mfma_f32_16x16x32_bf16 v[80:83], v[174:177], v[198:201], v[80:83]
	v_mfma_f32_16x16x32_bf16 v[68:71], v[166:169], v[206:209], v[68:71]
	v_mfma_f32_16x16x32_bf16 v[64:67], v[174:177], v[206:209], v[64:67]
	v_mfma_f32_16x16x32_bf16 v[118:121], v[170:173], v[186:189], v[118:121]
	v_mfma_f32_16x16x32_bf16 v[114:117], v[178:181], v[186:189], v[114:117]
	v_mfma_f32_16x16x32_bf16 v[102:105], v[170:173], v[194:197], v[102:105]
	v_mfma_f32_16x16x32_bf16 v[98:101], v[178:181], v[194:197], v[98:101]
	v_mfma_f32_16x16x32_bf16 v[84:87], v[170:173], v[202:205], v[84:87]
	v_mfma_f32_16x16x32_bf16 v[80:83], v[178:181], v[202:205], v[80:83]
	v_mfma_f32_16x16x32_bf16 v[68:71], v[170:173], v[210:213], v[68:71]
	v_mfma_f32_16x16x32_bf16 v[64:67], v[178:181], v[210:213], v[64:67]
	s_barrier
	v_mov_b32_e32 v96, v134
	s_mov_b32 m0, s79
	ds_read_b128 v[182:185], v149 offset:16384
	ds_read_b128 v[186:189], v149 offset:17408
	ds_read_b128 v[190:193], v149 offset:18432
	ds_read_b128 v[194:197], v149 offset:19456
	ds_read_b128 v[198:201], v149 offset:20480
	ds_read_b128 v[202:205], v149 offset:21504
	ds_read_b128 v[206:209], v149 offset:22528
	ds_read_b128 v[210:213], v149 offset:23552
	s_nop 0
	global_load_lds_dwordx4 v96, s[20:21]
	v_mov_b32_e32 v96, v137
	s_mov_b32 m0, s75
	s_nop 0
	global_load_lds_dwordx4 v96, s[20:21]
	v_mov_b32_e32 v96, v134
	s_mov_b32 m0, s76
	s_nop 0
	global_load_lds_dwordx4 v96, s[24:25]
	v_mov_b32_e32 v96, v137
	s_mov_b32 m0, s74
	s_nop 0
	global_load_lds_dwordx4 v96, s[24:25]
	v_mov_b32_e32 v96, v132
	s_mov_b32 m0, s60
	s_nop 0
	global_load_lds_dwordx4 v96, s[4:5]
	v_mov_b32_e32 v96, v135
	s_mov_b32 m0, s61
	s_nop 0
	global_load_lds_dwordx4 v96, s[4:5]
	s_waitcnt vmcnt(8)
	s_waitcnt lgkmcnt(0)
	s_barrier
; #define PG8_STAGE(bufoff, gbase, voff) do { _Pragma("unroll") for (int _i = 0; _i < 2; ++_i) \
;         __builtin_amdgcn_global_load_lds((const __attribute__((address_space(1))) unsigned*)((const __attribute__((address_space(1))) char*)(gbase) + (unsigned)lnd_v((int)(voff)[_i])), (LAS unsigned*)(lds + (bufoff) + ldsw + _i * 8192), 16, 0, 0); } while (0)
; #define PG8_LDA(dst, b, h) do { _Pragma("unroll") for (int m = 0; m < 4; ++m) _Pragma("unroll") for (int k = 0; k < 2; ++k) dst[m][k] = *(const LAS bf16x8*)(lds + PG8_SA(b, h) + aoff + m * 2048 + k * 1024); } while (0)
; #define PG8_LDB(dst, b, h) do { _Pragma("unroll") for (int n = 0; n < 2; ++n) _Pragma("unroll") for (int k = 0; k < 2; ++k) dst[n][k] = *(const LAS bf16x8*)(lds + PG8_SB(b, h) + boff + n * 2048 + k * 1024); } while (0)
; #define PG8_MMA(ai, bj, At, Bt) do { __builtin_amdgcn_s_setprio(1); _Pragma("unroll") for (int m = 0; m < 4; ++m) _Pragma("unroll") for (int n = 0; n < 2; ++n) _Pragma("unroll") for (int k = 0; k < 2; ++k) \
;         acc[ai][bj][m][n] = __builtin_amdgcn_mfma_f32_16x16x32_bf16(Bt[n][k], At[m][k], acc[ai][bj][m][n], 0, 0, 0); __builtin_amdgcn_s_setprio(0); } while (0)
; #define PG8_WAIT_V(n) asm volatile("s_waitcnt vmcnt(" #n ")" ::: "memory")
; #define PG8_WAIT_L(n) asm volatile("s_waitcnt lgkmcnt(" #n ")" ::: "memory")
; #define PG8_BAR __builtin_amdgcn_s_barrier()
; #define PG8_SCHED __builtin_amdgcn_sched_barrier(0)
; template <class Desc, class Epi>
; __device__ __forceinline__ void gemm_phase(const int wv_, LAS unsigned char* lds, const Desc& d, const Epi& E) {
;     ...
;             PG8_WAIT_V(8); PG8_WAIT_L(0); PG8_BAR; PG8_MMA(1, 0, At, B0); PG8_MMA(1, 1, At, B1); PG8_BAR; PG8_SCHED;
;             PG8_LDB(B0, 1, 0); PG8_LDB(B1, 1, 1); PG8_SCHED; PG8_LDA(At, 1, 0); PG8_STAGE(PG8_SA(0, 1), a2, sA1);
;             PG8_WAIT_V(8); PG8_WAIT_L(0); PG8_BAR; PG8_MMA(0, 0, At, B0); PG8_MMA(0, 1, At, B1); PG8_BAR; PG8_SCHED;
	s_waitcnt lgkmcnt(0)
	v_mfma_f32_16x16x32_bf16 v[60:63], v[150:153], v[182:185], v[60:63]
	v_mfma_f32_16x16x32_bf16 v[56:59], v[158:161], v[182:185], v[56:59]
	v_mfma_f32_16x16x32_bf16 v[44:47], v[150:153], v[190:193], v[44:47]
	v_mfma_f32_16x16x32_bf16 v[32:35], v[158:161], v[190:193], v[32:35]
	v_mfma_f32_16x16x32_bf16 v[16:19], v[150:153], v[198:201], v[16:19]
	v_mfma_f32_16x16x32_bf16 v[8:11], v[158:161], v[198:201], v[8:11]
	v_mfma_f32_16x16x32_bf16 v[4:7], v[150:153], v[206:209], v[4:7]
	v_mfma_f32_16x16x32_bf16 v[0:3], v[158:161], v[206:209], v[0:3]
	v_mfma_f32_16x16x32_bf16 v[60:63], v[154:157], v[186:189], v[60:63]
	v_mfma_f32_16x16x32_bf16 v[56:59], v[162:165], v[186:189], v[56:59]
	v_mfma_f32_16x16x32_bf16 v[44:47], v[154:157], v[194:197], v[44:47]
	v_mfma_f32_16x16x32_bf16 v[32:35], v[162:165], v[194:197], v[32:35]
	v_mfma_f32_16x16x32_bf16 v[16:19], v[154:157], v[202:205], v[16:19]
	v_mfma_f32_16x16x32_bf16 v[8:11], v[162:165], v[202:205], v[8:11]
	v_mfma_f32_16x16x32_bf16 v[4:7], v[154:157], v[210:213], v[4:7]
	v_mfma_f32_16x16x32_bf16 v[0:3], v[162:165], v[210:213], v[0:3]
	v_mfma_f32_16x16x32_bf16 v[52:55], v[166:169], v[182:185], v[52:55]
	v_mfma_f32_16x16x32_bf16 v[48:51], v[174:177], v[182:185], v[48:51]
	v_mfma_f32_16x16x32_bf16 v[28:31], v[166:169], v[190:193], v[28:31]
	v_mfma_f32_16x16x32_bf16 v[12:15], v[174:177], v[190:193], v[12:15]
	v_mfma_f32_16x16x32_bf16 v[36:39], v[166:169], v[198:201], v[36:39]
	v_mfma_f32_16x16x32_bf16 v[40:43], v[174:177], v[198:201], v[40:43]
	v_mfma_f32_16x16x32_bf16 v[20:23], v[166:169], v[206:209], v[20:23]
	v_mfma_f32_16x16x32_bf16 v[24:27], v[174:177], v[206:209], v[24:27]
	v_mfma_f32_16x16x32_bf16 v[52:55], v[170:173], v[186:189], v[52:55]
	v_mfma_f32_16x16x32_bf16 v[48:51], v[178:181], v[186:189], v[48:51]
	v_mfma_f32_16x16x32_bf16 v[28:31], v[170:173], v[194:197], v[28:31]
	v_mfma_f32_16x16x32_bf16 v[12:15], v[178:181], v[194:197], v[12:15]
	v_mfma_f32_16x16x32_bf16 v[36:39], v[170:173], v[202:205], v[36:39]
	v_mfma_f32_16x16x32_bf16 v[40:43], v[178:181], v[202:205], v[40:43]
	v_mfma_f32_16x16x32_bf16 v[20:23], v[170:173], v[210:213], v[20:23]
	v_mfma_f32_16x16x32_bf16 v[24:27], v[178:181], v[210:213], v[24:27]
	s_barrier
	v_add_u32_e32 v96, s73, v139
	ds_read_b128 v[150:153], v96
	ds_read_b128 v[154:157], v96 offset:1024
	ds_read_b128 v[158:161], v96 offset:2048
	ds_read_b128 v[162:165], v96 offset:3072
	v_add_u32_e32 v96, s72, v139
	ds_read_b128 v[166:169], v96
	ds_read_b128 v[170:173], v96 offset:1024
	ds_read_b128 v[174:177], v96 offset:2048
	ds_read_b128 v[178:181], v96 offset:3072
	v_mov_b32_e32 v96, v133
	s_mov_b32 m0, s63
	ds_read_b128 v[182:185], v149 offset:32768
	ds_read_b128 v[186:189], v149 offset:33792
	ds_read_b128 v[190:193], v149 offset:34816
	ds_read_b128 v[194:197], v149 offset:35840
	ds_read_b128 v[198:201], v149 offset:36864
	ds_read_b128 v[202:205], v149 offset:37888
	ds_read_b128 v[206:209], v149 offset:38912
	ds_read_b128 v[210:213], v149 offset:39936
	s_nop 0
	global_load_lds_dwordx4 v96, s[4:5]
	v_mov_b32_e32 v96, v136
	s_mov_b32 m0, s64
	s_nop 0
	global_load_lds_dwordx4 v96, s[4:5]
	s_waitcnt vmcnt(8)
	s_waitcnt lgkmcnt(0)
	s_barrier
	s_waitcnt lgkmcnt(0)
	v_mfma_f32_16x16x32_bf16 v[126:129], v[150:153], v[182:185], v[126:129]
	v_mfma_f32_16x16x32_bf16 v[122:125], v[158:161], v[182:185], v[122:125]
	v_mfma_f32_16x16x32_bf16 v[110:113], v[150:153], v[190:193], v[110:113]
	v_mfma_f32_16x16x32_bf16 v[106:109], v[158:161], v[190:193], v[106:109]
	v_mfma_f32_16x16x32_bf16 v[92:95], v[150:153], v[198:201], v[92:95]
	v_mfma_f32_16x16x32_bf16 v[88:91], v[158:161], v[198:201], v[88:91]
	v_mfma_f32_16x16x32_bf16 v[76:79], v[150:153], v[206:209], v[76:79]
	v_mfma_f32_16x16x32_bf16 v[72:75], v[158:161], v[206:209], v[72:75]
	v_mfma_f32_16x16x32_bf16 v[126:129], v[154:157], v[186:189], v[126:129]
	v_mfma_f32_16x16x32_bf16 v[122:125], v[162:165], v[186:189], v[122:125]
	v_mfma_f32_16x16x32_bf16 v[110:113], v[154:157], v[194:197], v[110:113]
	v_mfma_f32_16x16x32_bf16 v[106:109], v[162:165], v[194:197], v[106:109]
	v_mfma_f32_16x16x32_bf16 v[92:95], v[154:157], v[202:205], v[92:95]
	v_mfma_f32_16x16x32_bf16 v[88:91], v[162:165], v[202:205], v[88:91]
	v_mfma_f32_16x16x32_bf16 v[76:79], v[154:157], v[210:213], v[76:79]
	v_mfma_f32_16x16x32_bf16 v[72:75], v[162:165], v[210:213], v[72:75]
	v_mfma_f32_16x16x32_bf16 v[118:121], v[166:169], v[182:185], v[118:121]
	v_mfma_f32_16x16x32_bf16 v[114:117], v[174:177], v[182:185], v[114:117]
	v_mfma_f32_16x16x32_bf16 v[102:105], v[166:169], v[190:193], v[102:105]
	v_mfma_f32_16x16x32_bf16 v[98:101], v[174:177], v[190:193], v[98:101]
	v_mfma_f32_16x16x32_bf16 v[84:87], v[166:169], v[198:201], v[84:87]
	v_mfma_f32_16x16x32_bf16 v[80:83], v[174:177], v[198:201], v[80:83]
	v_mfma_f32_16x16x32_bf16 v[68:71], v[166:169], v[206:209], v[68:71]
	v_mfma_f32_16x16x32_bf16 v[64:67], v[174:177], v[206:209], v[64:67]
	v_mfma_f32_16x16x32_bf16 v[118:121], v[170:173], v[186:189], v[118:121]
	v_mfma_f32_16x16x32_bf16 v[114:117], v[178:181], v[186:189], v[114:117]
	v_mfma_f32_16x16x32_bf16 v[102:105], v[170:173], v[194:197], v[102:105]
	v_mfma_f32_16x16x32_bf16 v[98:101], v[178:181], v[194:197], v[98:101]
	v_mfma_f32_16x16x32_bf16 v[84:87], v[170:173], v[202:205], v[84:87]
	v_mfma_f32_16x16x32_bf16 v[80:83], v[178:181], v[202:205], v[80:83]
	v_mfma_f32_16x16x32_bf16 v[68:71], v[170:173], v[210:213], v[68:71]
	v_mfma_f32_16x16x32_bf16 v[64:67], v[178:181], v[210:213], v[64:67]
	s_barrier
; #define PG8_STAGE(bufoff, gbase, voff) do { _Pragma("unroll") for (int _i = 0; _i < 2; ++_i) \
;         __builtin_amdgcn_global_load_lds((const __attribute__((address_space(1))) unsigned*)((const __attribute__((address_space(1))) char*)(gbase) + (unsigned)lnd_v((int)(voff)[_i])), (LAS unsigned*)(lds + (bufoff) + ldsw + _i * 8192), 16, 0, 0); } while (0)
; #define PG8_LDA(dst, b, h) do { _Pragma("unroll") for (int m = 0; m < 4; ++m) _Pragma("unroll") for (int k = 0; k < 2; ++k) dst[m][k] = *(const LAS bf16x8*)(lds + PG8_SA(b, h) + aoff + m * 2048 + k * 1024); } while (0)
; #define PG8_MMA(ai, bj, At, Bt) do { __builtin_amdgcn_s_setprio(1); _Pragma("unroll") for (int m = 0; m < 4; ++m) _Pragma("unroll") for (int n = 0; n < 2; ++n) _Pragma("unroll") for (int k = 0; k < 2; ++k) \
;         acc[ai][bj][m][n] = __builtin_amdgcn_mfma_f32_16x16x32_bf16(Bt[n][k], At[m][k], acc[ai][bj][m][n], 0, 0, 0); __builtin_amdgcn_s_setprio(0); } while (0)
; #define PG8_WAIT_V(n) asm volatile("s_waitcnt vmcnt(" #n ")" ::: "memory")
; #define PG8_WAIT_L(n) asm volatile("s_waitcnt lgkmcnt(" #n ")" ::: "memory")
; #define PG8_BAR __builtin_amdgcn_s_barrier()
; #define PG8_SCHED __builtin_amdgcn_sched_barrier(0)
; template <class Desc, class Epi>
; __device__ __forceinline__ void gemm_phase(const int wv_, LAS unsigned char* lds, const Desc& d, const Epi& E) {
;     ...
;             PG8_LDA(At, 1, 1); PG8_STAGE(PG8_SB(1, 0), b3, voffB); PG8_STAGE(PG8_SB(1, 1), b3 + hstepB, voffB); PG8_STAGE(PG8_SA(1, 0), a3, sA0);
;             PG8_WAIT_V(8); PG8_WAIT_L(0); PG8_BAR; PG8_MMA(1, 0, At, B0); PG8_MMA(1, 1, At, B1); PG8_BAR; PG8_SCHED;
;         }
;         if (wr == 0) PG8_BAR;
	v_mov_b32_e32 v96, v134
	ds_read_b128 v[182:185], v149 offset:49152
	ds_read_b128 v[186:189], v149 offset:50176
	ds_read_b128 v[190:193], v149 offset:51200
	ds_read_b128 v[194:197], v149 offset:52224
	ds_read_b128 v[198:201], v149 offset:53248
	ds_read_b128 v[202:205], v149 offset:54272
	ds_read_b128 v[206:209], v149 offset:55296
	ds_read_b128 v[210:213], v149 offset:56320
	s_mov_b32 m0, s71
	v_lshl_add_u64 v[130:131], s[20:21], 0, v[96:97]
	v_lshl_add_u64 v[130:131], v[130:131], 0, s[30:31]
	v_mov_b32_e32 v96, v137
	global_load_lds_dwordx4 v[130:131], off
	s_mov_b32 m0, s29
	v_lshl_add_u64 v[130:131], s[20:21], 0, v[96:97]
	v_lshl_add_u64 v[130:131], v[130:131], 0, s[30:31]
	v_mov_b32_e32 v96, v134
	global_load_lds_dwordx4 v[130:131], off
	s_mov_b32 m0, s78
	s_nop 0
	global_load_lds_dwordx4 v96, s[22:23]
	v_mov_b32_e32 v96, v137
	s_mov_b32 m0, s77
	s_nop 0
	global_load_lds_dwordx4 v96, s[22:23]
	v_mov_b32_e32 v96, v132
	s_mov_b32 m0, s65
	v_lshl_add_u64 v[130:131], s[4:5], 0, v[96:97]
	v_lshl_add_u64 v[130:131], v[130:131], 0, s[30:31]
	v_mov_b32_e32 v96, v135
	global_load_lds_dwordx4 v[130:131], off
	s_mov_b32 m0, s66
	v_lshl_add_u64 v[130:131], s[4:5], 0, v[96:97]
	v_lshl_add_u64 v[130:131], v[130:131], 0, s[30:31]
	global_load_lds_dwordx4 v[130:131], off
	s_waitcnt vmcnt(8)
	s_waitcnt lgkmcnt(0)
	s_barrier
	s_waitcnt lgkmcnt(0)
	v_mfma_f32_16x16x32_bf16 v[60:63], v[150:153], v[182:185], v[60:63]
	v_mfma_f32_16x16x32_bf16 v[56:59], v[158:161], v[182:185], v[56:59]
	v_mfma_f32_16x16x32_bf16 v[44:47], v[150:153], v[190:193], v[44:47]
	v_mfma_f32_16x16x32_bf16 v[32:35], v[158:161], v[190:193], v[32:35]
	v_mfma_f32_16x16x32_bf16 v[16:19], v[150:153], v[198:201], v[16:19]
	v_mfma_f32_16x16x32_bf16 v[8:11], v[158:161], v[198:201], v[8:11]
	v_mfma_f32_16x16x32_bf16 v[4:7], v[150:153], v[206:209], v[4:7]
	v_mfma_f32_16x16x32_bf16 v[0:3], v[158:161], v[206:209], v[0:3]
	v_mfma_f32_16x16x32_bf16 v[60:63], v[154:157], v[186:189], v[60:63]
	v_mfma_f32_16x16x32_bf16 v[56:59], v[162:165], v[186:189], v[56:59]
	v_mfma_f32_16x16x32_bf16 v[44:47], v[154:157], v[194:197], v[44:47]
	v_mfma_f32_16x16x32_bf16 v[32:35], v[162:165], v[194:197], v[32:35]
	v_mfma_f32_16x16x32_bf16 v[16:19], v[154:157], v[202:205], v[16:19]
	v_mfma_f32_16x16x32_bf16 v[8:11], v[162:165], v[202:205], v[8:11]
	v_mfma_f32_16x16x32_bf16 v[4:7], v[154:157], v[210:213], v[4:7]
	v_mfma_f32_16x16x32_bf16 v[0:3], v[162:165], v[210:213], v[0:3]
	v_mfma_f32_16x16x32_bf16 v[52:55], v[166:169], v[182:185], v[52:55]
	v_mfma_f32_16x16x32_bf16 v[48:51], v[174:177], v[182:185], v[48:51]
	v_mfma_f32_16x16x32_bf16 v[28:31], v[166:169], v[190:193], v[28:31]
	v_mfma_f32_16x16x32_bf16 v[12:15], v[174:177], v[190:193], v[12:15]
	v_mfma_f32_16x16x32_bf16 v[36:39], v[166:169], v[198:201], v[36:39]
	v_mfma_f32_16x16x32_bf16 v[40:43], v[174:177], v[198:201], v[40:43]
	v_mfma_f32_16x16x32_bf16 v[20:23], v[166:169], v[206:209], v[20:23]
	v_mfma_f32_16x16x32_bf16 v[24:27], v[174:177], v[206:209], v[24:27]
	v_mfma_f32_16x16x32_bf16 v[52:55], v[170:173], v[186:189], v[52:55]
	v_mfma_f32_16x16x32_bf16 v[48:51], v[178:181], v[186:189], v[48:51]
	v_mfma_f32_16x16x32_bf16 v[28:31], v[170:173], v[194:197], v[28:31]
	v_mfma_f32_16x16x32_bf16 v[12:15], v[178:181], v[194:197], v[12:15]
	v_mfma_f32_16x16x32_bf16 v[36:39], v[170:173], v[202:205], v[36:39]
	v_mfma_f32_16x16x32_bf16 v[40:43], v[178:181], v[202:205], v[40:43]
	v_mfma_f32_16x16x32_bf16 v[20:23], v[170:173], v[210:213], v[20:23]
	v_mfma_f32_16x16x32_bf16 v[24:27], v[178:181], v[210:213], v[24:27]
	s_barrier
	s_movk_i32 s22, 0x100
	s_andn2_b64 vcc, exec, s[2:3]
	s_mov_b64 s[20:21], -1
	s_mov_b64 s[2:3], 0
	s_cbranch_vccz .LBB0_937
	s_and_b64 vcc, exec, s[40:41]
	s_cbranch_vccz .LBB0_940
	s_barrier

; #define PG8_STAGE(bufoff, gbase, voff) do { _Pragma("unroll") for (int _i = 0; _i < 2; ++_i) \
;         __builtin_amdgcn_global_load_lds((const __attribute__((address_space(1))) unsigned*)((const __attribute__((address_space(1))) char*)(gbase) + (unsigned)lnd_v((int)(voff)[_i])), (LAS unsigned*)(lds + (bufoff) + ldsw + _i * 8192), 16, 0, 0); } while (0)
; #define PG8_LDA(dst, b, h) do { _Pragma("unroll") for (int m = 0; m < 4; ++m) _Pragma("unroll") for (int k = 0; k < 2; ++k) dst[m][k] = *(const LAS bf16x8*)(lds + PG8_SA(b, h) + aoff + m * 2048 + k * 1024); } while (0)
; #define PG8_LDB(dst, b, h) do { _Pragma("unroll") for (int n = 0; n < 2; ++n) _Pragma("unroll") for (int k = 0; k < 2; ++k) dst[n][k] = *(const LAS bf16x8*)(lds + PG8_SB(b, h) + boff + n * 2048 + k * 1024); } while (0)
; #define PG8_WAIT_V(n) asm volatile("s_waitcnt vmcnt(" #n ")" ::: "memory")
; #define PG8_WAIT_L(n) asm volatile("s_waitcnt lgkmcnt(" #n ")" ::: "memory")
; #define PG8_BAR __builtin_amdgcn_s_barrier()
; template <class Desc, class Epi>
; __device__ __forceinline__ void gemm_phase(const int wv_, LAS unsigned char* lds, const Desc& d, const Epi& E) {
;     ...
;         for (int t = 0; t < nt; t += 2) {
;             const bool last = (t == nt - 2);
;             unsigned sA0[2], sA1[2];
;             if constexpr (Desc::GATHER) { sA0[0] = last ? voffAn[0] : voffA[0]; sA0[1] = last ? voffAn[1] : voffA[1]; sA1[0] = last ? voffAn1[0] : voffA1[0]; sA1[1] = last ? voffAn1[1] : voffA1[1]; }
;             else { sA0[0] = voffA[0]; sA0[1] = voffA[1]; sA1[0] = voffA1[0]; sA1[1] = voffA1[1]; }
;             const char* a1 = cA + (size_t)(t + 1) * kstep;
;             const char* a2 = last ? nA : cA + (size_t)(t + 2) * kstep; const char* b2 = last ? nB : cB + (size_t)(t + 2) * kstep;
;             const char* a3 = a2 + kstep; const char* b3 = b2 + kstep;
;             PG8_LDB(B0, 0, 0); PG8_LDB(B1, 0, 1); PG8_SCHED; PG8_LDA(At, 0, 0); PG8_STAGE(PG8_SA(1, 1), a1, voffA1);
;             PG8_WAIT_V(8); PG8_WAIT_L(0); PG8_BAR; PG8_MMA(0, 0, At, B0); PG8_MMA(0, 1, At, B1); PG8_BAR; PG8_SCHED;
;             PG8_LDA(At, 0, 1); PG8_STAGE(PG8_SB(0, 0), b2, voffB); PG8_STAGE(PG8_SB(0, 1), b2 + hstepB, voffB); PG8_STAGE(PG8_SA(0, 0), a2, sA0);
;             PG8_WAIT_V(8); PG8_WAIT_L(0); PG8_BAR; PG8_MMA(1, 0, At, B0); PG8_MMA(1, 1, At, B1); PG8_BAR; PG8_SCHED;
.LBB0_1075:
	s_add_u32 s4, s2, 0x80
	s_addc_u32 s5, s3, 0
	s_add_i32 s47, 0, 0x10000
	s_cmp_eq_u32 s29, 12
	s_cselect_b32 s5, s51, s5
	s_cselect_b32 s4, s50, s4
	v_add_u32_e32 v96, s47, v226
	s_cselect_b32 s21, s53, s26
	s_cselect_b32 s20, s52, s1
	s_add_i32 s49, 0, 0x14000
	ds_read_b128 v[118:121], v96
	ds_read_b128 v[126:129], v96 offset:1024
	ds_read_b128 v[130:133], v96 offset:2048
	ds_read_b128 v[134:137], v96 offset:3072
	v_add_u32_e32 v96, s49, v226
	ds_read_b128 v[142:145], v96
	ds_read_b128 v[150:153], v96 offset:1024
	ds_read_b128 v[154:157], v96 offset:2048
	ds_read_b128 v[158:161], v96 offset:3072
	v_mov_b32_e32 v96, v220
	ds_read_b128 v[162:165], v231
	ds_read_b128 v[166:169], v231 offset:1024
	ds_read_b128 v[170:173], v231 offset:2048
	ds_read_b128 v[174:177], v231 offset:3072
	ds_read_b128 v[178:181], v231 offset:4096
	ds_read_b128 v[182:185], v231 offset:5120
	ds_read_b128 v[186:189], v231 offset:6144
	ds_read_b128 v[190:193], v231 offset:7168
	s_add_i32 m0, s60, 0xc000
	s_nop 0
	global_load_lds_dwordx4 v96, s[2:3]
	v_mov_b32_e32 v96, v223
	s_add_i32 m0, s60, 0xe000
	s_nop 0
	global_load_lds_dwordx4 v96, s[2:3]
	s_waitcnt vmcnt(8)
	s_waitcnt lgkmcnt(0)
	s_barrier
	s_waitcnt lgkmcnt(0)
	v_mfma_f32_16x16x32_bf16 v[146:149], v[118:121], v[162:165], v[146:149]
	v_mfma_f32_16x16x32_bf16 v[138:141], v[130:133], v[162:165], v[138:141]
	v_mfma_f32_16x16x32_bf16 v[110:113], v[118:121], v[170:173], v[110:113]
	v_mfma_f32_16x16x32_bf16 v[106:109], v[130:133], v[170:173], v[106:109]
	v_mfma_f32_16x16x32_bf16 v[92:95], v[118:121], v[178:181], v[92:95]
	v_mfma_f32_16x16x32_bf16 v[88:91], v[130:133], v[178:181], v[88:91]
	v_mfma_f32_16x16x32_bf16 v[76:79], v[118:121], v[186:189], v[76:79]
	v_mfma_f32_16x16x32_bf16 v[72:75], v[130:133], v[186:189], v[72:75]
	v_mfma_f32_16x16x32_bf16 v[146:149], v[126:129], v[166:169], v[146:149]
	v_mfma_f32_16x16x32_bf16 v[138:141], v[134:137], v[166:169], v[138:141]
	v_mfma_f32_16x16x32_bf16 v[110:113], v[126:129], v[174:177], v[110:113]
	v_mfma_f32_16x16x32_bf16 v[106:109], v[134:137], v[174:177], v[106:109]
	v_mfma_f32_16x16x32_bf16 v[92:95], v[126:129], v[182:185], v[92:95]
	v_mfma_f32_16x16x32_bf16 v[88:91], v[134:137], v[182:185], v[88:91]
	v_mfma_f32_16x16x32_bf16 v[76:79], v[126:129], v[190:193], v[76:79]
	v_mfma_f32_16x16x32_bf16 v[72:75], v[134:137], v[190:193], v[72:75]
	v_mfma_f32_16x16x32_bf16 v[122:125], v[142:145], v[162:165], v[122:125]
	v_mfma_f32_16x16x32_bf16 v[114:117], v[154:157], v[162:165], v[114:117]
	v_mfma_f32_16x16x32_bf16 v[102:105], v[142:145], v[170:173], v[102:105]
	v_mfma_f32_16x16x32_bf16 v[98:101], v[154:157], v[170:173], v[98:101]
	v_mfma_f32_16x16x32_bf16 v[84:87], v[142:145], v[178:181], v[84:87]
	v_mfma_f32_16x16x32_bf16 v[80:83], v[154:157], v[178:181], v[80:83]
	v_mfma_f32_16x16x32_bf16 v[68:71], v[142:145], v[186:189], v[68:71]
	v_mfma_f32_16x16x32_bf16 v[64:67], v[154:157], v[186:189], v[64:67]
	v_mfma_f32_16x16x32_bf16 v[122:125], v[150:153], v[166:169], v[122:125]
	v_mfma_f32_16x16x32_bf16 v[114:117], v[158:161], v[166:169], v[114:117]
	v_mfma_f32_16x16x32_bf16 v[102:105], v[150:153], v[174:177], v[102:105]
	v_mfma_f32_16x16x32_bf16 v[98:101], v[158:161], v[174:177], v[98:101]
	v_mfma_f32_16x16x32_bf16 v[84:87], v[150:153], v[182:185], v[84:87]
	v_mfma_f32_16x16x32_bf16 v[80:83], v[158:161], v[182:185], v[80:83]
	v_mfma_f32_16x16x32_bf16 v[68:71], v[150:153], v[190:193], v[68:71]
	v_mfma_f32_16x16x32_bf16 v[64:67], v[158:161], v[190:193], v[64:67]
	s_barrier
	v_mov_b32_e32 v96, v221
	s_add_i32 s47, s47, s59
	ds_read_b128 v[162:165], v231 offset:16384
	ds_read_b128 v[166:169], v231 offset:17408
	ds_read_b128 v[170:173], v231 offset:18432
	ds_read_b128 v[174:177], v231 offset:19456
	ds_read_b128 v[178:181], v231 offset:20480
	ds_read_b128 v[182:185], v231 offset:21504
	ds_read_b128 v[186:189], v231 offset:22528
	ds_read_b128 v[190:193], v231 offset:23552
	s_mov_b32 m0, s47
	s_nop 0
	global_load_lds_dwordx4 v96, s[20:21]
	v_mov_b32_e32 v96, v224
	s_add_i32 m0, s47, 0x2000
	s_add_u32 s70, s20, 0x40000
	global_load_lds_dwordx4 v96, s[20:21]
	s_addc_u32 s71, s21, 0
	v_mov_b32_e32 v96, v221
	s_add_i32 s47, s49, s59
	s_mov_b32 m0, s47
	s_nop 0
	global_load_lds_dwordx4 v96, s[70:71]
	v_mov_b32_e32 v96, v224
	s_add_i32 m0, s47, 0x2000
	s_nop 0
	global_load_lds_dwordx4 v96, s[70:71]
	v_mov_b32_e32 v96, v219
	s_mov_b32 m0, s60
	s_nop 0
	global_load_lds_dwordx4 v96, s[4:5]
	v_mov_b32_e32 v96, v222
	s_mov_b32 m0, s62
	s_nop 0
	global_load_lds_dwordx4 v96, s[4:5]
	s_waitcnt vmcnt(8)
	s_waitcnt lgkmcnt(0)
	s_barrier
; #define PG8_STAGE(bufoff, gbase, voff) do { _Pragma("unroll") for (int _i = 0; _i < 2; ++_i) \
;         __builtin_amdgcn_global_load_lds((const __attribute__((address_space(1))) unsigned*)((const __attribute__((address_space(1))) char*)(gbase) + (unsigned)lnd_v((int)(voff)[_i])), (LAS unsigned*)(lds + (bufoff) + ldsw + _i * 8192), 16, 0, 0); } while (0)
; #define PG8_LDA(dst, b, h) do { _Pragma("unroll") for (int m = 0; m < 4; ++m) _Pragma("unroll") for (int k = 0; k < 2; ++k) dst[m][k] = *(const LAS bf16x8*)(lds + PG8_SA(b, h) + aoff + m * 2048 + k * 1024); } while (0)
; #define PG8_LDB(dst, b, h) do { _Pragma("unroll") for (int n = 0; n < 2; ++n) _Pragma("unroll") for (int k = 0; k < 2; ++k) dst[n][k] = *(const LAS bf16x8*)(lds + PG8_SB(b, h) + boff + n * 2048 + k * 1024); } while (0)
; #define PG8_MMA(ai, bj, At, Bt) do { __builtin_amdgcn_s_setprio(1); _Pragma("unroll") for (int m = 0; m < 4; ++m) _Pragma("unroll") for (int n = 0; n < 2; ++n) _Pragma("unroll") for (int k = 0; k < 2; ++k) \
;         acc[ai][bj][m][n] = __builtin_amdgcn_mfma_f32_16x16x32_bf16(Bt[n][k], At[m][k], acc[ai][bj][m][n], 0, 0, 0); __builtin_amdgcn_s_setprio(0); } while (0)
; #define PG8_WAIT_V(n) asm volatile("s_waitcnt vmcnt(" #n ")" ::: "memory")
; #define PG8_WAIT_L(n) asm volatile("s_waitcnt lgkmcnt(" #n ")" ::: "memory")
; #define PG8_BAR __builtin_amdgcn_s_barrier()
; #define PG8_SCHED __builtin_amdgcn_sched_barrier(0)
; template <class Desc, class Epi>
; __device__ __forceinline__ void gemm_phase(const int wv_, LAS unsigned char* lds, const Desc& d, const Epi& E) {
;     ...
;             PG8_WAIT_V(8); PG8_WAIT_L(0); PG8_BAR; PG8_MMA(1, 0, At, B0); PG8_MMA(1, 1, At, B1); PG8_BAR; PG8_SCHED;
;             PG8_LDB(B0, 1, 0); PG8_LDB(B1, 1, 1); PG8_SCHED; PG8_LDA(At, 1, 0); PG8_STAGE(PG8_SA(0, 1), a2, sA1);
;             PG8_WAIT_V(8); PG8_WAIT_L(0); PG8_BAR; PG8_MMA(0, 0, At, B0); PG8_MMA(0, 1, At, B1); PG8_BAR; PG8_SCHED;
	s_waitcnt lgkmcnt(0)
	v_mfma_f32_16x16x32_bf16 v[60:63], v[118:121], v[162:165], v[60:63]
	v_mfma_f32_16x16x32_bf16 v[56:59], v[130:133], v[162:165], v[56:59]
	v_mfma_f32_16x16x32_bf16 v[44:47], v[118:121], v[170:173], v[44:47]
	v_mfma_f32_16x16x32_bf16 v[40:43], v[130:133], v[170:173], v[40:43]
	v_mfma_f32_16x16x32_bf16 v[20:23], v[118:121], v[178:181], v[20:23]
	v_mfma_f32_16x16x32_bf16 v[16:19], v[130:133], v[178:181], v[16:19]
	v_mfma_f32_16x16x32_bf16 v[4:7], v[118:121], v[186:189], v[4:7]
	v_mfma_f32_16x16x32_bf16 v[0:3], v[130:133], v[186:189], v[0:3]
	v_mfma_f32_16x16x32_bf16 v[60:63], v[126:129], v[166:169], v[60:63]
	v_mfma_f32_16x16x32_bf16 v[56:59], v[134:137], v[166:169], v[56:59]
	v_mfma_f32_16x16x32_bf16 v[44:47], v[126:129], v[174:177], v[44:47]
	v_mfma_f32_16x16x32_bf16 v[40:43], v[134:137], v[174:177], v[40:43]
	v_mfma_f32_16x16x32_bf16 v[20:23], v[126:129], v[182:185], v[20:23]
	v_mfma_f32_16x16x32_bf16 v[16:19], v[134:137], v[182:185], v[16:19]
	v_mfma_f32_16x16x32_bf16 v[4:7], v[126:129], v[190:193], v[4:7]
	v_mfma_f32_16x16x32_bf16 v[0:3], v[134:137], v[190:193], v[0:3]
	v_mfma_f32_16x16x32_bf16 v[52:55], v[142:145], v[162:165], v[52:55]
	v_mfma_f32_16x16x32_bf16 v[48:51], v[154:157], v[162:165], v[48:51]
	v_mfma_f32_16x16x32_bf16 v[36:39], v[142:145], v[170:173], v[36:39]
	v_mfma_f32_16x16x32_bf16 v[32:35], v[154:157], v[170:173], v[32:35]
	v_mfma_f32_16x16x32_bf16 v[28:31], v[142:145], v[178:181], v[28:31]
	v_mfma_f32_16x16x32_bf16 v[24:27], v[154:157], v[178:181], v[24:27]
	v_mfma_f32_16x16x32_bf16 v[12:15], v[142:145], v[186:189], v[12:15]
	v_mfma_f32_16x16x32_bf16 v[8:11], v[154:157], v[186:189], v[8:11]
	v_mfma_f32_16x16x32_bf16 v[52:55], v[150:153], v[166:169], v[52:55]
	v_mfma_f32_16x16x32_bf16 v[48:51], v[158:161], v[166:169], v[48:51]
	v_mfma_f32_16x16x32_bf16 v[36:39], v[150:153], v[174:177], v[36:39]
	v_mfma_f32_16x16x32_bf16 v[32:35], v[158:161], v[174:177], v[32:35]
	v_mfma_f32_16x16x32_bf16 v[28:31], v[150:153], v[182:185], v[28:31]
	v_mfma_f32_16x16x32_bf16 v[24:27], v[158:161], v[182:185], v[24:27]
	v_mfma_f32_16x16x32_bf16 v[12:15], v[150:153], v[190:193], v[12:15]
	v_mfma_f32_16x16x32_bf16 v[8:11], v[158:161], v[190:193], v[8:11]
	s_barrier
	s_add_i32 s47, 0, 0x18000
	v_add_u32_e32 v96, s47, v226
	s_add_i32 s49, 0, 0x1c000
	ds_read_b128 v[118:121], v96
	ds_read_b128 v[126:129], v96 offset:1024
	ds_read_b128 v[130:133], v96 offset:2048
	ds_read_b128 v[134:137], v96 offset:3072
	v_add_u32_e32 v96, s49, v226
	ds_read_b128 v[142:145], v96
	ds_read_b128 v[150:153], v96 offset:1024
	ds_read_b128 v[154:157], v96 offset:2048
	ds_read_b128 v[158:161], v96 offset:3072
	v_mov_b32_e32 v96, v220
	s_mov_b32 m0, s63
	ds_read_b128 v[162:165], v231 offset:32768
	ds_read_b128 v[166:169], v231 offset:33792
	ds_read_b128 v[170:173], v231 offset:34816
	ds_read_b128 v[174:177], v231 offset:35840
	ds_read_b128 v[178:181], v231 offset:36864
	ds_read_b128 v[182:185], v231 offset:37888
	ds_read_b128 v[186:189], v231 offset:38912
	ds_read_b128 v[190:193], v231 offset:39936
	s_nop 0
	global_load_lds_dwordx4 v96, s[4:5]
	v_mov_b32_e32 v96, v223
	s_mov_b32 m0, s64
	s_nop 0
	global_load_lds_dwordx4 v96, s[4:5]
	s_waitcnt vmcnt(8)
	s_waitcnt lgkmcnt(0)
	s_barrier
	s_waitcnt lgkmcnt(0)
	v_mfma_f32_16x16x32_bf16 v[146:149], v[118:121], v[162:165], v[146:149]
	v_mfma_f32_16x16x32_bf16 v[138:141], v[130:133], v[162:165], v[138:141]
	v_mfma_f32_16x16x32_bf16 v[110:113], v[118:121], v[170:173], v[110:113]
	v_mfma_f32_16x16x32_bf16 v[106:109], v[130:133], v[170:173], v[106:109]
	v_mfma_f32_16x16x32_bf16 v[92:95], v[118:121], v[178:181], v[92:95]
	v_mfma_f32_16x16x32_bf16 v[88:91], v[130:133], v[178:181], v[88:91]
	v_mfma_f32_16x16x32_bf16 v[76:79], v[118:121], v[186:189], v[76:79]
	v_mfma_f32_16x16x32_bf16 v[72:75], v[130:133], v[186:189], v[72:75]
	v_mfma_f32_16x16x32_bf16 v[146:149], v[126:129], v[166:169], v[146:149]
	v_mfma_f32_16x16x32_bf16 v[138:141], v[134:137], v[166:169], v[138:141]
	v_mfma_f32_16x16x32_bf16 v[110:113], v[126:129], v[174:177], v[110:113]
	v_mfma_f32_16x16x32_bf16 v[106:109], v[134:137], v[174:177], v[106:109]
	v_mfma_f32_16x16x32_bf16 v[92:95], v[126:129], v[182:185], v[92:95]
	v_mfma_f32_16x16x32_bf16 v[88:91], v[134:137], v[182:185], v[88:91]
	v_mfma_f32_16x16x32_bf16 v[76:79], v[126:129], v[190:193], v[76:79]
	v_mfma_f32_16x16x32_bf16 v[72:75], v[134:137], v[190:193], v[72:75]
	v_mfma_f32_16x16x32_bf16 v[122:125], v[142:145], v[162:165], v[122:125]
	v_mfma_f32_16x16x32_bf16 v[114:117], v[154:157], v[162:165], v[114:117]
	v_mfma_f32_16x16x32_bf16 v[102:105], v[142:145], v[170:173], v[102:105]
	v_mfma_f32_16x16x32_bf16 v[98:101], v[154:157], v[170:173], v[98:101]
	v_mfma_f32_16x16x32_bf16 v[84:87], v[142:145], v[178:181], v[84:87]
	v_mfma_f32_16x16x32_bf16 v[80:83], v[154:157], v[178:181], v[80:83]
	v_mfma_f32_16x16x32_bf16 v[68:71], v[142:145], v[186:189], v[68:71]
	v_mfma_f32_16x16x32_bf16 v[64:67], v[154:157], v[186:189], v[64:67]
	v_mfma_f32_16x16x32_bf16 v[122:125], v[150:153], v[166:169], v[122:125]
	v_mfma_f32_16x16x32_bf16 v[114:117], v[158:161], v[166:169], v[114:117]
	v_mfma_f32_16x16x32_bf16 v[102:105], v[150:153], v[174:177], v[102:105]
	v_mfma_f32_16x16x32_bf16 v[98:101], v[158:161], v[174:177], v[98:101]
	v_mfma_f32_16x16x32_bf16 v[84:87], v[150:153], v[182:185], v[84:87]
	v_mfma_f32_16x16x32_bf16 v[80:83], v[158:161], v[182:185], v[80:83]
	v_mfma_f32_16x16x32_bf16 v[68:71], v[150:153], v[190:193], v[68:71]
	v_mfma_f32_16x16x32_bf16 v[64:67], v[158:161], v[190:193], v[64:67]
	s_barrier
; #define PG8_STAGE(bufoff, gbase, voff) do { _Pragma("unroll") for (int _i = 0; _i < 2; ++_i) \
;         __builtin_amdgcn_global_load_lds((const __attribute__((address_space(1))) unsigned*)((const __attribute__((address_space(1))) char*)(gbase) + (unsigned)lnd_v((int)(voff)[_i])), (LAS unsigned*)(lds + (bufoff) + ldsw + _i * 8192), 16, 0, 0); } while (0)
; #define PG8_LDA(dst, b, h) do { _Pragma("unroll") for (int m = 0; m < 4; ++m) _Pragma("unroll") for (int k = 0; k < 2; ++k) dst[m][k] = *(const LAS bf16x8*)(lds + PG8_SA(b, h) + aoff + m * 2048 + k * 1024); } while (0)
; #define PG8_MMA(ai, bj, At, Bt) do { __builtin_amdgcn_s_setprio(1); _Pragma("unroll") for (int m = 0; m < 4; ++m) _Pragma("unroll") for (int n = 0; n < 2; ++n) _Pragma("unroll") for (int k = 0; k < 2; ++k) \
;         acc[ai][bj][m][n] = __builtin_amdgcn_mfma_f32_16x16x32_bf16(Bt[n][k], At[m][k], acc[ai][bj][m][n], 0, 0, 0); __builtin_amdgcn_s_setprio(0); } while (0)
; #define PG8_WAIT_V(n) asm volatile("s_waitcnt vmcnt(" #n ")" ::: "memory")
; #define PG8_WAIT_L(n) asm volatile("s_waitcnt lgkmcnt(" #n ")" ::: "memory")
; #define PG8_BAR __builtin_amdgcn_s_barrier()
; #define PG8_SCHED __builtin_amdgcn_sched_barrier(0)
; template <class Desc, class Epi>
; __device__ __forceinline__ void gemm_phase(const int wv_, LAS unsigned char* lds, const Desc& d, const Epi& E) {
;     ...
;             PG8_LDA(At, 1, 1); PG8_STAGE(PG8_SB(1, 0), b3, voffB); PG8_STAGE(PG8_SB(1, 1), b3 + hstepB, voffB); PG8_STAGE(PG8_SA(1, 0), a3, sA0);
;             PG8_WAIT_V(8); PG8_WAIT_L(0); PG8_BAR; PG8_MMA(1, 0, At, B0); PG8_MMA(1, 1, At, B1); PG8_BAR; PG8_SCHED;
;         }
;         if (wr == 0) PG8_BAR;
	v_mov_b32_e32 v96, v221
	ds_read_b128 v[162:165], v231 offset:49152
	ds_read_b128 v[166:169], v231 offset:50176
	ds_read_b128 v[170:173], v231 offset:51200
	ds_read_b128 v[174:177], v231 offset:52224
	ds_read_b128 v[178:181], v231 offset:53248
	ds_read_b128 v[182:185], v231 offset:54272
	ds_read_b128 v[186:189], v231 offset:55296
	ds_read_b128 v[190:193], v231 offset:56320
	s_add_i32 s47, s47, s59
	v_lshl_add_u64 v[194:195], s[20:21], 0, v[96:97]
	v_lshl_add_u64 v[194:195], v[194:195], 0, s[30:31]
	s_mov_b32 m0, s47
	v_mov_b32_e32 v96, v224
	global_load_lds_dwordx4 v[194:195], off
	s_add_i32 m0, s47, 0x2000
	s_nop 0
	v_lshl_add_u64 v[194:195], s[20:21], 0, v[96:97]
	s_add_u32 s20, s20, 0x40080
	v_lshl_add_u64 v[194:195], v[194:195], 0, s[30:31]
	s_addc_u32 s21, s21, 0
	v_mov_b32_e32 v96, v221
	s_add_i32 s47, s49, s59
	global_load_lds_dwordx4 v[194:195], off
	s_mov_b32 m0, s47
	s_nop 0
	global_load_lds_dwordx4 v96, s[20:21]
	v_mov_b32_e32 v96, v224
	s_add_i32 m0, s47, 0x2000
	s_nop 0
	global_load_lds_dwordx4 v96, s[20:21]
	v_mov_b32_e32 v96, v219
	s_mov_b32 m0, s66
	v_lshl_add_u64 v[194:195], s[4:5], 0, v[96:97]
	v_lshl_add_u64 v[194:195], v[194:195], 0, s[30:31]
	v_mov_b32_e32 v96, v222
	global_load_lds_dwordx4 v[194:195], off
	s_mov_b32 m0, s67
	v_lshl_add_u64 v[194:195], s[4:5], 0, v[96:97]
	v_lshl_add_u64 v[194:195], v[194:195], 0, s[30:31]
	global_load_lds_dwordx4 v[194:195], off
	s_waitcnt vmcnt(8)
	s_waitcnt lgkmcnt(0)
	s_barrier
	s_waitcnt lgkmcnt(0)
	v_mfma_f32_16x16x32_bf16 v[60:63], v[118:121], v[162:165], v[60:63]
	v_mfma_f32_16x16x32_bf16 v[56:59], v[130:133], v[162:165], v[56:59]
	v_mfma_f32_16x16x32_bf16 v[44:47], v[118:121], v[170:173], v[44:47]
	v_mfma_f32_16x16x32_bf16 v[40:43], v[130:133], v[170:173], v[40:43]
	v_mfma_f32_16x16x32_bf16 v[20:23], v[118:121], v[178:181], v[20:23]
	v_mfma_f32_16x16x32_bf16 v[16:19], v[130:133], v[178:181], v[16:19]
	v_mfma_f32_16x16x32_bf16 v[4:7], v[118:121], v[186:189], v[4:7]
	v_mfma_f32_16x16x32_bf16 v[0:3], v[130:133], v[186:189], v[0:3]
	v_mfma_f32_16x16x32_bf16 v[60:63], v[126:129], v[166:169], v[60:63]
	v_mfma_f32_16x16x32_bf16 v[56:59], v[134:137], v[166:169], v[56:59]
	v_mfma_f32_16x16x32_bf16 v[44:47], v[126:129], v[174:177], v[44:47]
	v_mfma_f32_16x16x32_bf16 v[40:43], v[134:137], v[174:177], v[40:43]
	v_mfma_f32_16x16x32_bf16 v[20:23], v[126:129], v[182:185], v[20:23]
	v_mfma_f32_16x16x32_bf16 v[16:19], v[134:137], v[182:185], v[16:19]
	v_mfma_f32_16x16x32_bf16 v[4:7], v[126:129], v[190:193], v[4:7]
	v_mfma_f32_16x16x32_bf16 v[0:3], v[134:137], v[190:193], v[0:3]
	v_mfma_f32_16x16x32_bf16 v[52:55], v[142:145], v[162:165], v[52:55]
	v_mfma_f32_16x16x32_bf16 v[48:51], v[154:157], v[162:165], v[48:51]
	v_mfma_f32_16x16x32_bf16 v[36:39], v[142:145], v[170:173], v[36:39]
	v_mfma_f32_16x16x32_bf16 v[32:35], v[154:157], v[170:173], v[32:35]
	v_mfma_f32_16x16x32_bf16 v[28:31], v[142:145], v[178:181], v[28:31]
	v_mfma_f32_16x16x32_bf16 v[24:27], v[154:157], v[178:181], v[24:27]
	v_mfma_f32_16x16x32_bf16 v[12:15], v[142:145], v[186:189], v[12:15]
	v_mfma_f32_16x16x32_bf16 v[8:11], v[154:157], v[186:189], v[8:11]
	v_mfma_f32_16x16x32_bf16 v[52:55], v[150:153], v[166:169], v[52:55]
	v_mfma_f32_16x16x32_bf16 v[48:51], v[158:161], v[166:169], v[48:51]
	v_mfma_f32_16x16x32_bf16 v[36:39], v[150:153], v[174:177], v[36:39]
	v_mfma_f32_16x16x32_bf16 v[32:35], v[158:161], v[174:177], v[32:35]
	v_mfma_f32_16x16x32_bf16 v[28:31], v[150:153], v[182:185], v[28:31]
	v_mfma_f32_16x16x32_bf16 v[24:27], v[158:161], v[182:185], v[24:27]
	v_mfma_f32_16x16x32_bf16 v[12:15], v[150:153], v[190:193], v[12:15]
	v_mfma_f32_16x16x32_bf16 v[8:11], v[158:161], v[190:193], v[8:11]
	s_barrier
	s_add_i32 s29, s29, 2
	s_add_u32 s2, s2, 0x100
	s_addc_u32 s3, s3, 0
	s_add_u32 s1, s1, 0x100
	s_addc_u32 s26, s26, 0
	s_cmp_gt_u32 s29, 13
	s_cbranch_scc0 .LBB0_1075
	s_and_b64 vcc, exec, s[44:45]
	s_cbranch_vccz .LBB0_1078
	s_barrier

; #define PG8_STAGE(bufoff, gbase, voff) do { _Pragma("unroll") for (int _i = 0; _i < 2; ++_i) \
;         __builtin_amdgcn_global_load_lds((const __attribute__((address_space(1))) unsigned*)((const __attribute__((address_space(1))) char*)(gbase) + (unsigned)lnd_v((int)(voff)[_i])), (LAS unsigned*)(lds + (bufoff) + ldsw + _i * 8192), 16, 0, 0); } while (0)
; #define PG8_LDA(dst, b, h) do { _Pragma("unroll") for (int m = 0; m < 4; ++m) _Pragma("unroll") for (int k = 0; k < 2; ++k) dst[m][k] = *(const LAS bf16x8*)(lds + PG8_SA(b, h) + aoff + m * 2048 + k * 1024); } while (0)
; #define PG8_LDB(dst, b, h) do { _Pragma("unroll") for (int n = 0; n < 2; ++n) _Pragma("unroll") for (int k = 0; k < 2; ++k) dst[n][k] = *(const LAS bf16x8*)(lds + PG8_SB(b, h) + boff + n * 2048 + k * 1024); } while (0)
; #define PG8_WAIT_V(n) asm volatile("s_waitcnt vmcnt(" #n ")" ::: "memory")
; #define PG8_WAIT_L(n) asm volatile("s_waitcnt lgkmcnt(" #n ")" ::: "memory")
; #define PG8_BAR __builtin_amdgcn_s_barrier()
; template <class Desc, class Epi>
; __device__ __forceinline__ void gemm_phase(const int wv_, LAS unsigned char* lds, const Desc& d, const Epi& E) {
;     ...
;         for (int t = 0; t < nt; t += 2) {
;             const bool last = (t == nt - 2);
;             unsigned sA0[2], sA1[2];
;             if constexpr (Desc::GATHER) { sA0[0] = last ? voffAn[0] : voffA[0]; sA0[1] = last ? voffAn[1] : voffA[1]; sA1[0] = last ? voffAn1[0] : voffA1[0]; sA1[1] = last ? voffAn1[1] : voffA1[1]; }
;             else { sA0[0] = voffA[0]; sA0[1] = voffA[1]; sA1[0] = voffA1[0]; sA1[1] = voffA1[1]; }
;             const char* a1 = cA + (size_t)(t + 1) * kstep;
;             const char* a2 = last ? nA : cA + (size_t)(t + 2) * kstep; const char* b2 = last ? nB : cB + (size_t)(t + 2) * kstep;
;             const char* a3 = a2 + kstep; const char* b3 = b2 + kstep;
;             PG8_LDB(B0, 0, 0); PG8_LDB(B1, 0, 1); PG8_SCHED; PG8_LDA(At, 0, 0); PG8_STAGE(PG8_SA(1, 1), a1, voffA1);
;             PG8_WAIT_V(8); PG8_WAIT_L(0); PG8_BAR; PG8_MMA(0, 0, At, B0); PG8_MMA(0, 1, At, B1); PG8_BAR; PG8_SCHED;
;             PG8_LDA(At, 0, 1); PG8_STAGE(PG8_SB(0, 0), b2, voffB); PG8_STAGE(PG8_SB(0, 1), b2 + hstepB, voffB); PG8_STAGE(PG8_SA(0, 0), a2, sA0);
;             PG8_WAIT_V(8); PG8_WAIT_L(0); PG8_BAR; PG8_MMA(1, 0, At, B0); PG8_MMA(1, 1, At, B1); PG8_BAR; PG8_SCHED;
.LBB0_1161:
	s_add_u32 s4, s2, 0x80
	s_addc_u32 s5, s3, 0
	s_add_i32 s65, 0, 0x10000
	s_cmp_eq_u32 s45, 12
	s_cselect_b32 s5, s47, s5
	s_cselect_b32 s4, s46, s4
	v_add_u32_e32 v96, s65, v197
	s_cselect_b32 s21, s49, s29
	s_cselect_b32 s20, s48, s1
	s_add_i32 s68, 0, 0x14000
	ds_read_b128 v[130:133], v96
	ds_read_b128 v[134:137], v96 offset:1024
	ds_read_b128 v[138:141], v96 offset:2048
	ds_read_b128 v[142:145], v96 offset:3072
	v_add_u32_e32 v96, s68, v197
	ds_read_b128 v[146:149], v96
	ds_read_b128 v[150:153], v96 offset:1024
	ds_read_b128 v[154:157], v96 offset:2048
	ds_read_b128 v[158:161], v96 offset:3072
	v_mov_b32_e32 v96, v191
	ds_read_b128 v[162:165], v228
	ds_read_b128 v[166:169], v228 offset:1024
	ds_read_b128 v[170:173], v228 offset:2048
	ds_read_b128 v[174:177], v228 offset:3072
	ds_read_b128 v[178:181], v228 offset:4096
	ds_read_b128 v[182:185], v228 offset:5120
	ds_read_b128 v[186:189], v228 offset:6144
	ds_read_b128 v[230:233], v228 offset:7168
	s_add_i32 m0, s55, 0xc000
	s_nop 0
	global_load_lds_dwordx4 v96, s[2:3]
	v_mov_b32_e32 v96, v194
	s_add_i32 m0, s55, 0xe000
	s_nop 0
	global_load_lds_dwordx4 v96, s[2:3]
	s_waitcnt vmcnt(8)
	s_waitcnt lgkmcnt(0)
	s_barrier
	s_waitcnt lgkmcnt(0)
	v_mfma_f32_16x16x32_bf16 v[126:129], v[130:133], v[162:165], v[126:129]
	v_mfma_f32_16x16x32_bf16 v[122:125], v[138:141], v[162:165], v[122:125]
	v_mfma_f32_16x16x32_bf16 v[114:117], v[130:133], v[170:173], v[114:117]
	v_mfma_f32_16x16x32_bf16 v[106:109], v[138:141], v[170:173], v[106:109]
	v_mfma_f32_16x16x32_bf16 v[98:101], v[130:133], v[178:181], v[98:101]
	v_mfma_f32_16x16x32_bf16 v[88:91], v[138:141], v[178:181], v[88:91]
	v_mfma_f32_16x16x32_bf16 v[80:83], v[130:133], v[186:189], v[80:83]
	v_mfma_f32_16x16x32_bf16 v[72:75], v[138:141], v[186:189], v[72:75]
	v_mfma_f32_16x16x32_bf16 v[126:129], v[134:137], v[166:169], v[126:129]
	v_mfma_f32_16x16x32_bf16 v[122:125], v[142:145], v[166:169], v[122:125]
	v_mfma_f32_16x16x32_bf16 v[114:117], v[134:137], v[174:177], v[114:117]
	v_mfma_f32_16x16x32_bf16 v[106:109], v[142:145], v[174:177], v[106:109]
	v_mfma_f32_16x16x32_bf16 v[98:101], v[134:137], v[182:185], v[98:101]
	v_mfma_f32_16x16x32_bf16 v[88:91], v[142:145], v[182:185], v[88:91]
	v_mfma_f32_16x16x32_bf16 v[80:83], v[134:137], v[230:233], v[80:83]
	v_mfma_f32_16x16x32_bf16 v[72:75], v[142:145], v[230:233], v[72:75]
	v_mfma_f32_16x16x32_bf16 v[118:121], v[146:149], v[162:165], v[118:121]
	v_mfma_f32_16x16x32_bf16 v[110:113], v[154:157], v[162:165], v[110:113]
	v_mfma_f32_16x16x32_bf16 v[102:105], v[146:149], v[170:173], v[102:105]
	v_mfma_f32_16x16x32_bf16 v[92:95], v[154:157], v[170:173], v[92:95]
	v_mfma_f32_16x16x32_bf16 v[84:87], v[146:149], v[178:181], v[84:87]
	v_mfma_f32_16x16x32_bf16 v[76:79], v[154:157], v[178:181], v[76:79]
	v_mfma_f32_16x16x32_bf16 v[68:71], v[146:149], v[186:189], v[68:71]
	v_mfma_f32_16x16x32_bf16 v[64:67], v[154:157], v[186:189], v[64:67]
	v_mfma_f32_16x16x32_bf16 v[118:121], v[150:153], v[166:169], v[118:121]
	v_mfma_f32_16x16x32_bf16 v[110:113], v[158:161], v[166:169], v[110:113]
	v_mfma_f32_16x16x32_bf16 v[102:105], v[150:153], v[174:177], v[102:105]
	v_mfma_f32_16x16x32_bf16 v[92:95], v[158:161], v[174:177], v[92:95]
	v_mfma_f32_16x16x32_bf16 v[84:87], v[150:153], v[182:185], v[84:87]
	v_mfma_f32_16x16x32_bf16 v[76:79], v[158:161], v[182:185], v[76:79]
	v_mfma_f32_16x16x32_bf16 v[68:71], v[150:153], v[230:233], v[68:71]
	v_mfma_f32_16x16x32_bf16 v[64:67], v[158:161], v[230:233], v[64:67]
	s_barrier
	v_mov_b32_e32 v96, v192
	s_add_i32 s65, s65, s54
	ds_read_b128 v[162:165], v228 offset:16384
	ds_read_b128 v[166:169], v228 offset:17408
	ds_read_b128 v[170:173], v228 offset:18432
	ds_read_b128 v[174:177], v228 offset:19456
	ds_read_b128 v[178:181], v228 offset:20480
	ds_read_b128 v[182:185], v228 offset:21504
	ds_read_b128 v[186:189], v228 offset:22528
	ds_read_b128 v[230:233], v228 offset:23552
	s_mov_b32 m0, s65
	s_nop 0
	global_load_lds_dwordx4 v96, s[20:21]
	v_mov_b32_e32 v96, v195
	s_add_i32 m0, s65, 0x2000
	s_add_u32 s66, s20, 0x40000
	global_load_lds_dwordx4 v96, s[20:21]
	s_addc_u32 s67, s21, 0
	v_mov_b32_e32 v96, v192
	s_add_i32 s65, s68, s54
	s_mov_b32 m0, s65
	s_nop 0
	global_load_lds_dwordx4 v96, s[66:67]
	v_mov_b32_e32 v96, v195
	s_add_i32 m0, s65, 0x2000
	s_nop 0
	global_load_lds_dwordx4 v96, s[66:67]
	v_mov_b32_e32 v96, v190
	s_mov_b32 m0, s55
	s_nop 0
	global_load_lds_dwordx4 v96, s[4:5]
	v_mov_b32_e32 v96, v193
	s_mov_b32 m0, s56
	s_nop 0
	global_load_lds_dwordx4 v96, s[4:5]
	s_waitcnt vmcnt(8)
	s_waitcnt lgkmcnt(0)
	s_barrier
; #define PG8_STAGE(bufoff, gbase, voff) do { _Pragma("unroll") for (int _i = 0; _i < 2; ++_i) \
;         __builtin_amdgcn_global_load_lds((const __attribute__((address_space(1))) unsigned*)((const __attribute__((address_space(1))) char*)(gbase) + (unsigned)lnd_v((int)(voff)[_i])), (LAS unsigned*)(lds + (bufoff) + ldsw + _i * 8192), 16, 0, 0); } while (0)
; #define PG8_LDA(dst, b, h) do { _Pragma("unroll") for (int m = 0; m < 4; ++m) _Pragma("unroll") for (int k = 0; k < 2; ++k) dst[m][k] = *(const LAS bf16x8*)(lds + PG8_SA(b, h) + aoff + m * 2048 + k * 1024); } while (0)
; #define PG8_LDB(dst, b, h) do { _Pragma("unroll") for (int n = 0; n < 2; ++n) _Pragma("unroll") for (int k = 0; k < 2; ++k) dst[n][k] = *(const LAS bf16x8*)(lds + PG8_SB(b, h) + boff + n * 2048 + k * 1024); } while (0)
; #define PG8_MMA(ai, bj, At, Bt) do { __builtin_amdgcn_s_setprio(1); _Pragma("unroll") for (int m = 0; m < 4; ++m) _Pragma("unroll") for (int n = 0; n < 2; ++n) _Pragma("unroll") for (int k = 0; k < 2; ++k) \
;         acc[ai][bj][m][n] = __builtin_amdgcn_mfma_f32_16x16x32_bf16(Bt[n][k], At[m][k], acc[ai][bj][m][n], 0, 0, 0); __builtin_amdgcn_s_setprio(0); } while (0)
; #define PG8_WAIT_V(n) asm volatile("s_waitcnt vmcnt(" #n ")" ::: "memory")
; #define PG8_WAIT_L(n) asm volatile("s_waitcnt lgkmcnt(" #n ")" ::: "memory")
; #define PG8_BAR __builtin_amdgcn_s_barrier()
; #define PG8_SCHED __builtin_amdgcn_sched_barrier(0)
; template <class Desc, class Epi>
; __device__ __forceinline__ void gemm_phase(const int wv_, LAS unsigned char* lds, const Desc& d, const Epi& E) {
;     ...
;             PG8_WAIT_V(8); PG8_WAIT_L(0); PG8_BAR; PG8_MMA(1, 0, At, B0); PG8_MMA(1, 1, At, B1); PG8_BAR; PG8_SCHED;
;             PG8_LDB(B0, 1, 0); PG8_LDB(B1, 1, 1); PG8_SCHED; PG8_LDA(At, 1, 0); PG8_STAGE(PG8_SA(0, 1), a2, sA1);
;             PG8_WAIT_V(8); PG8_WAIT_L(0); PG8_BAR; PG8_MMA(0, 0, At, B0); PG8_MMA(0, 1, At, B1); PG8_BAR; PG8_SCHED;
	s_waitcnt lgkmcnt(0)
	v_mfma_f32_16x16x32_bf16 v[60:63], v[130:133], v[162:165], v[60:63]
	v_mfma_f32_16x16x32_bf16 v[56:59], v[138:141], v[162:165], v[56:59]
	v_mfma_f32_16x16x32_bf16 v[40:43], v[130:133], v[170:173], v[40:43]
	v_mfma_f32_16x16x32_bf16 v[32:35], v[138:141], v[170:173], v[32:35]
	v_mfma_f32_16x16x32_bf16 v[16:19], v[130:133], v[178:181], v[16:19]
	v_mfma_f32_16x16x32_bf16 v[8:11], v[138:141], v[178:181], v[8:11]
	v_mfma_f32_16x16x32_bf16 v[4:7], v[130:133], v[186:189], v[4:7]
	v_mfma_f32_16x16x32_bf16 v[0:3], v[138:141], v[186:189], v[0:3]
	v_mfma_f32_16x16x32_bf16 v[60:63], v[134:137], v[166:169], v[60:63]
	v_mfma_f32_16x16x32_bf16 v[56:59], v[142:145], v[166:169], v[56:59]
	v_mfma_f32_16x16x32_bf16 v[40:43], v[134:137], v[174:177], v[40:43]
	v_mfma_f32_16x16x32_bf16 v[32:35], v[142:145], v[174:177], v[32:35]
	v_mfma_f32_16x16x32_bf16 v[16:19], v[134:137], v[182:185], v[16:19]
	v_mfma_f32_16x16x32_bf16 v[8:11], v[142:145], v[182:185], v[8:11]
	v_mfma_f32_16x16x32_bf16 v[4:7], v[134:137], v[230:233], v[4:7]
	v_mfma_f32_16x16x32_bf16 v[0:3], v[142:145], v[230:233], v[0:3]
	v_mfma_f32_16x16x32_bf16 v[44:47], v[146:149], v[162:165], v[44:47]
	v_mfma_f32_16x16x32_bf16 v[36:39], v[154:157], v[162:165], v[36:39]
	v_mfma_f32_16x16x32_bf16 v[20:23], v[146:149], v[170:173], v[20:23]
	v_mfma_f32_16x16x32_bf16 v[12:15], v[154:157], v[170:173], v[12:15]
	v_mfma_f32_16x16x32_bf16 v[52:55], v[146:149], v[178:181], v[52:55]
	v_mfma_f32_16x16x32_bf16 v[48:51], v[154:157], v[178:181], v[48:51]
	v_mfma_f32_16x16x32_bf16 v[28:31], v[146:149], v[186:189], v[28:31]
	v_mfma_f32_16x16x32_bf16 v[24:27], v[154:157], v[186:189], v[24:27]
	v_mfma_f32_16x16x32_bf16 v[44:47], v[150:153], v[166:169], v[44:47]
	v_mfma_f32_16x16x32_bf16 v[36:39], v[158:161], v[166:169], v[36:39]
	v_mfma_f32_16x16x32_bf16 v[20:23], v[150:153], v[174:177], v[20:23]
	v_mfma_f32_16x16x32_bf16 v[12:15], v[158:161], v[174:177], v[12:15]
	v_mfma_f32_16x16x32_bf16 v[52:55], v[150:153], v[182:185], v[52:55]
	v_mfma_f32_16x16x32_bf16 v[48:51], v[158:161], v[182:185], v[48:51]
	v_mfma_f32_16x16x32_bf16 v[28:31], v[150:153], v[230:233], v[28:31]
	v_mfma_f32_16x16x32_bf16 v[24:27], v[158:161], v[230:233], v[24:27]
	s_barrier
	s_add_i32 s65, 0, 0x18000
	v_add_u32_e32 v96, s65, v197
	s_add_i32 s66, 0, 0x1c000
	ds_read_b128 v[130:133], v96
	ds_read_b128 v[134:137], v96 offset:1024
	ds_read_b128 v[138:141], v96 offset:2048
	ds_read_b128 v[142:145], v96 offset:3072
	v_add_u32_e32 v96, s66, v197
	ds_read_b128 v[146:149], v96
	ds_read_b128 v[150:153], v96 offset:1024
	ds_read_b128 v[154:157], v96 offset:2048
	ds_read_b128 v[158:161], v96 offset:3072
	v_mov_b32_e32 v96, v191
	s_mov_b32 m0, s57
	ds_read_b128 v[162:165], v228 offset:32768
	ds_read_b128 v[166:169], v228 offset:33792
	ds_read_b128 v[170:173], v228 offset:34816
	ds_read_b128 v[174:177], v228 offset:35840
	ds_read_b128 v[178:181], v228 offset:36864
	ds_read_b128 v[182:185], v228 offset:37888
	ds_read_b128 v[186:189], v228 offset:38912
	ds_read_b128 v[230:233], v228 offset:39936
	s_nop 0
	global_load_lds_dwordx4 v96, s[4:5]
	v_mov_b32_e32 v96, v194
	s_mov_b32 m0, s58
	s_nop 0
	global_load_lds_dwordx4 v96, s[4:5]
	s_waitcnt vmcnt(8)
	s_waitcnt lgkmcnt(0)
	s_barrier
	s_waitcnt lgkmcnt(0)
	v_mfma_f32_16x16x32_bf16 v[126:129], v[130:133], v[162:165], v[126:129]
	v_mfma_f32_16x16x32_bf16 v[122:125], v[138:141], v[162:165], v[122:125]
	v_mfma_f32_16x16x32_bf16 v[114:117], v[130:133], v[170:173], v[114:117]
	v_mfma_f32_16x16x32_bf16 v[106:109], v[138:141], v[170:173], v[106:109]
	v_mfma_f32_16x16x32_bf16 v[98:101], v[130:133], v[178:181], v[98:101]
	v_mfma_f32_16x16x32_bf16 v[88:91], v[138:141], v[178:181], v[88:91]
	v_mfma_f32_16x16x32_bf16 v[80:83], v[130:133], v[186:189], v[80:83]
	v_mfma_f32_16x16x32_bf16 v[72:75], v[138:141], v[186:189], v[72:75]
	v_mfma_f32_16x16x32_bf16 v[126:129], v[134:137], v[166:169], v[126:129]
	v_mfma_f32_16x16x32_bf16 v[122:125], v[142:145], v[166:169], v[122:125]
	v_mfma_f32_16x16x32_bf16 v[114:117], v[134:137], v[174:177], v[114:117]
	v_mfma_f32_16x16x32_bf16 v[106:109], v[142:145], v[174:177], v[106:109]
	v_mfma_f32_16x16x32_bf16 v[98:101], v[134:137], v[182:185], v[98:101]
	v_mfma_f32_16x16x32_bf16 v[88:91], v[142:145], v[182:185], v[88:91]
	v_mfma_f32_16x16x32_bf16 v[80:83], v[134:137], v[230:233], v[80:83]
	v_mfma_f32_16x16x32_bf16 v[72:75], v[142:145], v[230:233], v[72:75]
	v_mfma_f32_16x16x32_bf16 v[118:121], v[146:149], v[162:165], v[118:121]
	v_mfma_f32_16x16x32_bf16 v[110:113], v[154:157], v[162:165], v[110:113]
	v_mfma_f32_16x16x32_bf16 v[102:105], v[146:149], v[170:173], v[102:105]
	v_mfma_f32_16x16x32_bf16 v[92:95], v[154:157], v[170:173], v[92:95]
	v_mfma_f32_16x16x32_bf16 v[84:87], v[146:149], v[178:181], v[84:87]
	v_mfma_f32_16x16x32_bf16 v[76:79], v[154:157], v[178:181], v[76:79]
	v_mfma_f32_16x16x32_bf16 v[68:71], v[146:149], v[186:189], v[68:71]
	v_mfma_f32_16x16x32_bf16 v[64:67], v[154:157], v[186:189], v[64:67]
	v_mfma_f32_16x16x32_bf16 v[118:121], v[150:153], v[166:169], v[118:121]
	v_mfma_f32_16x16x32_bf16 v[110:113], v[158:161], v[166:169], v[110:113]
	v_mfma_f32_16x16x32_bf16 v[102:105], v[150:153], v[174:177], v[102:105]
	v_mfma_f32_16x16x32_bf16 v[92:95], v[158:161], v[174:177], v[92:95]
	v_mfma_f32_16x16x32_bf16 v[84:87], v[150:153], v[182:185], v[84:87]
	v_mfma_f32_16x16x32_bf16 v[76:79], v[158:161], v[182:185], v[76:79]
	v_mfma_f32_16x16x32_bf16 v[68:71], v[150:153], v[230:233], v[68:71]
	v_mfma_f32_16x16x32_bf16 v[64:67], v[158:161], v[230:233], v[64:67]
	s_barrier
; #define PG8_STAGE(bufoff, gbase, voff) do { _Pragma("unroll") for (int _i = 0; _i < 2; ++_i) \
;         __builtin_amdgcn_global_load_lds((const __attribute__((address_space(1))) unsigned*)((const __attribute__((address_space(1))) char*)(gbase) + (unsigned)lnd_v((int)(voff)[_i])), (LAS unsigned*)(lds + (bufoff) + ldsw + _i * 8192), 16, 0, 0); } while (0)
; #define PG8_LDA(dst, b, h) do { _Pragma("unroll") for (int m = 0; m < 4; ++m) _Pragma("unroll") for (int k = 0; k < 2; ++k) dst[m][k] = *(const LAS bf16x8*)(lds + PG8_SA(b, h) + aoff + m * 2048 + k * 1024); } while (0)
; #define PG8_MMA(ai, bj, At, Bt) do { __builtin_amdgcn_s_setprio(1); _Pragma("unroll") for (int m = 0; m < 4; ++m) _Pragma("unroll") for (int n = 0; n < 2; ++n) _Pragma("unroll") for (int k = 0; k < 2; ++k) \
;         acc[ai][bj][m][n] = __builtin_amdgcn_mfma_f32_16x16x32_bf16(Bt[n][k], At[m][k], acc[ai][bj][m][n], 0, 0, 0); __builtin_amdgcn_s_setprio(0); } while (0)
; #define PG8_WAIT_V(n) asm volatile("s_waitcnt vmcnt(" #n ")" ::: "memory")
; #define PG8_WAIT_L(n) asm volatile("s_waitcnt lgkmcnt(" #n ")" ::: "memory")
; #define PG8_BAR __builtin_amdgcn_s_barrier()
; #define PG8_SCHED __builtin_amdgcn_sched_barrier(0)
; template <class Desc, class Epi>
; __device__ __forceinline__ void gemm_phase(const int wv_, LAS unsigned char* lds, const Desc& d, const Epi& E) {
;     ...
;             PG8_LDA(At, 1, 1); PG8_STAGE(PG8_SB(1, 0), b3, voffB); PG8_STAGE(PG8_SB(1, 1), b3 + hstepB, voffB); PG8_STAGE(PG8_SA(1, 0), a3, sA0);
;             PG8_WAIT_V(8); PG8_WAIT_L(0); PG8_BAR; PG8_MMA(1, 0, At, B0); PG8_MMA(1, 1, At, B1); PG8_BAR; PG8_SCHED;
;         }
;         if (wr == 0) PG8_BAR;
	v_mov_b32_e32 v96, v192
	ds_read_b128 v[162:165], v228 offset:49152
	ds_read_b128 v[166:169], v228 offset:50176
	ds_read_b128 v[170:173], v228 offset:51200
	ds_read_b128 v[174:177], v228 offset:52224
	ds_read_b128 v[178:181], v228 offset:53248
	ds_read_b128 v[182:185], v228 offset:54272
	ds_read_b128 v[186:189], v228 offset:55296
	ds_read_b128 v[230:233], v228 offset:56320
	s_add_i32 s65, s65, s54
	v_lshl_add_u64 v[234:235], s[20:21], 0, v[96:97]
	v_lshl_add_u64 v[234:235], v[234:235], 0, s[30:31]
	s_mov_b32 m0, s65
	v_mov_b32_e32 v96, v195
	global_load_lds_dwordx4 v[234:235], off
	s_add_i32 m0, s65, 0x2000
	s_nop 0
	v_lshl_add_u64 v[234:235], s[20:21], 0, v[96:97]
	s_add_u32 s20, s20, 0x40080
	v_lshl_add_u64 v[234:235], v[234:235], 0, s[30:31]
	s_addc_u32 s21, s21, 0
	v_mov_b32_e32 v96, v192
	s_add_i32 s65, s66, s54
	global_load_lds_dwordx4 v[234:235], off
	s_mov_b32 m0, s65
	s_nop 0
	global_load_lds_dwordx4 v96, s[20:21]
	v_mov_b32_e32 v96, v195
	s_add_i32 m0, s65, 0x2000
	s_nop 0
	global_load_lds_dwordx4 v96, s[20:21]
	v_mov_b32_e32 v96, v190
	s_mov_b32 m0, s59
	v_lshl_add_u64 v[234:235], s[4:5], 0, v[96:97]
	v_lshl_add_u64 v[234:235], v[234:235], 0, s[30:31]
	v_mov_b32_e32 v96, v193
	global_load_lds_dwordx4 v[234:235], off
	s_mov_b32 m0, s60
	v_lshl_add_u64 v[234:235], s[4:5], 0, v[96:97]
	v_lshl_add_u64 v[234:235], v[234:235], 0, s[30:31]
	global_load_lds_dwordx4 v[234:235], off
	s_waitcnt vmcnt(8)
	s_waitcnt lgkmcnt(0)
	s_barrier
	s_waitcnt lgkmcnt(0)
	v_mfma_f32_16x16x32_bf16 v[60:63], v[130:133], v[162:165], v[60:63]
	v_mfma_f32_16x16x32_bf16 v[56:59], v[138:141], v[162:165], v[56:59]
	v_mfma_f32_16x16x32_bf16 v[40:43], v[130:133], v[170:173], v[40:43]
	v_mfma_f32_16x16x32_bf16 v[32:35], v[138:141], v[170:173], v[32:35]
	v_mfma_f32_16x16x32_bf16 v[16:19], v[130:133], v[178:181], v[16:19]
	v_mfma_f32_16x16x32_bf16 v[8:11], v[138:141], v[178:181], v[8:11]
	v_mfma_f32_16x16x32_bf16 v[4:7], v[130:133], v[186:189], v[4:7]
	v_mfma_f32_16x16x32_bf16 v[0:3], v[138:141], v[186:189], v[0:3]
	v_mfma_f32_16x16x32_bf16 v[60:63], v[134:137], v[166:169], v[60:63]
	v_mfma_f32_16x16x32_bf16 v[56:59], v[142:145], v[166:169], v[56:59]
	v_mfma_f32_16x16x32_bf16 v[40:43], v[134:137], v[174:177], v[40:43]
	v_mfma_f32_16x16x32_bf16 v[32:35], v[142:145], v[174:177], v[32:35]
	v_mfma_f32_16x16x32_bf16 v[16:19], v[134:137], v[182:185], v[16:19]
	v_mfma_f32_16x16x32_bf16 v[8:11], v[142:145], v[182:185], v[8:11]
	v_mfma_f32_16x16x32_bf16 v[4:7], v[134:137], v[230:233], v[4:7]
	v_mfma_f32_16x16x32_bf16 v[0:3], v[142:145], v[230:233], v[0:3]
	v_mfma_f32_16x16x32_bf16 v[44:47], v[146:149], v[162:165], v[44:47]
	v_mfma_f32_16x16x32_bf16 v[36:39], v[154:157], v[162:165], v[36:39]
	v_mfma_f32_16x16x32_bf16 v[20:23], v[146:149], v[170:173], v[20:23]
	v_mfma_f32_16x16x32_bf16 v[12:15], v[154:157], v[170:173], v[12:15]
	v_mfma_f32_16x16x32_bf16 v[52:55], v[146:149], v[178:181], v[52:55]
	v_mfma_f32_16x16x32_bf16 v[48:51], v[154:157], v[178:181], v[48:51]
	v_mfma_f32_16x16x32_bf16 v[28:31], v[146:149], v[186:189], v[28:31]
	v_mfma_f32_16x16x32_bf16 v[24:27], v[154:157], v[186:189], v[24:27]
	v_mfma_f32_16x16x32_bf16 v[44:47], v[150:153], v[166:169], v[44:47]
	v_mfma_f32_16x16x32_bf16 v[36:39], v[158:161], v[166:169], v[36:39]
	v_mfma_f32_16x16x32_bf16 v[20:23], v[150:153], v[174:177], v[20:23]
	v_mfma_f32_16x16x32_bf16 v[12:15], v[158:161], v[174:177], v[12:15]
	v_mfma_f32_16x16x32_bf16 v[52:55], v[150:153], v[182:185], v[52:55]
	v_mfma_f32_16x16x32_bf16 v[48:51], v[158:161], v[182:185], v[48:51]
	v_mfma_f32_16x16x32_bf16 v[28:31], v[150:153], v[230:233], v[28:31]
	v_mfma_f32_16x16x32_bf16 v[24:27], v[158:161], v[230:233], v[24:27]
	s_barrier
	s_add_i32 s45, s45, 2
	s_add_u32 s2, s2, 0x100
	s_addc_u32 s3, s3, 0
	s_add_u32 s1, s1, 0x100
	s_addc_u32 s29, s29, 0
	s_cmp_gt_u32 s45, 13
	s_cbranch_scc0 .LBB0_1161
	s_and_b64 vcc, exec, s[42:43]
	s_cbranch_vccz .LBB0_1164
	s_barrier

; #define PG8_STAGE(bufoff, gbase, voff) do { _Pragma("unroll") for (int _i = 0; _i < 2; ++_i) \
;         __builtin_amdgcn_global_load_lds((const __attribute__((address_space(1))) unsigned*)((const __attribute__((address_space(1))) char*)(gbase) + (unsigned)lnd_v((int)(voff)[_i])), (LAS unsigned*)(lds + (bufoff) + ldsw + _i * 8192), 16, 0, 0); } while (0)
; #define PG8_LDA(dst, b, h) do { _Pragma("unroll") for (int m = 0; m < 4; ++m) _Pragma("unroll") for (int k = 0; k < 2; ++k) dst[m][k] = *(const LAS bf16x8*)(lds + PG8_SA(b, h) + aoff + m * 2048 + k * 1024); } while (0)
; #define PG8_LDB(dst, b, h) do { _Pragma("unroll") for (int n = 0; n < 2; ++n) _Pragma("unroll") for (int k = 0; k < 2; ++k) dst[n][k] = *(const LAS bf16x8*)(lds + PG8_SB(b, h) + boff + n * 2048 + k * 1024); } while (0)
; #define PG8_WAIT_V(n) asm volatile("s_waitcnt vmcnt(" #n ")" ::: "memory")
; #define PG8_WAIT_L(n) asm volatile("s_waitcnt lgkmcnt(" #n ")" ::: "memory")
; #define PG8_BAR __builtin_amdgcn_s_barrier()
; template <class Desc, class Epi>
; __device__ __forceinline__ void gemm_phase(const int wv_, LAS unsigned char* lds, const Desc& d, const Epi& E) {
;     ...
;         for (int t = 0; t < nt; t += 2) {
;             const bool last = (t == nt - 2);
;             unsigned sA0[2], sA1[2];
;             if constexpr (Desc::GATHER) { sA0[0] = last ? voffAn[0] : voffA[0]; sA0[1] = last ? voffAn[1] : voffA[1]; sA1[0] = last ? voffAn1[0] : voffA1[0]; sA1[1] = last ? voffAn1[1] : voffA1[1]; }
;             else { sA0[0] = voffA[0]; sA0[1] = voffA[1]; sA1[0] = voffA1[0]; sA1[1] = voffA1[1]; }
;             const char* a1 = cA + (size_t)(t + 1) * kstep;
;             const char* a2 = last ? nA : cA + (size_t)(t + 2) * kstep; const char* b2 = last ? nB : cB + (size_t)(t + 2) * kstep;
;             const char* a3 = a2 + kstep; const char* b3 = b2 + kstep;
;             PG8_LDB(B0, 0, 0); PG8_LDB(B1, 0, 1); PG8_SCHED; PG8_LDA(At, 0, 0); PG8_STAGE(PG8_SA(1, 1), a1, voffA1);
;             PG8_WAIT_V(8); PG8_WAIT_L(0); PG8_BAR; PG8_MMA(0, 0, At, B0); PG8_MMA(0, 1, At, B1); PG8_BAR; PG8_SCHED;
;             PG8_LDA(At, 0, 1); PG8_STAGE(PG8_SB(0, 0), b2, voffB); PG8_STAGE(PG8_SB(0, 1), b2 + hstepB, voffB); PG8_STAGE(PG8_SA(0, 0), a2, sA0);
;             PG8_WAIT_V(8); PG8_WAIT_L(0); PG8_BAR; PG8_MMA(1, 0, At, B0); PG8_MMA(1, 1, At, B1); PG8_BAR; PG8_SCHED;
.LBB0_1262:
	s_add_u32 s4, s2, 0x80
	s_addc_u32 s5, s3, 0
	s_add_i32 s62, 0, 0x10000
	s_cmp_eq_u32 s61, 12
	s_cselect_b32 s5, s45, s5
	s_cselect_b32 s4, s44, s4
	v_add_u32_e32 v96, s62, v213
	s_cselect_b32 s21, s47, s43
	s_cselect_b32 s20, s46, s29
	s_add_i32 s64, 0, 0x14000
	ds_read_b128 v[130:133], v96
	ds_read_b128 v[134:137], v96 offset:1024
	ds_read_b128 v[138:141], v96 offset:2048
	ds_read_b128 v[142:145], v96 offset:3072
	v_add_u32_e32 v96, s64, v213
	ds_read_b128 v[146:149], v96
	ds_read_b128 v[150:153], v96 offset:1024
	ds_read_b128 v[154:157], v96 offset:2048
	ds_read_b128 v[158:161], v96 offset:3072
	v_mov_b32_e32 v96, v207
	ds_read_b128 v[162:165], v221
	ds_read_b128 v[166:169], v221 offset:1024
	ds_read_b128 v[170:173], v221 offset:2048
	ds_read_b128 v[174:177], v221 offset:3072
	ds_read_b128 v[178:181], v221 offset:4096
	ds_read_b128 v[182:185], v221 offset:5120
	ds_read_b128 v[186:189], v221 offset:6144
	ds_read_b128 v[190:193], v221 offset:7168
	s_add_i32 m0, s53, 0xc000
	s_nop 0
	global_load_lds_dwordx4 v96, s[2:3]
	v_mov_b32_e32 v96, v210
	s_add_i32 m0, s53, 0xe000
	s_nop 0
	global_load_lds_dwordx4 v96, s[2:3]
	s_waitcnt vmcnt(8)
	s_waitcnt lgkmcnt(0)
	s_barrier
	s_waitcnt lgkmcnt(0)
	v_mfma_f32_16x16x32_bf16 v[126:129], v[130:133], v[162:165], v[126:129]
	v_mfma_f32_16x16x32_bf16 v[122:125], v[138:141], v[162:165], v[122:125]
	v_mfma_f32_16x16x32_bf16 v[110:113], v[130:133], v[170:173], v[110:113]
	v_mfma_f32_16x16x32_bf16 v[106:109], v[138:141], v[170:173], v[106:109]
	v_mfma_f32_16x16x32_bf16 v[92:95], v[130:133], v[178:181], v[92:95]
	v_mfma_f32_16x16x32_bf16 v[88:91], v[138:141], v[178:181], v[88:91]
	v_mfma_f32_16x16x32_bf16 v[76:79], v[130:133], v[186:189], v[76:79]
	v_mfma_f32_16x16x32_bf16 v[72:75], v[138:141], v[186:189], v[72:75]
	v_mfma_f32_16x16x32_bf16 v[126:129], v[134:137], v[166:169], v[126:129]
	v_mfma_f32_16x16x32_bf16 v[122:125], v[142:145], v[166:169], v[122:125]
	v_mfma_f32_16x16x32_bf16 v[110:113], v[134:137], v[174:177], v[110:113]
	v_mfma_f32_16x16x32_bf16 v[106:109], v[142:145], v[174:177], v[106:109]
	v_mfma_f32_16x16x32_bf16 v[92:95], v[134:137], v[182:185], v[92:95]
	v_mfma_f32_16x16x32_bf16 v[88:91], v[142:145], v[182:185], v[88:91]
	v_mfma_f32_16x16x32_bf16 v[76:79], v[134:137], v[190:193], v[76:79]
	v_mfma_f32_16x16x32_bf16 v[72:75], v[142:145], v[190:193], v[72:75]
	v_mfma_f32_16x16x32_bf16 v[118:121], v[146:149], v[162:165], v[118:121]
	v_mfma_f32_16x16x32_bf16 v[114:117], v[154:157], v[162:165], v[114:117]
	v_mfma_f32_16x16x32_bf16 v[102:105], v[146:149], v[170:173], v[102:105]
	v_mfma_f32_16x16x32_bf16 v[98:101], v[154:157], v[170:173], v[98:101]
	v_mfma_f32_16x16x32_bf16 v[84:87], v[146:149], v[178:181], v[84:87]
	v_mfma_f32_16x16x32_bf16 v[80:83], v[154:157], v[178:181], v[80:83]
	v_mfma_f32_16x16x32_bf16 v[68:71], v[146:149], v[186:189], v[68:71]
	v_mfma_f32_16x16x32_bf16 v[64:67], v[154:157], v[186:189], v[64:67]
	v_mfma_f32_16x16x32_bf16 v[118:121], v[150:153], v[166:169], v[118:121]
	v_mfma_f32_16x16x32_bf16 v[114:117], v[158:161], v[166:169], v[114:117]
	v_mfma_f32_16x16x32_bf16 v[102:105], v[150:153], v[174:177], v[102:105]
	v_mfma_f32_16x16x32_bf16 v[98:101], v[158:161], v[174:177], v[98:101]
	v_mfma_f32_16x16x32_bf16 v[84:87], v[150:153], v[182:185], v[84:87]
	v_mfma_f32_16x16x32_bf16 v[80:83], v[158:161], v[182:185], v[80:83]
	v_mfma_f32_16x16x32_bf16 v[68:71], v[150:153], v[190:193], v[68:71]
	v_mfma_f32_16x16x32_bf16 v[64:67], v[158:161], v[190:193], v[64:67]
	s_barrier
	v_mov_b32_e32 v96, v208
	s_add_i32 s62, s62, s52
	ds_read_b128 v[162:165], v221 offset:16384
	ds_read_b128 v[166:169], v221 offset:17408
	ds_read_b128 v[170:173], v221 offset:18432
	ds_read_b128 v[174:177], v221 offset:19456
	ds_read_b128 v[178:181], v221 offset:20480
	ds_read_b128 v[182:185], v221 offset:21504
	ds_read_b128 v[186:189], v221 offset:22528
	ds_read_b128 v[190:193], v221 offset:23552
	s_mov_b32 m0, s62
	s_nop 0
	global_load_lds_dwordx4 v96, s[20:21]
	v_mov_b32_e32 v96, v211
	s_add_i32 m0, s62, 0x2000
	s_add_u32 s62, s20, 0x40000
	global_load_lds_dwordx4 v96, s[20:21]
	s_addc_u32 s63, s21, 0
	v_mov_b32_e32 v96, v208
	s_add_i32 s64, s64, s52
	s_mov_b32 m0, s64
	s_nop 0
	global_load_lds_dwordx4 v96, s[62:63]
	v_mov_b32_e32 v96, v211
	s_add_i32 m0, s64, 0x2000
	s_nop 0
	global_load_lds_dwordx4 v96, s[62:63]
	v_mov_b32_e32 v96, v206
	s_mov_b32 m0, s53
	s_nop 0
	global_load_lds_dwordx4 v96, s[4:5]
	v_mov_b32_e32 v96, v209
	s_mov_b32 m0, s54
	s_nop 0
	global_load_lds_dwordx4 v96, s[4:5]
	s_waitcnt vmcnt(8)
	s_waitcnt lgkmcnt(0)
	s_barrier
; #define PG8_STAGE(bufoff, gbase, voff) do { _Pragma("unroll") for (int _i = 0; _i < 2; ++_i) \
;         __builtin_amdgcn_global_load_lds((const __attribute__((address_space(1))) unsigned*)((const __attribute__((address_space(1))) char*)(gbase) + (unsigned)lnd_v((int)(voff)[_i])), (LAS unsigned*)(lds + (bufoff) + ldsw + _i * 8192), 16, 0, 0); } while (0)
; #define PG8_LDA(dst, b, h) do { _Pragma("unroll") for (int m = 0; m < 4; ++m) _Pragma("unroll") for (int k = 0; k < 2; ++k) dst[m][k] = *(const LAS bf16x8*)(lds + PG8_SA(b, h) + aoff + m * 2048 + k * 1024); } while (0)
; #define PG8_LDB(dst, b, h) do { _Pragma("unroll") for (int n = 0; n < 2; ++n) _Pragma("unroll") for (int k = 0; k < 2; ++k) dst[n][k] = *(const LAS bf16x8*)(lds + PG8_SB(b, h) + boff + n * 2048 + k * 1024); } while (0)
; #define PG8_MMA(ai, bj, At, Bt) do { __builtin_amdgcn_s_setprio(1); _Pragma("unroll") for (int m = 0; m < 4; ++m) _Pragma("unroll") for (int n = 0; n < 2; ++n) _Pragma("unroll") for (int k = 0; k < 2; ++k) \
;         acc[ai][bj][m][n] = __builtin_amdgcn_mfma_f32_16x16x32_bf16(Bt[n][k], At[m][k], acc[ai][bj][m][n], 0, 0, 0); __builtin_amdgcn_s_setprio(0); } while (0)
; #define PG8_WAIT_V(n) asm volatile("s_waitcnt vmcnt(" #n ")" ::: "memory")
; #define PG8_WAIT_L(n) asm volatile("s_waitcnt lgkmcnt(" #n ")" ::: "memory")
; #define PG8_BAR __builtin_amdgcn_s_barrier()
; #define PG8_SCHED __builtin_amdgcn_sched_barrier(0)
; template <class Desc, class Epi>
; __device__ __forceinline__ void gemm_phase(const int wv_, LAS unsigned char* lds, const Desc& d, const Epi& E) {
;     ...
;             PG8_WAIT_V(8); PG8_WAIT_L(0); PG8_BAR; PG8_MMA(1, 0, At, B0); PG8_MMA(1, 1, At, B1); PG8_BAR; PG8_SCHED;
;             PG8_LDB(B0, 1, 0); PG8_LDB(B1, 1, 1); PG8_SCHED; PG8_LDA(At, 1, 0); PG8_STAGE(PG8_SA(0, 1), a2, sA1);
;             PG8_WAIT_V(8); PG8_WAIT_L(0); PG8_BAR; PG8_MMA(0, 0, At, B0); PG8_MMA(0, 1, At, B1); PG8_BAR; PG8_SCHED;
	s_waitcnt lgkmcnt(0)
	v_mfma_f32_16x16x32_bf16 v[60:63], v[130:133], v[162:165], v[60:63]
	v_mfma_f32_16x16x32_bf16 v[56:59], v[138:141], v[162:165], v[56:59]
	v_mfma_f32_16x16x32_bf16 v[44:47], v[130:133], v[170:173], v[44:47]
	v_mfma_f32_16x16x32_bf16 v[40:43], v[138:141], v[170:173], v[40:43]
	v_mfma_f32_16x16x32_bf16 v[24:27], v[130:133], v[178:181], v[24:27]
	v_mfma_f32_16x16x32_bf16 v[16:19], v[138:141], v[178:181], v[16:19]
	v_mfma_f32_16x16x32_bf16 v[4:7], v[130:133], v[186:189], v[4:7]
	v_mfma_f32_16x16x32_bf16 v[0:3], v[138:141], v[186:189], v[0:3]
	v_mfma_f32_16x16x32_bf16 v[60:63], v[134:137], v[166:169], v[60:63]
	v_mfma_f32_16x16x32_bf16 v[56:59], v[142:145], v[166:169], v[56:59]
	v_mfma_f32_16x16x32_bf16 v[44:47], v[134:137], v[174:177], v[44:47]
	v_mfma_f32_16x16x32_bf16 v[40:43], v[142:145], v[174:177], v[40:43]
	v_mfma_f32_16x16x32_bf16 v[24:27], v[134:137], v[182:185], v[24:27]
	v_mfma_f32_16x16x32_bf16 v[16:19], v[142:145], v[182:185], v[16:19]
	v_mfma_f32_16x16x32_bf16 v[4:7], v[134:137], v[190:193], v[4:7]
	v_mfma_f32_16x16x32_bf16 v[0:3], v[142:145], v[190:193], v[0:3]
	v_mfma_f32_16x16x32_bf16 v[52:55], v[146:149], v[162:165], v[52:55]
	v_mfma_f32_16x16x32_bf16 v[48:51], v[154:157], v[162:165], v[48:51]
	v_mfma_f32_16x16x32_bf16 v[28:31], v[146:149], v[170:173], v[28:31]
	v_mfma_f32_16x16x32_bf16 v[20:23], v[154:157], v[170:173], v[20:23]
	v_mfma_f32_16x16x32_bf16 v[36:39], v[146:149], v[178:181], v[36:39]
	v_mfma_f32_16x16x32_bf16 v[32:35], v[154:157], v[178:181], v[32:35]
	v_mfma_f32_16x16x32_bf16 v[12:15], v[146:149], v[186:189], v[12:15]
	v_mfma_f32_16x16x32_bf16 v[8:11], v[154:157], v[186:189], v[8:11]
	v_mfma_f32_16x16x32_bf16 v[52:55], v[150:153], v[166:169], v[52:55]
	v_mfma_f32_16x16x32_bf16 v[48:51], v[158:161], v[166:169], v[48:51]
	v_mfma_f32_16x16x32_bf16 v[28:31], v[150:153], v[174:177], v[28:31]
	v_mfma_f32_16x16x32_bf16 v[20:23], v[158:161], v[174:177], v[20:23]
	v_mfma_f32_16x16x32_bf16 v[36:39], v[150:153], v[182:185], v[36:39]
	v_mfma_f32_16x16x32_bf16 v[32:35], v[158:161], v[182:185], v[32:35]
	v_mfma_f32_16x16x32_bf16 v[12:15], v[150:153], v[190:193], v[12:15]
	v_mfma_f32_16x16x32_bf16 v[8:11], v[158:161], v[190:193], v[8:11]
	s_barrier
	s_add_i32 s62, 0, 0x18000
	v_add_u32_e32 v96, s62, v213
	s_add_i32 s63, 0, 0x1c000
	ds_read_b128 v[130:133], v96
	ds_read_b128 v[134:137], v96 offset:1024
	ds_read_b128 v[138:141], v96 offset:2048
	ds_read_b128 v[142:145], v96 offset:3072
	v_add_u32_e32 v96, s63, v213
	ds_read_b128 v[146:149], v96
	ds_read_b128 v[150:153], v96 offset:1024
	ds_read_b128 v[154:157], v96 offset:2048
	ds_read_b128 v[158:161], v96 offset:3072
	v_mov_b32_e32 v96, v207
	s_mov_b32 m0, s55
	ds_read_b128 v[162:165], v221 offset:32768
	ds_read_b128 v[166:169], v221 offset:33792
	ds_read_b128 v[170:173], v221 offset:34816
	ds_read_b128 v[174:177], v221 offset:35840
	ds_read_b128 v[178:181], v221 offset:36864
	ds_read_b128 v[182:185], v221 offset:37888
	ds_read_b128 v[186:189], v221 offset:38912
	ds_read_b128 v[190:193], v221 offset:39936
	s_nop 0
	global_load_lds_dwordx4 v96, s[4:5]
	v_mov_b32_e32 v96, v210
	s_mov_b32 m0, s56
	s_nop 0
	global_load_lds_dwordx4 v96, s[4:5]
	s_waitcnt vmcnt(8)
	s_waitcnt lgkmcnt(0)
	s_barrier
	s_waitcnt lgkmcnt(0)
	v_mfma_f32_16x16x32_bf16 v[126:129], v[130:133], v[162:165], v[126:129]
	v_mfma_f32_16x16x32_bf16 v[122:125], v[138:141], v[162:165], v[122:125]
	v_mfma_f32_16x16x32_bf16 v[110:113], v[130:133], v[170:173], v[110:113]
	v_mfma_f32_16x16x32_bf16 v[106:109], v[138:141], v[170:173], v[106:109]
	v_mfma_f32_16x16x32_bf16 v[92:95], v[130:133], v[178:181], v[92:95]
	v_mfma_f32_16x16x32_bf16 v[88:91], v[138:141], v[178:181], v[88:91]
	v_mfma_f32_16x16x32_bf16 v[76:79], v[130:133], v[186:189], v[76:79]
	v_mfma_f32_16x16x32_bf16 v[72:75], v[138:141], v[186:189], v[72:75]
	v_mfma_f32_16x16x32_bf16 v[126:129], v[134:137], v[166:169], v[126:129]
	v_mfma_f32_16x16x32_bf16 v[122:125], v[142:145], v[166:169], v[122:125]
	v_mfma_f32_16x16x32_bf16 v[110:113], v[134:137], v[174:177], v[110:113]
	v_mfma_f32_16x16x32_bf16 v[106:109], v[142:145], v[174:177], v[106:109]
	v_mfma_f32_16x16x32_bf16 v[92:95], v[134:137], v[182:185], v[92:95]
	v_mfma_f32_16x16x32_bf16 v[88:91], v[142:145], v[182:185], v[88:91]
	v_mfma_f32_16x16x32_bf16 v[76:79], v[134:137], v[190:193], v[76:79]
	v_mfma_f32_16x16x32_bf16 v[72:75], v[142:145], v[190:193], v[72:75]
	v_mfma_f32_16x16x32_bf16 v[118:121], v[146:149], v[162:165], v[118:121]
	v_mfma_f32_16x16x32_bf16 v[114:117], v[154:157], v[162:165], v[114:117]
	v_mfma_f32_16x16x32_bf16 v[102:105], v[146:149], v[170:173], v[102:105]
	v_mfma_f32_16x16x32_bf16 v[98:101], v[154:157], v[170:173], v[98:101]
	v_mfma_f32_16x16x32_bf16 v[84:87], v[146:149], v[178:181], v[84:87]
	v_mfma_f32_16x16x32_bf16 v[80:83], v[154:157], v[178:181], v[80:83]
	v_mfma_f32_16x16x32_bf16 v[68:71], v[146:149], v[186:189], v[68:71]
	v_mfma_f32_16x16x32_bf16 v[64:67], v[154:157], v[186:189], v[64:67]
	v_mfma_f32_16x16x32_bf16 v[118:121], v[150:153], v[166:169], v[118:121]
	v_mfma_f32_16x16x32_bf16 v[114:117], v[158:161], v[166:169], v[114:117]
	v_mfma_f32_16x16x32_bf16 v[102:105], v[150:153], v[174:177], v[102:105]
	v_mfma_f32_16x16x32_bf16 v[98:101], v[158:161], v[174:177], v[98:101]
	v_mfma_f32_16x16x32_bf16 v[84:87], v[150:153], v[182:185], v[84:87]
	v_mfma_f32_16x16x32_bf16 v[80:83], v[158:161], v[182:185], v[80:83]
	v_mfma_f32_16x16x32_bf16 v[68:71], v[150:153], v[190:193], v[68:71]
	v_mfma_f32_16x16x32_bf16 v[64:67], v[158:161], v[190:193], v[64:67]
	s_barrier
; #define PG8_STAGE(bufoff, gbase, voff) do { _Pragma("unroll") for (int _i = 0; _i < 2; ++_i) \
;         __builtin_amdgcn_global_load_lds((const __attribute__((address_space(1))) unsigned*)((const __attribute__((address_space(1))) char*)(gbase) + (unsigned)lnd_v((int)(voff)[_i])), (LAS unsigned*)(lds + (bufoff) + ldsw + _i * 8192), 16, 0, 0); } while (0)
; #define PG8_LDA(dst, b, h) do { _Pragma("unroll") for (int m = 0; m < 4; ++m) _Pragma("unroll") for (int k = 0; k < 2; ++k) dst[m][k] = *(const LAS bf16x8*)(lds + PG8_SA(b, h) + aoff + m * 2048 + k * 1024); } while (0)
; #define PG8_MMA(ai, bj, At, Bt) do { __builtin_amdgcn_s_setprio(1); _Pragma("unroll") for (int m = 0; m < 4; ++m) _Pragma("unroll") for (int n = 0; n < 2; ++n) _Pragma("unroll") for (int k = 0; k < 2; ++k) \
;         acc[ai][bj][m][n] = __builtin_amdgcn_mfma_f32_16x16x32_bf16(Bt[n][k], At[m][k], acc[ai][bj][m][n], 0, 0, 0); __builtin_amdgcn_s_setprio(0); } while (0)
; #define PG8_WAIT_V(n) asm volatile("s_waitcnt vmcnt(" #n ")" ::: "memory")
; #define PG8_WAIT_L(n) asm volatile("s_waitcnt lgkmcnt(" #n ")" ::: "memory")
; #define PG8_BAR __builtin_amdgcn_s_barrier()
; #define PG8_SCHED __builtin_amdgcn_sched_barrier(0)
; template <class Desc, class Epi>
; __device__ __forceinline__ void gemm_phase(const int wv_, LAS unsigned char* lds, const Desc& d, const Epi& E) {
;     ...
;             PG8_LDA(At, 1, 1); PG8_STAGE(PG8_SB(1, 0), b3, voffB); PG8_STAGE(PG8_SB(1, 1), b3 + hstepB, voffB); PG8_STAGE(PG8_SA(1, 0), a3, sA0);
;             PG8_WAIT_V(8); PG8_WAIT_L(0); PG8_BAR; PG8_MMA(1, 0, At, B0); PG8_MMA(1, 1, At, B1); PG8_BAR; PG8_SCHED;
;         }
;         if (wr == 0) PG8_BAR;
	v_mov_b32_e32 v96, v208
	ds_read_b128 v[162:165], v221 offset:49152
	ds_read_b128 v[166:169], v221 offset:50176
	ds_read_b128 v[170:173], v221 offset:51200
	ds_read_b128 v[174:177], v221 offset:52224
	ds_read_b128 v[178:181], v221 offset:53248
	ds_read_b128 v[182:185], v221 offset:54272
	ds_read_b128 v[186:189], v221 offset:55296
	ds_read_b128 v[190:193], v221 offset:56320
	s_add_i32 s62, s62, s52
	v_lshl_add_u64 v[194:195], s[20:21], 0, v[96:97]
	v_lshl_add_u64 v[194:195], v[194:195], 0, s[30:31]
	s_mov_b32 m0, s62
	v_mov_b32_e32 v96, v211
	global_load_lds_dwordx4 v[194:195], off
	s_add_i32 m0, s62, 0x2000
	s_nop 0
	v_lshl_add_u64 v[194:195], s[20:21], 0, v[96:97]
	s_add_u32 s20, s20, 0x40080
	v_lshl_add_u64 v[194:195], v[194:195], 0, s[30:31]
	s_addc_u32 s21, s21, 0
	v_mov_b32_e32 v96, v208
	s_add_i32 s62, s63, s52
	global_load_lds_dwordx4 v[194:195], off
	s_mov_b32 m0, s62
	s_nop 0
	global_load_lds_dwordx4 v96, s[20:21]
	v_mov_b32_e32 v96, v211
	s_add_i32 m0, s62, 0x2000
	s_nop 0
	global_load_lds_dwordx4 v96, s[20:21]
	v_mov_b32_e32 v96, v206
	s_mov_b32 m0, s57
	v_lshl_add_u64 v[194:195], s[4:5], 0, v[96:97]
	v_lshl_add_u64 v[194:195], v[194:195], 0, s[30:31]
	v_mov_b32_e32 v96, v209
	global_load_lds_dwordx4 v[194:195], off
	s_mov_b32 m0, s58
	v_lshl_add_u64 v[194:195], s[4:5], 0, v[96:97]
	v_lshl_add_u64 v[194:195], v[194:195], 0, s[30:31]
	global_load_lds_dwordx4 v[194:195], off
	s_waitcnt vmcnt(8)
	s_waitcnt lgkmcnt(0)
	s_barrier
	s_waitcnt lgkmcnt(0)
	v_mfma_f32_16x16x32_bf16 v[60:63], v[130:133], v[162:165], v[60:63]
	v_mfma_f32_16x16x32_bf16 v[56:59], v[138:141], v[162:165], v[56:59]
	v_mfma_f32_16x16x32_bf16 v[44:47], v[130:133], v[170:173], v[44:47]
	v_mfma_f32_16x16x32_bf16 v[40:43], v[138:141], v[170:173], v[40:43]
	v_mfma_f32_16x16x32_bf16 v[24:27], v[130:133], v[178:181], v[24:27]
	v_mfma_f32_16x16x32_bf16 v[16:19], v[138:141], v[178:181], v[16:19]
	v_mfma_f32_16x16x32_bf16 v[4:7], v[130:133], v[186:189], v[4:7]
	v_mfma_f32_16x16x32_bf16 v[0:3], v[138:141], v[186:189], v[0:3]
	v_mfma_f32_16x16x32_bf16 v[60:63], v[134:137], v[166:169], v[60:63]
	v_mfma_f32_16x16x32_bf16 v[56:59], v[142:145], v[166:169], v[56:59]
	v_mfma_f32_16x16x32_bf16 v[44:47], v[134:137], v[174:177], v[44:47]
	v_mfma_f32_16x16x32_bf16 v[40:43], v[142:145], v[174:177], v[40:43]
	v_mfma_f32_16x16x32_bf16 v[24:27], v[134:137], v[182:185], v[24:27]
	v_mfma_f32_16x16x32_bf16 v[16:19], v[142:145], v[182:185], v[16:19]
	v_mfma_f32_16x16x32_bf16 v[4:7], v[134:137], v[190:193], v[4:7]
	v_mfma_f32_16x16x32_bf16 v[0:3], v[142:145], v[190:193], v[0:3]
	v_mfma_f32_16x16x32_bf16 v[52:55], v[146:149], v[162:165], v[52:55]
	v_mfma_f32_16x16x32_bf16 v[48:51], v[154:157], v[162:165], v[48:51]
	v_mfma_f32_16x16x32_bf16 v[28:31], v[146:149], v[170:173], v[28:31]
	v_mfma_f32_16x16x32_bf16 v[20:23], v[154:157], v[170:173], v[20:23]
	v_mfma_f32_16x16x32_bf16 v[36:39], v[146:149], v[178:181], v[36:39]
	v_mfma_f32_16x16x32_bf16 v[32:35], v[154:157], v[178:181], v[32:35]
	v_mfma_f32_16x16x32_bf16 v[12:15], v[146:149], v[186:189], v[12:15]
	v_mfma_f32_16x16x32_bf16 v[8:11], v[154:157], v[186:189], v[8:11]
	v_mfma_f32_16x16x32_bf16 v[52:55], v[150:153], v[166:169], v[52:55]
	v_mfma_f32_16x16x32_bf16 v[48:51], v[158:161], v[166:169], v[48:51]
	v_mfma_f32_16x16x32_bf16 v[28:31], v[150:153], v[174:177], v[28:31]
	v_mfma_f32_16x16x32_bf16 v[20:23], v[158:161], v[174:177], v[20:23]
	v_mfma_f32_16x16x32_bf16 v[36:39], v[150:153], v[182:185], v[36:39]
	v_mfma_f32_16x16x32_bf16 v[32:35], v[158:161], v[182:185], v[32:35]
	v_mfma_f32_16x16x32_bf16 v[12:15], v[150:153], v[190:193], v[12:15]
	v_mfma_f32_16x16x32_bf16 v[8:11], v[158:161], v[190:193], v[8:11]
	s_barrier
	s_add_i32 s61, s61, 2
	s_add_u32 s2, s2, 0x100
	s_addc_u32 s3, s3, 0
	s_add_u32 s29, s29, 0x100
	s_addc_u32 s43, s43, 0
	s_cmp_gt_u32 s61, 13
	s_cbranch_scc0 .LBB0_1262
	s_and_b64 vcc, exec, s[40:41]
	s_cbranch_vccz .LBB0_1265
	s_barrier

; #define PG8_STAGE(bufoff, gbase, voff) do { _Pragma("unroll") for (int _i = 0; _i < 2; ++_i) \
;         __builtin_amdgcn_global_load_lds((const __attribute__((address_space(1))) unsigned*)((const __attribute__((address_space(1))) char*)(gbase) + (unsigned)lnd_v((int)(voff)[_i])), (LAS unsigned*)(lds + (bufoff) + ldsw + _i * 8192), 16, 0, 0); } while (0)
; #define PG8_LDA(dst, b, h) do { _Pragma("unroll") for (int m = 0; m < 4; ++m) _Pragma("unroll") for (int k = 0; k < 2; ++k) dst[m][k] = *(const LAS bf16x8*)(lds + PG8_SA(b, h) + aoff + m * 2048 + k * 1024); } while (0)
; #define PG8_LDB(dst, b, h) do { _Pragma("unroll") for (int n = 0; n < 2; ++n) _Pragma("unroll") for (int k = 0; k < 2; ++k) dst[n][k] = *(const LAS bf16x8*)(lds + PG8_SB(b, h) + boff + n * 2048 + k * 1024); } while (0)
; #define PG8_WAIT_V(n) asm volatile("s_waitcnt vmcnt(" #n ")" ::: "memory")
; #define PG8_WAIT_L(n) asm volatile("s_waitcnt lgkmcnt(" #n ")" ::: "memory")
; #define PG8_BAR __builtin_amdgcn_s_barrier()
; #define PG8_SCHED __builtin_amdgcn_sched_barrier(0)
; template <class Desc, class Epi>
; __device__ __forceinline__ void gemm_phase(const int wv_, LAS unsigned char* lds, const Desc& d, const Epi& E) {
;     ...
;         for (int t = 0; t < nt; t += 2) {
;             const bool last = (t == nt - 2);
;             unsigned sA0[2], sA1[2];
;             if constexpr (Desc::GATHER) { sA0[0] = last ? voffAn[0] : voffA[0]; sA0[1] = last ? voffAn[1] : voffA[1]; sA1[0] = last ? voffAn1[0] : voffA1[0]; sA1[1] = last ? voffAn1[1] : voffA1[1]; }
;             else { sA0[0] = voffA[0]; sA0[1] = voffA[1]; sA1[0] = voffA1[0]; sA1[1] = voffA1[1]; }
;             const char* a1 = cA + (size_t)(t + 1) * kstep;
;             const char* a2 = last ? nA : cA + (size_t)(t + 2) * kstep; const char* b2 = last ? nB : cB + (size_t)(t + 2) * kstep;
;             const char* a3 = a2 + kstep; const char* b3 = b2 + kstep;
;             PG8_LDB(B0, 0, 0); PG8_LDB(B1, 0, 1); PG8_SCHED; PG8_LDA(At, 0, 0); PG8_STAGE(PG8_SA(1, 1), a1, voffA1);
;             PG8_WAIT_V(8); PG8_WAIT_L(0); PG8_BAR; PG8_MMA(0, 0, At, B0); PG8_MMA(0, 1, At, B1); PG8_BAR; PG8_SCHED;
;             PG8_LDA(At, 0, 1); PG8_STAGE(PG8_SB(0, 0), b2, voffB); PG8_STAGE(PG8_SB(0, 1), b2 + hstepB, voffB); PG8_STAGE(PG8_SA(0, 0), a2, sA0);
.LBB0_1481:
	s_add_u32 s52, s50, s22
	s_addc_u32 s53, s51, 0
	s_add_u32 s23, s52, 0x100
	s_addc_u32 s24, s53, 0
	s_and_b64 s[4:5], s[20:21], exec
	s_cselect_b32 s4, s42, s23
	s_cselect_b32 s5, s43, s24
	s_add_u32 s22, s48, s22
	s_addc_u32 s23, s49, 0
	s_add_u32 s22, s22, 0x100
	s_addc_u32 s23, s23, 0
	s_add_i32 s77, 0, 0x10000
	s_and_b64 s[20:21], s[20:21], exec
	s_cselect_b32 s21, s45, s23
	s_cselect_b32 s20, s44, s22
	s_add_i32 s23, 0, 0x14000
	v_add_u32_e32 v96, s77, v139
	s_add_i32 s79, s77, s59
	ds_read_b128 v[150:153], v96
	ds_read_b128 v[154:157], v96 offset:1024
	ds_read_b128 v[158:161], v96 offset:2048
	ds_read_b128 v[162:165], v96 offset:3072
	v_add_u32_e32 v96, s23, v139
	s_add_i32 m0, s60, 0xc000
	s_add_i32 s80, s60, 0xe000
	s_add_i32 s75, s79, 0x2000
	ds_read_b128 v[166:169], v96
	ds_read_b128 v[170:173], v96 offset:1024
	ds_read_b128 v[174:177], v96 offset:2048
	ds_read_b128 v[178:181], v96 offset:3072
	s_add_u32 s24, s20, 0x40000
	s_addc_u32 s25, s21, 0
	s_add_i32 s73, 0, 0x18000
	s_add_i32 s76, s23, s59
	s_add_i32 s71, s73, s59
	s_add_i32 s74, s76, 0x2000
	s_add_i32 s72, 0, 0x1c000
	s_add_i32 s29, s71, 0x2000
	s_add_u32 s22, s20, 0x40080
	s_addc_u32 s23, s21, 0
	s_add_i32 s78, s72, s59
	s_add_i32 s77, s78, 0x2000
	v_mov_b32_e32 v96, v133
	ds_read_b128 v[182:185], v149
	ds_read_b128 v[186:189], v149 offset:1024
	ds_read_b128 v[190:193], v149 offset:2048
	ds_read_b128 v[194:197], v149 offset:3072
	ds_read_b128 v[198:201], v149 offset:4096
	ds_read_b128 v[202:205], v149 offset:5120
	ds_read_b128 v[206:209], v149 offset:6144
	ds_read_b128 v[210:213], v149 offset:7168
	s_nop 0
	v_lshl_add_u64 v[130:131], s[52:53], 0, v[96:97]
	v_lshl_add_u64 v[130:131], v[130:131], 0, s[30:31]
	v_mov_b32_e32 v96, v136
	global_load_lds_dwordx4 v[130:131], off
	s_mov_b32 m0, s80
	v_lshl_add_u64 v[130:131], s[52:53], 0, v[96:97]
	v_lshl_add_u64 v[130:131], v[130:131], 0, s[30:31]
	global_load_lds_dwordx4 v[130:131], off
	s_waitcnt vmcnt(8)
	s_waitcnt lgkmcnt(0)
	s_barrier
	s_waitcnt lgkmcnt(0)
	v_mfma_f32_16x16x32_bf16 v[126:129], v[150:153], v[182:185], v[126:129]
	v_mfma_f32_16x16x32_bf16 v[122:125], v[158:161], v[182:185], v[122:125]
	v_mfma_f32_16x16x32_bf16 v[110:113], v[150:153], v[190:193], v[110:113]
	v_mfma_f32_16x16x32_bf16 v[106:109], v[158:161], v[190:193], v[106:109]
	v_mfma_f32_16x16x32_bf16 v[92:95], v[150:153], v[198:201], v[92:95]
	v_mfma_f32_16x16x32_bf16 v[88:91], v[158:161], v[198:201], v[88:91]
	v_mfma_f32_16x16x32_bf16 v[76:79], v[150:153], v[206:209], v[76:79]
	v_mfma_f32_16x16x32_bf16 v[72:75], v[158:161], v[206:209], v[72:75]
	v_mfma_f32_16x16x32_bf16 v[126:129], v[154:157], v[186:189], v[126:129]
	v_mfma_f32_16x16x32_bf16 v[122:125], v[162:165], v[186:189], v[122:125]
	v_mfma_f32_16x16x32_bf16 v[110:113], v[154:157], v[194:197], v[110:113]
	v_mfma_f32_16x16x32_bf16 v[106:109], v[162:165], v[194:197], v[106:109]
	v_mfma_f32_16x16x32_bf16 v[92:95], v[154:157], v[202:205], v[92:95]
	v_mfma_f32_16x16x32_bf16 v[88:91], v[162:165], v[202:205], v[88:91]
	v_mfma_f32_16x16x32_bf16 v[76:79], v[154:157], v[210:213], v[76:79]
	v_mfma_f32_16x16x32_bf16 v[72:75], v[162:165], v[210:213], v[72:75]
	v_mfma_f32_16x16x32_bf16 v[118:121], v[166:169], v[182:185], v[118:121]
	v_mfma_f32_16x16x32_bf16 v[114:117], v[174:177], v[182:185], v[114:117]
	v_mfma_f32_16x16x32_bf16 v[102:105], v[166:169], v[190:193], v[102:105]
	v_mfma_f32_16x16x32_bf16 v[98:101], v[174:177], v[190:193], v[98:101]
	v_mfma_f32_16x16x32_bf16 v[84:87], v[166:169], v[198:201], v[84:87]
	v_mfma_f32_16x16x32_bf16 v[80:83], v[174:177], v[198:201], v[80:83]
	v_mfma_f32_16x16x32_bf16 v[68:71], v[166:169], v[206:209], v[68:71]
	v_mfma_f32_16x16x32_bf16 v[64:67], v[174:177], v[206:209], v[64:67]
	v_mfma_f32_16x16x32_bf16 v[118:121], v[170:173], v[186:189], v[118:121]
	v_mfma_f32_16x16x32_bf16 v[114:117], v[178:181], v[186:189], v[114:117]
	v_mfma_f32_16x16x32_bf16 v[102:105], v[170:173], v[194:197], v[102:105]
	v_mfma_f32_16x16x32_bf16 v[98:101], v[178:181], v[194:197], v[98:101]
	v_mfma_f32_16x16x32_bf16 v[84:87], v[170:173], v[202:205], v[84:87]
	v_mfma_f32_16x16x32_bf16 v[80:83], v[178:181], v[202:205], v[80:83]
	v_mfma_f32_16x16x32_bf16 v[68:71], v[170:173], v[210:213], v[68:71]
	v_mfma_f32_16x16x32_bf16 v[64:67], v[178:181], v[210:213], v[64:67]
	s_barrier
	v_mov_b32_e32 v96, v134
	s_mov_b32 m0, s79
	ds_read_b128 v[182:185], v149 offset:16384
	ds_read_b128 v[186:189], v149 offset:17408
	ds_read_b128 v[190:193], v149 offset:18432
	ds_read_b128 v[194:197], v149 offset:19456
	ds_read_b128 v[198:201], v149 offset:20480
	ds_read_b128 v[202:205], v149 offset:21504
	ds_read_b128 v[206:209], v149 offset:22528
	ds_read_b128 v[210:213], v149 offset:23552
	s_nop 0
	global_load_lds_dwordx4 v96, s[20:21]
	v_mov_b32_e32 v96, v137
	s_mov_b32 m0, s75
	s_nop 0
	global_load_lds_dwordx4 v96, s[20:21]
	v_mov_b32_e32 v96, v134
	s_mov_b32 m0, s76
	s_nop 0
	global_load_lds_dwordx4 v96, s[24:25]
	v_mov_b32_e32 v96, v137
	s_mov_b32 m0, s74
	s_nop 0
	global_load_lds_dwordx4 v96, s[24:25]
	v_mov_b32_e32 v96, v132
	s_mov_b32 m0, s60
	s_nop 0
	global_load_lds_dwordx4 v96, s[4:5]
	v_mov_b32_e32 v96, v135
	s_mov_b32 m0, s61
	s_nop 0
	global_load_lds_dwordx4 v96, s[4:5]
	s_waitcnt vmcnt(8)
	s_waitcnt lgkmcnt(0)
	s_barrier
; #define PG8_STAGE(bufoff, gbase, voff) do { _Pragma("unroll") for (int _i = 0; _i < 2; ++_i) \
;         __builtin_amdgcn_global_load_lds((const __attribute__((address_space(1))) unsigned*)((const __attribute__((address_space(1))) char*)(gbase) + (unsigned)lnd_v((int)(voff)[_i])), (LAS unsigned*)(lds + (bufoff) + ldsw + _i * 8192), 16, 0, 0); } while (0)
; #define PG8_LDA(dst, b, h) do { _Pragma("unroll") for (int m = 0; m < 4; ++m) _Pragma("unroll") for (int k = 0; k < 2; ++k) dst[m][k] = *(const LAS bf16x8*)(lds + PG8_SA(b, h) + aoff + m * 2048 + k * 1024); } while (0)
; #define PG8_LDB(dst, b, h) do { _Pragma("unroll") for (int n = 0; n < 2; ++n) _Pragma("unroll") for (int k = 0; k < 2; ++k) dst[n][k] = *(const LAS bf16x8*)(lds + PG8_SB(b, h) + boff + n * 2048 + k * 1024); } while (0)
; #define PG8_MMA(ai, bj, At, Bt) do { __builtin_amdgcn_s_setprio(1); _Pragma("unroll") for (int m = 0; m < 4; ++m) _Pragma("unroll") for (int n = 0; n < 2; ++n) _Pragma("unroll") for (int k = 0; k < 2; ++k) \
;         acc[ai][bj][m][n] = __builtin_amdgcn_mfma_f32_16x16x32_bf16(Bt[n][k], At[m][k], acc[ai][bj][m][n], 0, 0, 0); __builtin_amdgcn_s_setprio(0); } while (0)
; #define PG8_WAIT_V(n) asm volatile("s_waitcnt vmcnt(" #n ")" ::: "memory")
; #define PG8_WAIT_L(n) asm volatile("s_waitcnt lgkmcnt(" #n ")" ::: "memory")
; #define PG8_BAR __builtin_amdgcn_s_barrier()
; #define PG8_SCHED __builtin_amdgcn_sched_barrier(0)
; template <class Desc, class Epi>
; __device__ __forceinline__ void gemm_phase(const int wv_, LAS unsigned char* lds, const Desc& d, const Epi& E) {
;     ...
;             PG8_WAIT_V(8); PG8_WAIT_L(0); PG8_BAR; PG8_MMA(1, 0, At, B0); PG8_MMA(1, 1, At, B1); PG8_BAR; PG8_SCHED;
;             PG8_LDB(B0, 1, 0); PG8_LDB(B1, 1, 1); PG8_SCHED; PG8_LDA(At, 1, 0); PG8_STAGE(PG8_SA(0, 1), a2, sA1);
;             PG8_WAIT_V(8); PG8_WAIT_L(0); PG8_BAR; PG8_MMA(0, 0, At, B0); PG8_MMA(0, 1, At, B1); PG8_BAR; PG8_SCHED;
	s_waitcnt lgkmcnt(0)
	v_mfma_f32_16x16x32_bf16 v[60:63], v[150:153], v[182:185], v[60:63]
	v_mfma_f32_16x16x32_bf16 v[56:59], v[158:161], v[182:185], v[56:59]
	v_mfma_f32_16x16x32_bf16 v[44:47], v[150:153], v[190:193], v[44:47]
	v_mfma_f32_16x16x32_bf16 v[32:35], v[158:161], v[190:193], v[32:35]
	v_mfma_f32_16x16x32_bf16 v[16:19], v[150:153], v[198:201], v[16:19]
	v_mfma_f32_16x16x32_bf16 v[8:11], v[158:161], v[198:201], v[8:11]
	v_mfma_f32_16x16x32_bf16 v[4:7], v[150:153], v[206:209], v[4:7]
	v_mfma_f32_16x16x32_bf16 v[0:3], v[158:161], v[206:209], v[0:3]
	v_mfma_f32_16x16x32_bf16 v[60:63], v[154:157], v[186:189], v[60:63]
	v_mfma_f32_16x16x32_bf16 v[56:59], v[162:165], v[186:189], v[56:59]
	v_mfma_f32_16x16x32_bf16 v[44:47], v[154:157], v[194:197], v[44:47]
	v_mfma_f32_16x16x32_bf16 v[32:35], v[162:165], v[194:197], v[32:35]
	v_mfma_f32_16x16x32_bf16 v[16:19], v[154:157], v[202:205], v[16:19]
	v_mfma_f32_16x16x32_bf16 v[8:11], v[162:165], v[202:205], v[8:11]
	v_mfma_f32_16x16x32_bf16 v[4:7], v[154:157], v[210:213], v[4:7]
	v_mfma_f32_16x16x32_bf16 v[0:3], v[162:165], v[210:213], v[0:3]
	v_mfma_f32_16x16x32_bf16 v[52:55], v[166:169], v[182:185], v[52:55]
	v_mfma_f32_16x16x32_bf16 v[48:51], v[174:177], v[182:185], v[48:51]
	v_mfma_f32_16x16x32_bf16 v[28:31], v[166:169], v[190:193], v[28:31]
	v_mfma_f32_16x16x32_bf16 v[12:15], v[174:177], v[190:193], v[12:15]
	v_mfma_f32_16x16x32_bf16 v[36:39], v[166:169], v[198:201], v[36:39]
	v_mfma_f32_16x16x32_bf16 v[40:43], v[174:177], v[198:201], v[40:43]
	v_mfma_f32_16x16x32_bf16 v[20:23], v[166:169], v[206:209], v[20:23]
	v_mfma_f32_16x16x32_bf16 v[24:27], v[174:177], v[206:209], v[24:27]
	v_mfma_f32_16x16x32_bf16 v[52:55], v[170:173], v[186:189], v[52:55]
	v_mfma_f32_16x16x32_bf16 v[48:51], v[178:181], v[186:189], v[48:51]
	v_mfma_f32_16x16x32_bf16 v[28:31], v[170:173], v[194:197], v[28:31]
	v_mfma_f32_16x16x32_bf16 v[12:15], v[178:181], v[194:197], v[12:15]
	v_mfma_f32_16x16x32_bf16 v[36:39], v[170:173], v[202:205], v[36:39]
	v_mfma_f32_16x16x32_bf16 v[40:43], v[178:181], v[202:205], v[40:43]
	v_mfma_f32_16x16x32_bf16 v[20:23], v[170:173], v[210:213], v[20:23]
	v_mfma_f32_16x16x32_bf16 v[24:27], v[178:181], v[210:213], v[24:27]
	s_barrier
	v_add_u32_e32 v96, s73, v139
	ds_read_b128 v[150:153], v96
	ds_read_b128 v[154:157], v96 offset:1024
	ds_read_b128 v[158:161], v96 offset:2048
	ds_read_b128 v[162:165], v96 offset:3072
	v_add_u32_e32 v96, s72, v139
	ds_read_b128 v[166:169], v96
	ds_read_b128 v[170:173], v96 offset:1024
	ds_read_b128 v[174:177], v96 offset:2048
	ds_read_b128 v[178:181], v96 offset:3072
	v_mov_b32_e32 v96, v133
	s_mov_b32 m0, s62
	ds_read_b128 v[182:185], v149 offset:32768
	ds_read_b128 v[186:189], v149 offset:33792
	ds_read_b128 v[190:193], v149 offset:34816
	ds_read_b128 v[194:197], v149 offset:35840
	ds_read_b128 v[198:201], v149 offset:36864
	ds_read_b128 v[202:205], v149 offset:37888
	ds_read_b128 v[206:209], v149 offset:38912
	ds_read_b128 v[210:213], v149 offset:39936
	s_nop 0
	global_load_lds_dwordx4 v96, s[4:5]
	v_mov_b32_e32 v96, v136
	s_mov_b32 m0, s63
	s_nop 0
	global_load_lds_dwordx4 v96, s[4:5]
	s_waitcnt vmcnt(8)
	s_waitcnt lgkmcnt(0)
	s_barrier
	s_waitcnt lgkmcnt(0)
	v_mfma_f32_16x16x32_bf16 v[126:129], v[150:153], v[182:185], v[126:129]
	v_mfma_f32_16x16x32_bf16 v[122:125], v[158:161], v[182:185], v[122:125]
	v_mfma_f32_16x16x32_bf16 v[110:113], v[150:153], v[190:193], v[110:113]
	v_mfma_f32_16x16x32_bf16 v[106:109], v[158:161], v[190:193], v[106:109]
	v_mfma_f32_16x16x32_bf16 v[92:95], v[150:153], v[198:201], v[92:95]
	v_mfma_f32_16x16x32_bf16 v[88:91], v[158:161], v[198:201], v[88:91]
	v_mfma_f32_16x16x32_bf16 v[76:79], v[150:153], v[206:209], v[76:79]
	v_mfma_f32_16x16x32_bf16 v[72:75], v[158:161], v[206:209], v[72:75]
	v_mfma_f32_16x16x32_bf16 v[126:129], v[154:157], v[186:189], v[126:129]
	v_mfma_f32_16x16x32_bf16 v[122:125], v[162:165], v[186:189], v[122:125]
	v_mfma_f32_16x16x32_bf16 v[110:113], v[154:157], v[194:197], v[110:113]
	v_mfma_f32_16x16x32_bf16 v[106:109], v[162:165], v[194:197], v[106:109]
	v_mfma_f32_16x16x32_bf16 v[92:95], v[154:157], v[202:205], v[92:95]
	v_mfma_f32_16x16x32_bf16 v[88:91], v[162:165], v[202:205], v[88:91]
	v_mfma_f32_16x16x32_bf16 v[76:79], v[154:157], v[210:213], v[76:79]
	v_mfma_f32_16x16x32_bf16 v[72:75], v[162:165], v[210:213], v[72:75]
	v_mfma_f32_16x16x32_bf16 v[118:121], v[166:169], v[182:185], v[118:121]
	v_mfma_f32_16x16x32_bf16 v[114:117], v[174:177], v[182:185], v[114:117]
	v_mfma_f32_16x16x32_bf16 v[102:105], v[166:169], v[190:193], v[102:105]
	v_mfma_f32_16x16x32_bf16 v[98:101], v[174:177], v[190:193], v[98:101]
	v_mfma_f32_16x16x32_bf16 v[84:87], v[166:169], v[198:201], v[84:87]
	v_mfma_f32_16x16x32_bf16 v[80:83], v[174:177], v[198:201], v[80:83]
	v_mfma_f32_16x16x32_bf16 v[68:71], v[166:169], v[206:209], v[68:71]
	v_mfma_f32_16x16x32_bf16 v[64:67], v[174:177], v[206:209], v[64:67]
	v_mfma_f32_16x16x32_bf16 v[118:121], v[170:173], v[186:189], v[118:121]
	v_mfma_f32_16x16x32_bf16 v[114:117], v[178:181], v[186:189], v[114:117]
	v_mfma_f32_16x16x32_bf16 v[102:105], v[170:173], v[194:197], v[102:105]
	v_mfma_f32_16x16x32_bf16 v[98:101], v[178:181], v[194:197], v[98:101]
	v_mfma_f32_16x16x32_bf16 v[84:87], v[170:173], v[202:205], v[84:87]
	v_mfma_f32_16x16x32_bf16 v[80:83], v[178:181], v[202:205], v[80:83]
	v_mfma_f32_16x16x32_bf16 v[68:71], v[170:173], v[210:213], v[68:71]
	v_mfma_f32_16x16x32_bf16 v[64:67], v[178:181], v[210:213], v[64:67]
	s_barrier
; #define PG8_STAGE(bufoff, gbase, voff) do { _Pragma("unroll") for (int _i = 0; _i < 2; ++_i) \
;         __builtin_amdgcn_global_load_lds((const __attribute__((address_space(1))) unsigned*)((const __attribute__((address_space(1))) char*)(gbase) + (unsigned)lnd_v((int)(voff)[_i])), (LAS unsigned*)(lds + (bufoff) + ldsw + _i * 8192), 16, 0, 0); } while (0)
; #define PG8_LDA(dst, b, h) do { _Pragma("unroll") for (int m = 0; m < 4; ++m) _Pragma("unroll") for (int k = 0; k < 2; ++k) dst[m][k] = *(const LAS bf16x8*)(lds + PG8_SA(b, h) + aoff + m * 2048 + k * 1024); } while (0)
; #define PG8_MMA(ai, bj, At, Bt) do { __builtin_amdgcn_s_setprio(1); _Pragma("unroll") for (int m = 0; m < 4; ++m) _Pragma("unroll") for (int n = 0; n < 2; ++n) _Pragma("unroll") for (int k = 0; k < 2; ++k) \
;         acc[ai][bj][m][n] = __builtin_amdgcn_mfma_f32_16x16x32_bf16(Bt[n][k], At[m][k], acc[ai][bj][m][n], 0, 0, 0); __builtin_amdgcn_s_setprio(0); } while (0)
; #define PG8_WAIT_V(n) asm volatile("s_waitcnt vmcnt(" #n ")" ::: "memory")
; #define PG8_WAIT_L(n) asm volatile("s_waitcnt lgkmcnt(" #n ")" ::: "memory")
; #define PG8_BAR __builtin_amdgcn_s_barrier()
; #define PG8_SCHED __builtin_amdgcn_sched_barrier(0)
; template <class Desc, class Epi>
; __device__ __forceinline__ void gemm_phase(const int wv_, LAS unsigned char* lds, const Desc& d, const Epi& E) {
;     ...
;             PG8_LDA(At, 1, 1); PG8_STAGE(PG8_SB(1, 0), b3, voffB); PG8_STAGE(PG8_SB(1, 1), b3 + hstepB, voffB); PG8_STAGE(PG8_SA(1, 0), a3, sA0);
;             PG8_WAIT_V(8); PG8_WAIT_L(0); PG8_BAR; PG8_MMA(1, 0, At, B0); PG8_MMA(1, 1, At, B1); PG8_BAR; PG8_SCHED;
;         }
;         if (wr == 0) PG8_BAR;
	v_mov_b32_e32 v96, v134
	ds_read_b128 v[182:185], v149 offset:49152
	ds_read_b128 v[186:189], v149 offset:50176
	ds_read_b128 v[190:193], v149 offset:51200
	ds_read_b128 v[194:197], v149 offset:52224
	ds_read_b128 v[198:201], v149 offset:53248
	ds_read_b128 v[202:205], v149 offset:54272
	ds_read_b128 v[206:209], v149 offset:55296
	ds_read_b128 v[210:213], v149 offset:56320
	s_mov_b32 m0, s71
	v_lshl_add_u64 v[130:131], s[20:21], 0, v[96:97]
	v_lshl_add_u64 v[130:131], v[130:131], 0, s[30:31]
	v_mov_b32_e32 v96, v137
	global_load_lds_dwordx4 v[130:131], off
	s_mov_b32 m0, s29
	v_lshl_add_u64 v[130:131], s[20:21], 0, v[96:97]
	v_lshl_add_u64 v[130:131], v[130:131], 0, s[30:31]
	v_mov_b32_e32 v96, v134
	global_load_lds_dwordx4 v[130:131], off
	s_mov_b32 m0, s78
	s_nop 0
	global_load_lds_dwordx4 v96, s[22:23]
	v_mov_b32_e32 v96, v137
	s_mov_b32 m0, s77
	s_nop 0
	global_load_lds_dwordx4 v96, s[22:23]
	v_mov_b32_e32 v96, v132
	s_mov_b32 m0, s65
	v_lshl_add_u64 v[130:131], s[4:5], 0, v[96:97]
	v_lshl_add_u64 v[130:131], v[130:131], 0, s[30:31]
	v_mov_b32_e32 v96, v135
	global_load_lds_dwordx4 v[130:131], off
	s_mov_b32 m0, s66
	v_lshl_add_u64 v[130:131], s[4:5], 0, v[96:97]
	v_lshl_add_u64 v[130:131], v[130:131], 0, s[30:31]
	global_load_lds_dwordx4 v[130:131], off
	s_waitcnt vmcnt(8)
	s_waitcnt lgkmcnt(0)
	s_barrier
	s_waitcnt lgkmcnt(0)
	v_mfma_f32_16x16x32_bf16 v[60:63], v[150:153], v[182:185], v[60:63]
	v_mfma_f32_16x16x32_bf16 v[56:59], v[158:161], v[182:185], v[56:59]
	v_mfma_f32_16x16x32_bf16 v[44:47], v[150:153], v[190:193], v[44:47]
	v_mfma_f32_16x16x32_bf16 v[32:35], v[158:161], v[190:193], v[32:35]
	v_mfma_f32_16x16x32_bf16 v[16:19], v[150:153], v[198:201], v[16:19]
	v_mfma_f32_16x16x32_bf16 v[8:11], v[158:161], v[198:201], v[8:11]
	v_mfma_f32_16x16x32_bf16 v[4:7], v[150:153], v[206:209], v[4:7]
	v_mfma_f32_16x16x32_bf16 v[0:3], v[158:161], v[206:209], v[0:3]
	v_mfma_f32_16x16x32_bf16 v[60:63], v[154:157], v[186:189], v[60:63]
	v_mfma_f32_16x16x32_bf16 v[56:59], v[162:165], v[186:189], v[56:59]
	v_mfma_f32_16x16x32_bf16 v[44:47], v[154:157], v[194:197], v[44:47]
	v_mfma_f32_16x16x32_bf16 v[32:35], v[162:165], v[194:197], v[32:35]
	v_mfma_f32_16x16x32_bf16 v[16:19], v[154:157], v[202:205], v[16:19]
	v_mfma_f32_16x16x32_bf16 v[8:11], v[162:165], v[202:205], v[8:11]
	v_mfma_f32_16x16x32_bf16 v[4:7], v[154:157], v[210:213], v[4:7]
	v_mfma_f32_16x16x32_bf16 v[0:3], v[162:165], v[210:213], v[0:3]
	v_mfma_f32_16x16x32_bf16 v[52:55], v[166:169], v[182:185], v[52:55]
	v_mfma_f32_16x16x32_bf16 v[48:51], v[174:177], v[182:185], v[48:51]
	v_mfma_f32_16x16x32_bf16 v[28:31], v[166:169], v[190:193], v[28:31]
	v_mfma_f32_16x16x32_bf16 v[12:15], v[174:177], v[190:193], v[12:15]
	v_mfma_f32_16x16x32_bf16 v[36:39], v[166:169], v[198:201], v[36:39]
	v_mfma_f32_16x16x32_bf16 v[40:43], v[174:177], v[198:201], v[40:43]
	v_mfma_f32_16x16x32_bf16 v[20:23], v[166:169], v[206:209], v[20:23]
	v_mfma_f32_16x16x32_bf16 v[24:27], v[174:177], v[206:209], v[24:27]
	v_mfma_f32_16x16x32_bf16 v[52:55], v[170:173], v[186:189], v[52:55]
	v_mfma_f32_16x16x32_bf16 v[48:51], v[178:181], v[186:189], v[48:51]
	v_mfma_f32_16x16x32_bf16 v[28:31], v[170:173], v[194:197], v[28:31]
	v_mfma_f32_16x16x32_bf16 v[12:15], v[178:181], v[194:197], v[12:15]
	v_mfma_f32_16x16x32_bf16 v[36:39], v[170:173], v[202:205], v[36:39]
	v_mfma_f32_16x16x32_bf16 v[40:43], v[178:181], v[202:205], v[40:43]
	v_mfma_f32_16x16x32_bf16 v[20:23], v[170:173], v[210:213], v[20:23]
	v_mfma_f32_16x16x32_bf16 v[24:27], v[178:181], v[210:213], v[24:27]
	s_barrier
	s_movk_i32 s22, 0x100
	s_andn2_b64 vcc, exec, s[2:3]
	s_mov_b64 s[20:21], -1
	s_mov_b64 s[2:3], 0
	s_cbranch_vccz .LBB0_1481
	s_and_b64 vcc, exec, s[40:41]
	s_cbranch_vccz .LBB0_1484
	s_barrier

; #define PG8_AOFF(ord, U, O0, O1) do { _Pragma("unroll") for (int _i = 0; _i < 2; ++_i) { \
;         O0[_i] = d.rowbyte(U, (int)tix[(ord) * 256 + Rr[_i]]) + (unsigned)(Cc[_i] * 2); O1[_i] = d.rowbyte(U, (int)tix[(ord) * 256 + HALF + Rr[_i]]) + (unsigned)(Cc[_i] * 2); } } while (0)
; #define PG8_STAGE(bufoff, gbase, voff) do { _Pragma("unroll") for (int _i = 0; _i < 2; ++_i) \
;         __builtin_amdgcn_global_load_lds((const __attribute__((address_space(1))) unsigned*)((const __attribute__((address_space(1))) char*)(gbase) + (unsigned)lnd_v((int)(voff)[_i])), (LAS unsigned*)(lds + (bufoff) + ldsw + _i * 8192), 16, 0, 0); } while (0)
; #define PG8_WAIT_V(n) asm volatile("s_waitcnt vmcnt(" #n ")" ::: "memory")
; #define PG8_WAIT_L(n) asm volatile("s_waitcnt lgkmcnt(" #n ")" ::: "memory")
; #define PG8_BAR __builtin_amdgcn_s_barrier()
; template <class Desc, class Epi>
; __device__ __forceinline__ void gemm_phase(const int wv_, LAS unsigned char* lds, const Desc& d, const Epi& E) {
;     ...
;         if constexpr (Desc::GATHER) { if (has_next) PG8_AOFF(ui + 1, nxt, voffAn, voffAn1); else { voffAn[0] = voffA[0]; voffAn[1] = voffA[1]; voffAn1[0] = voffA1[0]; voffAn1[1] = voffA1[1]; } }
;         const char* nA = has_next ? (const char*)nxt.a : cA; const char* nB = has_next ? (const char*)nxt.b : cB;
;         for (int t = 0; t < nt; t += 2) {
;             const bool last = (t == nt - 2);
;             unsigned sA0[2], sA1[2];
;             if constexpr (Desc::GATHER) { sA0[0] = last ? voffAn[0] : voffA[0]; sA0[1] = last ? voffAn[1] : voffA[1]; sA1[0] = last ? voffAn1[0] : voffA1[0]; sA1[1] = last ? voffAn1[1] : voffA1[1]; }
;             else { sA0[0] = voffA[0]; sA0[1] = voffA[1]; sA1[0] = voffA1[0]; sA1[1] = voffA1[1]; }
;             const char* a1 = cA + (size_t)(t + 1) * kstep;
;             const char* a2 = last ? nA : cA + (size_t)(t + 2) * kstep; const char* b2 = last ? nB : cB + (size_t)(t + 2) * kstep;
;             const char* a3 = a2 + kstep; const char* b3 = b2 + kstep;
;             PG8_LDB(B0, 0, 0); PG8_LDB(B1, 0, 1); PG8_SCHED; PG8_LDA(At, 0, 0); PG8_STAGE(PG8_SA(1, 1), a1, voffA1);
;             PG8_WAIT_V(8); PG8_WAIT_L(0); PG8_BAR; PG8_MMA(0, 0, At, B0); PG8_MMA(0, 1, At, B1); PG8_BAR; PG8_SCHED;
;             PG8_LDA(At, 0, 1); PG8_STAGE(PG8_SB(0, 0), b2, voffB); PG8_STAGE(PG8_SB(0, 1), b2 + hstepB, voffB); PG8_STAGE(PG8_SA(0, 0), a2, sA0);
.LBB0_1565:
	s_add_u32 s4, s2, 0x100
	s_addc_u32 s5, s3, 0
	s_add_u32 s22, s29, s2
	s_addc_u32 s23, s59, s3
	s_cmp_eq_u32 s75, 12
	s_cselect_b64 vcc, -1, 0
	s_and_b64 s[20:21], vcc, exec
	s_cselect_b32 s20, 0, s4
	s_cselect_b32 s21, 0, s5
	s_cselect_b32 s22, s54, s22
	s_cselect_b32 s23, s55, s23
	s_add_u32 s20, s42, s20
	s_addc_u32 s21, s43, s21
	s_add_i32 s76, 0, 0x10000
	v_add_u32_e32 v135, s76, v143
	s_add_i32 s77, 0, 0x14000
	ds_read_b128 v[160:163], v135
	ds_read_b128 v[164:167], v135 offset:1024
	ds_read_b128 v[168:171], v135 offset:2048
	ds_read_b128 v[172:175], v135 offset:3072
	v_add_u32_e32 v135, s77, v143
	ds_read_b128 v[176:179], v135
	ds_read_b128 v[180:183], v135 offset:1024
	ds_read_b128 v[184:187], v135 offset:2048
	ds_read_b128 v[188:191], v135 offset:3072
	v_cndmask_b32_e32 v134, v157, v153, vcc
	v_cndmask_b32_e32 v132, v159, v154, vcc
	v_cndmask_b32_e32 v96, v131, v155, vcc
	v_cndmask_b32_e32 v133, v158, v156, vcc
	s_add_i32 m0, s64, 0xc000
	v_mov_b32_e32 v135, v131
	s_add_u32 s2, s40, s2
	ds_read_b128 v[192:195], v152
	ds_read_b128 v[196:199], v152 offset:1024
	ds_read_b128 v[200:203], v152 offset:2048
	ds_read_b128 v[204:207], v152 offset:3072
	ds_read_b128 v[208:211], v152 offset:4096
	ds_read_b128 v[212:215], v152 offset:5120
	ds_read_b128 v[220:223], v152 offset:6144
	ds_read_b128 v[224:227], v152 offset:7168
	s_addc_u32 s3, s41, s3
	global_load_lds_dwordx4 v135, s[2:3]
	v_mov_b32_e32 v135, v158
	s_add_i32 m0, s64, 0xe000
	s_nop 0
	global_load_lds_dwordx4 v135, s[2:3]
	s_waitcnt vmcnt(8)
	s_waitcnt lgkmcnt(0)
	s_barrier
	s_waitcnt lgkmcnt(0)
	v_mfma_f32_16x16x32_bf16 v[122:125], v[160:163], v[192:195], v[122:125]
	v_mfma_f32_16x16x32_bf16 v[114:117], v[168:171], v[192:195], v[114:117]
	v_mfma_f32_16x16x32_bf16 v[106:109], v[160:163], v[200:203], v[106:109]
	v_mfma_f32_16x16x32_bf16 v[98:101], v[168:171], v[200:203], v[98:101]
	v_mfma_f32_16x16x32_bf16 v[88:91], v[160:163], v[208:211], v[88:91]
	v_mfma_f32_16x16x32_bf16 v[80:83], v[168:171], v[208:211], v[80:83]
	v_mfma_f32_16x16x32_bf16 v[72:75], v[160:163], v[220:223], v[72:75]
	v_mfma_f32_16x16x32_bf16 v[64:67], v[168:171], v[220:223], v[64:67]
	v_mfma_f32_16x16x32_bf16 v[122:125], v[164:167], v[196:199], v[122:125]
	v_mfma_f32_16x16x32_bf16 v[114:117], v[172:175], v[196:199], v[114:117]
	v_mfma_f32_16x16x32_bf16 v[106:109], v[164:167], v[204:207], v[106:109]
	v_mfma_f32_16x16x32_bf16 v[98:101], v[172:175], v[204:207], v[98:101]
	v_mfma_f32_16x16x32_bf16 v[88:91], v[164:167], v[212:215], v[88:91]
	v_mfma_f32_16x16x32_bf16 v[80:83], v[172:175], v[212:215], v[80:83]
	v_mfma_f32_16x16x32_bf16 v[72:75], v[164:167], v[224:227], v[72:75]
	v_mfma_f32_16x16x32_bf16 v[64:67], v[172:175], v[224:227], v[64:67]
	v_mfma_f32_16x16x32_bf16 v[126:129], v[176:179], v[192:195], v[126:129]
	v_mfma_f32_16x16x32_bf16 v[118:121], v[184:187], v[192:195], v[118:121]
	v_mfma_f32_16x16x32_bf16 v[110:113], v[176:179], v[200:203], v[110:113]
	v_mfma_f32_16x16x32_bf16 v[102:105], v[184:187], v[200:203], v[102:105]
	v_mfma_f32_16x16x32_bf16 v[92:95], v[176:179], v[208:211], v[92:95]
	v_mfma_f32_16x16x32_bf16 v[84:87], v[184:187], v[208:211], v[84:87]
	v_mfma_f32_16x16x32_bf16 v[76:79], v[176:179], v[220:223], v[76:79]
	v_mfma_f32_16x16x32_bf16 v[68:71], v[184:187], v[220:223], v[68:71]
	v_mfma_f32_16x16x32_bf16 v[126:129], v[180:183], v[196:199], v[126:129]
	v_mfma_f32_16x16x32_bf16 v[118:121], v[188:191], v[196:199], v[118:121]
	v_mfma_f32_16x16x32_bf16 v[110:113], v[180:183], v[204:207], v[110:113]
	v_mfma_f32_16x16x32_bf16 v[102:105], v[188:191], v[204:207], v[102:105]
	v_mfma_f32_16x16x32_bf16 v[92:95], v[180:183], v[212:215], v[92:95]
	v_mfma_f32_16x16x32_bf16 v[84:87], v[188:191], v[212:215], v[84:87]
	v_mfma_f32_16x16x32_bf16 v[76:79], v[180:183], v[224:227], v[76:79]
	v_mfma_f32_16x16x32_bf16 v[68:71], v[188:191], v[224:227], v[68:71]
	s_barrier
	v_mov_b32_e32 v135, v138
	s_add_i32 s2, s76, s63
	ds_read_b128 v[192:195], v152 offset:16384
	ds_read_b128 v[196:199], v152 offset:17408
	ds_read_b128 v[200:203], v152 offset:18432
	ds_read_b128 v[204:207], v152 offset:19456
	ds_read_b128 v[208:211], v152 offset:20480
	ds_read_b128 v[212:215], v152 offset:21504
	ds_read_b128 v[220:223], v152 offset:22528
	ds_read_b128 v[224:227], v152 offset:23552
	s_mov_b32 m0, s2
	s_nop 0
	global_load_lds_dwordx4 v135, s[22:23]
	v_mov_b32_e32 v135, v141
	s_add_i32 m0, s2, 0x2000
	s_add_u32 s2, s22, 0x40000
	global_load_lds_dwordx4 v135, s[22:23]
	s_addc_u32 s3, s23, 0
	v_mov_b32_e32 v135, v138
	s_add_i32 s76, s77, s63
	s_mov_b32 m0, s76
	s_nop 0
	global_load_lds_dwordx4 v135, s[2:3]
	v_mov_b32_e32 v135, v141
	s_add_i32 m0, s76, 0x2000
	s_nop 0
	global_load_lds_dwordx4 v135, s[2:3]
	v_mov_b32_e32 v135, v134
	s_mov_b32 m0, s64
	s_nop 0
	global_load_lds_dwordx4 v135, s[20:21]
	v_mov_b32_e32 v135, v132
	s_mov_b32 m0, s65
	s_nop 0
	global_load_lds_dwordx4 v135, s[20:21]
	s_waitcnt vmcnt(8)
	s_waitcnt lgkmcnt(0)
	s_barrier
; #define PG8_STAGE(bufoff, gbase, voff) do { _Pragma("unroll") for (int _i = 0; _i < 2; ++_i) \
;         __builtin_amdgcn_global_load_lds((const __attribute__((address_space(1))) unsigned*)((const __attribute__((address_space(1))) char*)(gbase) + (unsigned)lnd_v((int)(voff)[_i])), (LAS unsigned*)(lds + (bufoff) + ldsw + _i * 8192), 16, 0, 0); } while (0)
; #define PG8_LDA(dst, b, h) do { _Pragma("unroll") for (int m = 0; m < 4; ++m) _Pragma("unroll") for (int k = 0; k < 2; ++k) dst[m][k] = *(const LAS bf16x8*)(lds + PG8_SA(b, h) + aoff + m * 2048 + k * 1024); } while (0)
; #define PG8_LDB(dst, b, h) do { _Pragma("unroll") for (int n = 0; n < 2; ++n) _Pragma("unroll") for (int k = 0; k < 2; ++k) dst[n][k] = *(const LAS bf16x8*)(lds + PG8_SB(b, h) + boff + n * 2048 + k * 1024); } while (0)
; #define PG8_MMA(ai, bj, At, Bt) do { __builtin_amdgcn_s_setprio(1); _Pragma("unroll") for (int m = 0; m < 4; ++m) _Pragma("unroll") for (int n = 0; n < 2; ++n) _Pragma("unroll") for (int k = 0; k < 2; ++k) \
;         acc[ai][bj][m][n] = __builtin_amdgcn_mfma_f32_16x16x32_bf16(Bt[n][k], At[m][k], acc[ai][bj][m][n], 0, 0, 0); __builtin_amdgcn_s_setprio(0); } while (0)
; #define PG8_WAIT_V(n) asm volatile("s_waitcnt vmcnt(" #n ")" ::: "memory")
; #define PG8_WAIT_L(n) asm volatile("s_waitcnt lgkmcnt(" #n ")" ::: "memory")
; #define PG8_BAR __builtin_amdgcn_s_barrier()
; #define PG8_SCHED __builtin_amdgcn_sched_barrier(0)
; template <class Desc, class Epi>
; __device__ __forceinline__ void gemm_phase(const int wv_, LAS unsigned char* lds, const Desc& d, const Epi& E) {
;     ...
;             PG8_WAIT_V(8); PG8_WAIT_L(0); PG8_BAR; PG8_MMA(1, 0, At, B0); PG8_MMA(1, 1, At, B1); PG8_BAR; PG8_SCHED;
;             PG8_LDB(B0, 1, 0); PG8_LDB(B1, 1, 1); PG8_SCHED; PG8_LDA(At, 1, 0); PG8_STAGE(PG8_SA(0, 1), a2, sA1);
;             PG8_WAIT_V(8); PG8_WAIT_L(0); PG8_BAR; PG8_MMA(0, 0, At, B0); PG8_MMA(0, 1, At, B1); PG8_BAR; PG8_SCHED;
	s_waitcnt lgkmcnt(0)
	v_mfma_f32_16x16x32_bf16 v[56:59], v[160:163], v[192:195], v[56:59]
	v_mfma_f32_16x16x32_bf16 v[48:51], v[168:171], v[192:195], v[48:51]
	v_mfma_f32_16x16x32_bf16 v[40:43], v[160:163], v[200:203], v[40:43]
	v_mfma_f32_16x16x32_bf16 v[32:35], v[168:171], v[200:203], v[32:35]
	v_mfma_f32_16x16x32_bf16 v[24:27], v[160:163], v[208:211], v[24:27]
	v_mfma_f32_16x16x32_bf16 v[16:19], v[168:171], v[208:211], v[16:19]
	v_mfma_f32_16x16x32_bf16 v[8:11], v[160:163], v[220:223], v[8:11]
	v_mfma_f32_16x16x32_bf16 v[4:7], v[168:171], v[220:223], v[4:7]
	v_mfma_f32_16x16x32_bf16 v[56:59], v[164:167], v[196:199], v[56:59]
	v_mfma_f32_16x16x32_bf16 v[48:51], v[172:175], v[196:199], v[48:51]
	v_mfma_f32_16x16x32_bf16 v[40:43], v[164:167], v[204:207], v[40:43]
	v_mfma_f32_16x16x32_bf16 v[32:35], v[172:175], v[204:207], v[32:35]
	v_mfma_f32_16x16x32_bf16 v[24:27], v[164:167], v[212:215], v[24:27]
	v_mfma_f32_16x16x32_bf16 v[16:19], v[172:175], v[212:215], v[16:19]
	v_mfma_f32_16x16x32_bf16 v[8:11], v[164:167], v[224:227], v[8:11]
	v_mfma_f32_16x16x32_bf16 v[4:7], v[172:175], v[224:227], v[4:7]
	v_mfma_f32_16x16x32_bf16 v[60:63], v[176:179], v[192:195], v[60:63]
	v_mfma_f32_16x16x32_bf16 v[52:55], v[184:187], v[192:195], v[52:55]
	v_mfma_f32_16x16x32_bf16 v[44:47], v[176:179], v[200:203], v[44:47]
	v_mfma_f32_16x16x32_bf16 v[36:39], v[184:187], v[200:203], v[36:39]
	v_mfma_f32_16x16x32_bf16 v[28:31], v[176:179], v[208:211], v[28:31]
	v_mfma_f32_16x16x32_bf16 v[20:23], v[184:187], v[208:211], v[20:23]
	v_mfma_f32_16x16x32_bf16 v[12:15], v[176:179], v[220:223], v[12:15]
	v_mfma_f32_16x16x32_bf16 v[0:3], v[184:187], v[220:223], v[0:3]
	v_mfma_f32_16x16x32_bf16 v[60:63], v[180:183], v[196:199], v[60:63]
	v_mfma_f32_16x16x32_bf16 v[52:55], v[188:191], v[196:199], v[52:55]
	v_mfma_f32_16x16x32_bf16 v[44:47], v[180:183], v[204:207], v[44:47]
	v_mfma_f32_16x16x32_bf16 v[36:39], v[188:191], v[204:207], v[36:39]
	v_mfma_f32_16x16x32_bf16 v[28:31], v[180:183], v[212:215], v[28:31]
	v_mfma_f32_16x16x32_bf16 v[20:23], v[188:191], v[212:215], v[20:23]
	v_mfma_f32_16x16x32_bf16 v[12:15], v[180:183], v[224:227], v[12:15]
	v_mfma_f32_16x16x32_bf16 v[0:3], v[188:191], v[224:227], v[0:3]
	s_barrier
	s_add_i32 s2, 0, 0x18000
	v_add_u32_e32 v135, s2, v143
	s_add_i32 s76, 0, 0x1c000
	ds_read_b128 v[160:163], v135
	ds_read_b128 v[164:167], v135 offset:1024
	ds_read_b128 v[168:171], v135 offset:2048
	ds_read_b128 v[172:175], v135 offset:3072
	v_add_u32_e32 v135, s76, v143
	ds_read_b128 v[176:179], v135
	ds_read_b128 v[180:183], v135 offset:1024
	ds_read_b128 v[184:187], v135 offset:2048
	ds_read_b128 v[188:191], v135 offset:3072
	s_mov_b32 m0, s68
	ds_read_b128 v[192:195], v152 offset:32768
	ds_read_b128 v[196:199], v152 offset:33792
	ds_read_b128 v[200:203], v152 offset:34816
	ds_read_b128 v[204:207], v152 offset:35840
	ds_read_b128 v[208:211], v152 offset:36864
	ds_read_b128 v[212:215], v152 offset:37888
	ds_read_b128 v[220:223], v152 offset:38912
	ds_read_b128 v[224:227], v152 offset:39936
	s_nop 0
	global_load_lds_dwordx4 v96, s[20:21]
	s_mov_b32 m0, s69
	s_nop 0
	global_load_lds_dwordx4 v133, s[20:21]
	s_waitcnt vmcnt(8)
	s_waitcnt lgkmcnt(0)
	s_barrier
	s_waitcnt lgkmcnt(0)
	v_mfma_f32_16x16x32_bf16 v[122:125], v[160:163], v[192:195], v[122:125]
	v_mfma_f32_16x16x32_bf16 v[114:117], v[168:171], v[192:195], v[114:117]
	v_mfma_f32_16x16x32_bf16 v[106:109], v[160:163], v[200:203], v[106:109]
	v_mfma_f32_16x16x32_bf16 v[98:101], v[168:171], v[200:203], v[98:101]
	v_mfma_f32_16x16x32_bf16 v[88:91], v[160:163], v[208:211], v[88:91]
	v_mfma_f32_16x16x32_bf16 v[80:83], v[168:171], v[208:211], v[80:83]
	v_mfma_f32_16x16x32_bf16 v[72:75], v[160:163], v[220:223], v[72:75]
	v_mfma_f32_16x16x32_bf16 v[64:67], v[168:171], v[220:223], v[64:67]
	v_mfma_f32_16x16x32_bf16 v[122:125], v[164:167], v[196:199], v[122:125]
	v_mfma_f32_16x16x32_bf16 v[114:117], v[172:175], v[196:199], v[114:117]
	v_mfma_f32_16x16x32_bf16 v[106:109], v[164:167], v[204:207], v[106:109]
	v_mfma_f32_16x16x32_bf16 v[98:101], v[172:175], v[204:207], v[98:101]
	v_mfma_f32_16x16x32_bf16 v[88:91], v[164:167], v[212:215], v[88:91]
	v_mfma_f32_16x16x32_bf16 v[80:83], v[172:175], v[212:215], v[80:83]
	v_mfma_f32_16x16x32_bf16 v[72:75], v[164:167], v[224:227], v[72:75]
	v_mfma_f32_16x16x32_bf16 v[64:67], v[172:175], v[224:227], v[64:67]
	v_mfma_f32_16x16x32_bf16 v[126:129], v[176:179], v[192:195], v[126:129]
	v_mfma_f32_16x16x32_bf16 v[118:121], v[184:187], v[192:195], v[118:121]
	v_mfma_f32_16x16x32_bf16 v[110:113], v[176:179], v[200:203], v[110:113]
	v_mfma_f32_16x16x32_bf16 v[102:105], v[184:187], v[200:203], v[102:105]
	v_mfma_f32_16x16x32_bf16 v[92:95], v[176:179], v[208:211], v[92:95]
	v_mfma_f32_16x16x32_bf16 v[84:87], v[184:187], v[208:211], v[84:87]
	v_mfma_f32_16x16x32_bf16 v[76:79], v[176:179], v[220:223], v[76:79]
	v_mfma_f32_16x16x32_bf16 v[68:71], v[184:187], v[220:223], v[68:71]
	v_mfma_f32_16x16x32_bf16 v[126:129], v[180:183], v[196:199], v[126:129]
	v_mfma_f32_16x16x32_bf16 v[118:121], v[188:191], v[196:199], v[118:121]
	v_mfma_f32_16x16x32_bf16 v[110:113], v[180:183], v[204:207], v[110:113]
	v_mfma_f32_16x16x32_bf16 v[102:105], v[188:191], v[204:207], v[102:105]
	v_mfma_f32_16x16x32_bf16 v[92:95], v[180:183], v[212:215], v[92:95]
	v_mfma_f32_16x16x32_bf16 v[84:87], v[188:191], v[212:215], v[84:87]
	v_mfma_f32_16x16x32_bf16 v[76:79], v[180:183], v[224:227], v[76:79]
	v_mfma_f32_16x16x32_bf16 v[68:71], v[188:191], v[224:227], v[68:71]
	s_barrier
; #define PG8_STAGE(bufoff, gbase, voff) do { _Pragma("unroll") for (int _i = 0; _i < 2; ++_i) \
;         __builtin_amdgcn_global_load_lds((const __attribute__((address_space(1))) unsigned*)((const __attribute__((address_space(1))) char*)(gbase) + (unsigned)lnd_v((int)(voff)[_i])), (LAS unsigned*)(lds + (bufoff) + ldsw + _i * 8192), 16, 0, 0); } while (0)
; #define PG8_LDA(dst, b, h) do { _Pragma("unroll") for (int m = 0; m < 4; ++m) _Pragma("unroll") for (int k = 0; k < 2; ++k) dst[m][k] = *(const LAS bf16x8*)(lds + PG8_SA(b, h) + aoff + m * 2048 + k * 1024); } while (0)
; #define PG8_MMA(ai, bj, At, Bt) do { __builtin_amdgcn_s_setprio(1); _Pragma("unroll") for (int m = 0; m < 4; ++m) _Pragma("unroll") for (int n = 0; n < 2; ++n) _Pragma("unroll") for (int k = 0; k < 2; ++k) \
;         acc[ai][bj][m][n] = __builtin_amdgcn_mfma_f32_16x16x32_bf16(Bt[n][k], At[m][k], acc[ai][bj][m][n], 0, 0, 0); __builtin_amdgcn_s_setprio(0); } while (0)
; #define PG8_WAIT_V(n) asm volatile("s_waitcnt vmcnt(" #n ")" ::: "memory")
; #define PG8_WAIT_L(n) asm volatile("s_waitcnt lgkmcnt(" #n ")" ::: "memory")
; #define PG8_BAR __builtin_amdgcn_s_barrier()
; #define PG8_SCHED __builtin_amdgcn_sched_barrier(0)
; template <class Desc, class Epi>
; __device__ __forceinline__ void gemm_phase(const int wv_, LAS unsigned char* lds, const Desc& d, const Epi& E) {
;     ...
;             PG8_LDA(At, 1, 1); PG8_STAGE(PG8_SB(1, 0), b3, voffB); PG8_STAGE(PG8_SB(1, 1), b3 + hstepB, voffB); PG8_STAGE(PG8_SA(1, 0), a3, sA0);
;             PG8_WAIT_V(8); PG8_WAIT_L(0); PG8_BAR; PG8_MMA(1, 0, At, B0); PG8_MMA(1, 1, At, B1); PG8_BAR; PG8_SCHED;
;         }
;         if (wr == 0) PG8_BAR;
	v_mov_b32_e32 v96, v138
	ds_read_b128 v[192:195], v152 offset:49152
	ds_read_b128 v[196:199], v152 offset:50176
	ds_read_b128 v[200:203], v152 offset:51200
	ds_read_b128 v[204:207], v152 offset:52224
	ds_read_b128 v[208:211], v152 offset:53248
	ds_read_b128 v[212:215], v152 offset:54272
	ds_read_b128 v[220:223], v152 offset:55296
	ds_read_b128 v[224:227], v152 offset:56320
	s_add_i32 s2, s2, s63
	v_lshl_add_u64 v[228:229], s[22:23], 0, v[96:97]
	v_lshl_add_u64 v[228:229], v[228:229], 0, s[30:31]
	s_mov_b32 m0, s2
	v_mov_b32_e32 v96, v141
	global_load_lds_dwordx4 v[228:229], off
	s_add_i32 m0, s2, 0x2000
	s_add_u32 s2, s22, 0x40080
	v_lshl_add_u64 v[228:229], s[22:23], 0, v[96:97]
	v_lshl_add_u64 v[228:229], v[228:229], 0, s[30:31]
	s_addc_u32 s3, s23, 0
	v_mov_b32_e32 v96, v138
	s_add_i32 s22, s76, s63
	global_load_lds_dwordx4 v[228:229], off
	s_mov_b32 m0, s22
	v_mov_b32_e32 v135, v97
	global_load_lds_dwordx4 v96, s[2:3]
	v_mov_b32_e32 v96, v141
	s_add_i32 m0, s22, 0x2000
	v_mov_b32_e32 v133, v97
	global_load_lds_dwordx4 v96, s[2:3]
	s_mov_b32 m0, s70
	v_lshl_add_u64 v[134:135], s[20:21], 0, v[134:135]
	v_lshl_add_u64 v[134:135], v[134:135], 0, s[30:31]
	global_load_lds_dwordx4 v[134:135], off
	s_mov_b32 m0, s71
	v_lshl_add_u64 v[132:133], s[20:21], 0, v[132:133]
	v_lshl_add_u64 v[132:133], v[132:133], 0, s[30:31]
	global_load_lds_dwordx4 v[132:133], off
	s_waitcnt vmcnt(8)
	s_waitcnt lgkmcnt(0)
	s_barrier
	s_waitcnt lgkmcnt(0)
	v_mfma_f32_16x16x32_bf16 v[56:59], v[160:163], v[192:195], v[56:59]
	v_mfma_f32_16x16x32_bf16 v[48:51], v[168:171], v[192:195], v[48:51]
	v_mfma_f32_16x16x32_bf16 v[40:43], v[160:163], v[200:203], v[40:43]
	v_mfma_f32_16x16x32_bf16 v[32:35], v[168:171], v[200:203], v[32:35]
	v_mfma_f32_16x16x32_bf16 v[24:27], v[160:163], v[208:211], v[24:27]
	v_mfma_f32_16x16x32_bf16 v[16:19], v[168:171], v[208:211], v[16:19]
	v_mfma_f32_16x16x32_bf16 v[8:11], v[160:163], v[220:223], v[8:11]
	v_mfma_f32_16x16x32_bf16 v[4:7], v[168:171], v[220:223], v[4:7]
	v_mfma_f32_16x16x32_bf16 v[56:59], v[164:167], v[196:199], v[56:59]
	v_mfma_f32_16x16x32_bf16 v[48:51], v[172:175], v[196:199], v[48:51]
	v_mfma_f32_16x16x32_bf16 v[40:43], v[164:167], v[204:207], v[40:43]
	v_mfma_f32_16x16x32_bf16 v[32:35], v[172:175], v[204:207], v[32:35]
	v_mfma_f32_16x16x32_bf16 v[24:27], v[164:167], v[212:215], v[24:27]
	v_mfma_f32_16x16x32_bf16 v[16:19], v[172:175], v[212:215], v[16:19]
	v_mfma_f32_16x16x32_bf16 v[8:11], v[164:167], v[224:227], v[8:11]
	v_mfma_f32_16x16x32_bf16 v[4:7], v[172:175], v[224:227], v[4:7]
	v_mfma_f32_16x16x32_bf16 v[60:63], v[176:179], v[192:195], v[60:63]
	v_mfma_f32_16x16x32_bf16 v[52:55], v[184:187], v[192:195], v[52:55]
	v_mfma_f32_16x16x32_bf16 v[44:47], v[176:179], v[200:203], v[44:47]
	v_mfma_f32_16x16x32_bf16 v[36:39], v[184:187], v[200:203], v[36:39]
	v_mfma_f32_16x16x32_bf16 v[28:31], v[176:179], v[208:211], v[28:31]
	v_mfma_f32_16x16x32_bf16 v[20:23], v[184:187], v[208:211], v[20:23]
	v_mfma_f32_16x16x32_bf16 v[12:15], v[176:179], v[220:223], v[12:15]
	v_mfma_f32_16x16x32_bf16 v[0:3], v[184:187], v[220:223], v[0:3]
	v_mfma_f32_16x16x32_bf16 v[60:63], v[180:183], v[196:199], v[60:63]
	v_mfma_f32_16x16x32_bf16 v[52:55], v[188:191], v[196:199], v[52:55]
	v_mfma_f32_16x16x32_bf16 v[44:47], v[180:183], v[204:207], v[44:47]
	v_mfma_f32_16x16x32_bf16 v[36:39], v[188:191], v[204:207], v[36:39]
	v_mfma_f32_16x16x32_bf16 v[28:31], v[180:183], v[212:215], v[28:31]
	v_mfma_f32_16x16x32_bf16 v[20:23], v[188:191], v[212:215], v[20:23]
	v_mfma_f32_16x16x32_bf16 v[12:15], v[180:183], v[224:227], v[12:15]
	v_mfma_f32_16x16x32_bf16 v[0:3], v[188:191], v[224:227], v[0:3]
	s_barrier
	s_add_i32 s75, s75, 2
	s_cmp_gt_u32 s75, 13
	s_mov_b64 s[2:3], s[4:5]
	s_cbranch_scc0 .LBB0_1565
	s_and_b64 vcc, exec, s[52:53]
	s_cbranch_vccz .LBB0_1568
	s_barrier

; #define PG8_AOFF(ord, U, O0, O1) do { _Pragma("unroll") for (int _i = 0; _i < 2; ++_i) { \
;         O0[_i] = d.rowbyte(U, (int)tix[(ord) * 256 + Rr[_i]]) + (unsigned)(Cc[_i] * 2); O1[_i] = d.rowbyte(U, (int)tix[(ord) * 256 + HALF + Rr[_i]]) + (unsigned)(Cc[_i] * 2); } } while (0)
; #define PG8_STAGE(bufoff, gbase, voff) do { _Pragma("unroll") for (int _i = 0; _i < 2; ++_i) \
;         __builtin_amdgcn_global_load_lds((const __attribute__((address_space(1))) unsigned*)((const __attribute__((address_space(1))) char*)(gbase) + (unsigned)lnd_v((int)(voff)[_i])), (LAS unsigned*)(lds + (bufoff) + ldsw + _i * 8192), 16, 0, 0); } while (0)
; #define PG8_WAIT_V(n) asm volatile("s_waitcnt vmcnt(" #n ")" ::: "memory")
; #define PG8_WAIT_L(n) asm volatile("s_waitcnt lgkmcnt(" #n ")" ::: "memory")
; #define PG8_BAR __builtin_amdgcn_s_barrier()
; template <class Desc, class Epi>
; __device__ __forceinline__ void gemm_phase(const int wv_, LAS unsigned char* lds, const Desc& d, const Epi& E) {
;     ...
;         if constexpr (Desc::GATHER) { if (has_next) PG8_AOFF(ui + 1, nxt, voffAn, voffAn1); else { voffAn[0] = voffA[0]; voffAn[1] = voffA[1]; voffAn1[0] = voffA1[0]; voffAn1[1] = voffA1[1]; } }
;         const char* nA = has_next ? (const char*)nxt.a : cA; const char* nB = has_next ? (const char*)nxt.b : cB;
;         for (int t = 0; t < nt; t += 2) {
;             const bool last = (t == nt - 2);
;             unsigned sA0[2], sA1[2];
;             if constexpr (Desc::GATHER) { sA0[0] = last ? voffAn[0] : voffA[0]; sA0[1] = last ? voffAn[1] : voffA[1]; sA1[0] = last ? voffAn1[0] : voffA1[0]; sA1[1] = last ? voffAn1[1] : voffA1[1]; }
;             else { sA0[0] = voffA[0]; sA0[1] = voffA[1]; sA1[0] = voffA1[0]; sA1[1] = voffA1[1]; }
;             const char* a1 = cA + (size_t)(t + 1) * kstep;
;             const char* a2 = last ? nA : cA + (size_t)(t + 2) * kstep; const char* b2 = last ? nB : cB + (size_t)(t + 2) * kstep;
;             const char* a3 = a2 + kstep; const char* b3 = b2 + kstep;
;             PG8_LDB(B0, 0, 0); PG8_LDB(B1, 0, 1); PG8_SCHED; PG8_LDA(At, 0, 0); PG8_STAGE(PG8_SA(1, 1), a1, voffA1);
;             PG8_WAIT_V(8); PG8_WAIT_L(0); PG8_BAR; PG8_MMA(0, 0, At, B0); PG8_MMA(0, 1, At, B1); PG8_BAR; PG8_SCHED;
;             PG8_LDA(At, 0, 1); PG8_STAGE(PG8_SB(0, 0), b2, voffB); PG8_STAGE(PG8_SB(0, 1), b2 + hstepB, voffB); PG8_STAGE(PG8_SA(0, 0), a2, sA0);
.LBB0_1861:
	s_add_u32 s4, s2, 0x100
	s_addc_u32 s5, s3, 0
	s_add_u32 s22, s29, s2
	s_addc_u32 s23, s51, s3
	s_cmp_eq_u32 s66, 12
	s_cselect_b64 vcc, -1, 0
	s_and_b64 s[20:21], vcc, exec
	s_cselect_b32 s20, 0, s4
	s_cselect_b32 s21, 0, s5
	s_cselect_b32 s22, s46, s22
	s_cselect_b32 s23, s47, s23
	s_add_u32 s20, s42, s20
	s_addc_u32 s21, s43, s21
	s_add_i32 s67, 0, 0x10000
	v_add_u32_e32 v135, s67, v143
	s_add_i32 s68, 0, 0x14000
	ds_read_b128 v[160:163], v135
	ds_read_b128 v[164:167], v135 offset:1024
	ds_read_b128 v[168:171], v135 offset:2048
	ds_read_b128 v[172:175], v135 offset:3072
	v_add_u32_e32 v135, s68, v143
	ds_read_b128 v[176:179], v135
	ds_read_b128 v[180:183], v135 offset:1024
	ds_read_b128 v[184:187], v135 offset:2048
	ds_read_b128 v[188:191], v135 offset:3072
	v_cndmask_b32_e32 v134, v157, v153, vcc
	v_cndmask_b32_e32 v132, v159, v154, vcc
	v_cndmask_b32_e32 v96, v131, v155, vcc
	v_cndmask_b32_e32 v133, v158, v156, vcc
	s_add_i32 m0, s57, 0xc000
	v_mov_b32_e32 v135, v131
	s_add_u32 s2, s38, s2
	ds_read_b128 v[192:195], v152
	ds_read_b128 v[196:199], v152 offset:1024
	ds_read_b128 v[200:203], v152 offset:2048
	ds_read_b128 v[204:207], v152 offset:3072
	ds_read_b128 v[208:211], v152 offset:4096
	ds_read_b128 v[212:215], v152 offset:5120
	ds_read_b128 v[220:223], v152 offset:6144
	ds_read_b128 v[224:227], v152 offset:7168
	s_addc_u32 s3, s39, s3
	global_load_lds_dwordx4 v135, s[2:3]
	v_mov_b32_e32 v135, v158
	s_add_i32 m0, s57, 0xe000
	s_nop 0
	global_load_lds_dwordx4 v135, s[2:3]
	s_waitcnt vmcnt(8)
	s_waitcnt lgkmcnt(0)
	s_barrier
	s_waitcnt lgkmcnt(0)
	v_mfma_f32_16x16x32_bf16 v[122:125], v[160:163], v[192:195], v[122:125]
	v_mfma_f32_16x16x32_bf16 v[114:117], v[168:171], v[192:195], v[114:117]
	v_mfma_f32_16x16x32_bf16 v[106:109], v[160:163], v[200:203], v[106:109]
	v_mfma_f32_16x16x32_bf16 v[98:101], v[168:171], v[200:203], v[98:101]
	v_mfma_f32_16x16x32_bf16 v[88:91], v[160:163], v[208:211], v[88:91]
	v_mfma_f32_16x16x32_bf16 v[80:83], v[168:171], v[208:211], v[80:83]
	v_mfma_f32_16x16x32_bf16 v[72:75], v[160:163], v[220:223], v[72:75]
	v_mfma_f32_16x16x32_bf16 v[64:67], v[168:171], v[220:223], v[64:67]
	v_mfma_f32_16x16x32_bf16 v[122:125], v[164:167], v[196:199], v[122:125]
	v_mfma_f32_16x16x32_bf16 v[114:117], v[172:175], v[196:199], v[114:117]
	v_mfma_f32_16x16x32_bf16 v[106:109], v[164:167], v[204:207], v[106:109]
	v_mfma_f32_16x16x32_bf16 v[98:101], v[172:175], v[204:207], v[98:101]
	v_mfma_f32_16x16x32_bf16 v[88:91], v[164:167], v[212:215], v[88:91]
	v_mfma_f32_16x16x32_bf16 v[80:83], v[172:175], v[212:215], v[80:83]
	v_mfma_f32_16x16x32_bf16 v[72:75], v[164:167], v[224:227], v[72:75]
	v_mfma_f32_16x16x32_bf16 v[64:67], v[172:175], v[224:227], v[64:67]
	v_mfma_f32_16x16x32_bf16 v[126:129], v[176:179], v[192:195], v[126:129]
	v_mfma_f32_16x16x32_bf16 v[118:121], v[184:187], v[192:195], v[118:121]
	v_mfma_f32_16x16x32_bf16 v[110:113], v[176:179], v[200:203], v[110:113]
	v_mfma_f32_16x16x32_bf16 v[102:105], v[184:187], v[200:203], v[102:105]
	v_mfma_f32_16x16x32_bf16 v[92:95], v[176:179], v[208:211], v[92:95]
	v_mfma_f32_16x16x32_bf16 v[84:87], v[184:187], v[208:211], v[84:87]
	v_mfma_f32_16x16x32_bf16 v[76:79], v[176:179], v[220:223], v[76:79]
	v_mfma_f32_16x16x32_bf16 v[68:71], v[184:187], v[220:223], v[68:71]
	v_mfma_f32_16x16x32_bf16 v[126:129], v[180:183], v[196:199], v[126:129]
	v_mfma_f32_16x16x32_bf16 v[118:121], v[188:191], v[196:199], v[118:121]
	v_mfma_f32_16x16x32_bf16 v[110:113], v[180:183], v[204:207], v[110:113]
	v_mfma_f32_16x16x32_bf16 v[102:105], v[188:191], v[204:207], v[102:105]
	v_mfma_f32_16x16x32_bf16 v[92:95], v[180:183], v[212:215], v[92:95]
	v_mfma_f32_16x16x32_bf16 v[84:87], v[188:191], v[212:215], v[84:87]
	v_mfma_f32_16x16x32_bf16 v[76:79], v[180:183], v[224:227], v[76:79]
	v_mfma_f32_16x16x32_bf16 v[68:71], v[188:191], v[224:227], v[68:71]
	s_barrier
	v_mov_b32_e32 v135, v138
	s_add_i32 s2, s67, s56
	ds_read_b128 v[192:195], v152 offset:16384
	ds_read_b128 v[196:199], v152 offset:17408
	ds_read_b128 v[200:203], v152 offset:18432
	ds_read_b128 v[204:207], v152 offset:19456
	ds_read_b128 v[208:211], v152 offset:20480
	ds_read_b128 v[212:215], v152 offset:21504
	ds_read_b128 v[220:223], v152 offset:22528
	ds_read_b128 v[224:227], v152 offset:23552
	s_mov_b32 m0, s2
	s_nop 0
	global_load_lds_dwordx4 v135, s[22:23]
	v_mov_b32_e32 v135, v141
	s_add_i32 m0, s2, 0x2000
	s_add_u32 s2, s22, 0x40000
	global_load_lds_dwordx4 v135, s[22:23]
	s_addc_u32 s3, s23, 0
	v_mov_b32_e32 v135, v138
	s_add_i32 s67, s68, s56
	s_mov_b32 m0, s67
	s_nop 0
	global_load_lds_dwordx4 v135, s[2:3]
	v_mov_b32_e32 v135, v141
	s_add_i32 m0, s67, 0x2000
	s_nop 0
	global_load_lds_dwordx4 v135, s[2:3]
	v_mov_b32_e32 v135, v134
	s_mov_b32 m0, s57
	s_nop 0
	global_load_lds_dwordx4 v135, s[20:21]
	v_mov_b32_e32 v135, v132
	s_mov_b32 m0, s58
	s_nop 0
	global_load_lds_dwordx4 v135, s[20:21]
	s_waitcnt vmcnt(8)
	s_waitcnt lgkmcnt(0)
	s_barrier
; #define PG8_STAGE(bufoff, gbase, voff) do { _Pragma("unroll") for (int _i = 0; _i < 2; ++_i) \
;         __builtin_amdgcn_global_load_lds((const __attribute__((address_space(1))) unsigned*)((const __attribute__((address_space(1))) char*)(gbase) + (unsigned)lnd_v((int)(voff)[_i])), (LAS unsigned*)(lds + (bufoff) + ldsw + _i * 8192), 16, 0, 0); } while (0)
; #define PG8_LDA(dst, b, h) do { _Pragma("unroll") for (int m = 0; m < 4; ++m) _Pragma("unroll") for (int k = 0; k < 2; ++k) dst[m][k] = *(const LAS bf16x8*)(lds + PG8_SA(b, h) + aoff + m * 2048 + k * 1024); } while (0)
; #define PG8_LDB(dst, b, h) do { _Pragma("unroll") for (int n = 0; n < 2; ++n) _Pragma("unroll") for (int k = 0; k < 2; ++k) dst[n][k] = *(const LAS bf16x8*)(lds + PG8_SB(b, h) + boff + n * 2048 + k * 1024); } while (0)
; #define PG8_MMA(ai, bj, At, Bt) do { __builtin_amdgcn_s_setprio(1); _Pragma("unroll") for (int m = 0; m < 4; ++m) _Pragma("unroll") for (int n = 0; n < 2; ++n) _Pragma("unroll") for (int k = 0; k < 2; ++k) \
;         acc[ai][bj][m][n] = __builtin_amdgcn_mfma_f32_16x16x32_bf16(Bt[n][k], At[m][k], acc[ai][bj][m][n], 0, 0, 0); __builtin_amdgcn_s_setprio(0); } while (0)
; #define PG8_WAIT_V(n) asm volatile("s_waitcnt vmcnt(" #n ")" ::: "memory")
; #define PG8_WAIT_L(n) asm volatile("s_waitcnt lgkmcnt(" #n ")" ::: "memory")
; #define PG8_BAR __builtin_amdgcn_s_barrier()
; #define PG8_SCHED __builtin_amdgcn_sched_barrier(0)
; template <class Desc, class Epi>
; __device__ __forceinline__ void gemm_phase(const int wv_, LAS unsigned char* lds, const Desc& d, const Epi& E) {
;     ...
;             PG8_WAIT_V(8); PG8_WAIT_L(0); PG8_BAR; PG8_MMA(1, 0, At, B0); PG8_MMA(1, 1, At, B1); PG8_BAR; PG8_SCHED;
;             PG8_LDB(B0, 1, 0); PG8_LDB(B1, 1, 1); PG8_SCHED; PG8_LDA(At, 1, 0); PG8_STAGE(PG8_SA(0, 1), a2, sA1);
;             PG8_WAIT_V(8); PG8_WAIT_L(0); PG8_BAR; PG8_MMA(0, 0, At, B0); PG8_MMA(0, 1, At, B1); PG8_BAR; PG8_SCHED;
	s_waitcnt lgkmcnt(0)
	v_mfma_f32_16x16x32_bf16 v[56:59], v[160:163], v[192:195], v[56:59]
	v_mfma_f32_16x16x32_bf16 v[48:51], v[168:171], v[192:195], v[48:51]
	v_mfma_f32_16x16x32_bf16 v[40:43], v[160:163], v[200:203], v[40:43]
	v_mfma_f32_16x16x32_bf16 v[32:35], v[168:171], v[200:203], v[32:35]
	v_mfma_f32_16x16x32_bf16 v[24:27], v[160:163], v[208:211], v[24:27]
	v_mfma_f32_16x16x32_bf16 v[16:19], v[168:171], v[208:211], v[16:19]
	v_mfma_f32_16x16x32_bf16 v[8:11], v[160:163], v[220:223], v[8:11]
	v_mfma_f32_16x16x32_bf16 v[4:7], v[168:171], v[220:223], v[4:7]
	v_mfma_f32_16x16x32_bf16 v[56:59], v[164:167], v[196:199], v[56:59]
	v_mfma_f32_16x16x32_bf16 v[48:51], v[172:175], v[196:199], v[48:51]
	v_mfma_f32_16x16x32_bf16 v[40:43], v[164:167], v[204:207], v[40:43]
	v_mfma_f32_16x16x32_bf16 v[32:35], v[172:175], v[204:207], v[32:35]
	v_mfma_f32_16x16x32_bf16 v[24:27], v[164:167], v[212:215], v[24:27]
	v_mfma_f32_16x16x32_bf16 v[16:19], v[172:175], v[212:215], v[16:19]
	v_mfma_f32_16x16x32_bf16 v[8:11], v[164:167], v[224:227], v[8:11]
	v_mfma_f32_16x16x32_bf16 v[4:7], v[172:175], v[224:227], v[4:7]
	v_mfma_f32_16x16x32_bf16 v[60:63], v[176:179], v[192:195], v[60:63]
	v_mfma_f32_16x16x32_bf16 v[52:55], v[184:187], v[192:195], v[52:55]
	v_mfma_f32_16x16x32_bf16 v[44:47], v[176:179], v[200:203], v[44:47]
	v_mfma_f32_16x16x32_bf16 v[36:39], v[184:187], v[200:203], v[36:39]
	v_mfma_f32_16x16x32_bf16 v[28:31], v[176:179], v[208:211], v[28:31]
	v_mfma_f32_16x16x32_bf16 v[20:23], v[184:187], v[208:211], v[20:23]
	v_mfma_f32_16x16x32_bf16 v[12:15], v[176:179], v[220:223], v[12:15]
	v_mfma_f32_16x16x32_bf16 v[0:3], v[184:187], v[220:223], v[0:3]
	v_mfma_f32_16x16x32_bf16 v[60:63], v[180:183], v[196:199], v[60:63]
	v_mfma_f32_16x16x32_bf16 v[52:55], v[188:191], v[196:199], v[52:55]
	v_mfma_f32_16x16x32_bf16 v[44:47], v[180:183], v[204:207], v[44:47]
	v_mfma_f32_16x16x32_bf16 v[36:39], v[188:191], v[204:207], v[36:39]
	v_mfma_f32_16x16x32_bf16 v[28:31], v[180:183], v[212:215], v[28:31]
	v_mfma_f32_16x16x32_bf16 v[20:23], v[188:191], v[212:215], v[20:23]
	v_mfma_f32_16x16x32_bf16 v[12:15], v[180:183], v[224:227], v[12:15]
	v_mfma_f32_16x16x32_bf16 v[0:3], v[188:191], v[224:227], v[0:3]
	s_barrier
	s_add_i32 s2, 0, 0x18000
	v_add_u32_e32 v135, s2, v143
	s_add_i32 s67, 0, 0x1c000
	ds_read_b128 v[160:163], v135
	ds_read_b128 v[164:167], v135 offset:1024
	ds_read_b128 v[168:171], v135 offset:2048
	ds_read_b128 v[172:175], v135 offset:3072
	v_add_u32_e32 v135, s67, v143
	ds_read_b128 v[176:179], v135
	ds_read_b128 v[180:183], v135 offset:1024
	ds_read_b128 v[184:187], v135 offset:2048
	ds_read_b128 v[188:191], v135 offset:3072
	s_mov_b32 m0, s59
	ds_read_b128 v[192:195], v152 offset:32768
	ds_read_b128 v[196:199], v152 offset:33792
	ds_read_b128 v[200:203], v152 offset:34816
	ds_read_b128 v[204:207], v152 offset:35840
	ds_read_b128 v[208:211], v152 offset:36864
	ds_read_b128 v[212:215], v152 offset:37888
	ds_read_b128 v[220:223], v152 offset:38912
	ds_read_b128 v[224:227], v152 offset:39936
	s_nop 0
	global_load_lds_dwordx4 v96, s[20:21]
	s_mov_b32 m0, s60
	s_nop 0
	global_load_lds_dwordx4 v133, s[20:21]
	s_waitcnt vmcnt(8)
	s_waitcnt lgkmcnt(0)
	s_barrier
	s_waitcnt lgkmcnt(0)
	v_mfma_f32_16x16x32_bf16 v[122:125], v[160:163], v[192:195], v[122:125]
	v_mfma_f32_16x16x32_bf16 v[114:117], v[168:171], v[192:195], v[114:117]
	v_mfma_f32_16x16x32_bf16 v[106:109], v[160:163], v[200:203], v[106:109]
	v_mfma_f32_16x16x32_bf16 v[98:101], v[168:171], v[200:203], v[98:101]
	v_mfma_f32_16x16x32_bf16 v[88:91], v[160:163], v[208:211], v[88:91]
	v_mfma_f32_16x16x32_bf16 v[80:83], v[168:171], v[208:211], v[80:83]
	v_mfma_f32_16x16x32_bf16 v[72:75], v[160:163], v[220:223], v[72:75]
	v_mfma_f32_16x16x32_bf16 v[64:67], v[168:171], v[220:223], v[64:67]
	v_mfma_f32_16x16x32_bf16 v[122:125], v[164:167], v[196:199], v[122:125]
	v_mfma_f32_16x16x32_bf16 v[114:117], v[172:175], v[196:199], v[114:117]
	v_mfma_f32_16x16x32_bf16 v[106:109], v[164:167], v[204:207], v[106:109]
	v_mfma_f32_16x16x32_bf16 v[98:101], v[172:175], v[204:207], v[98:101]
	v_mfma_f32_16x16x32_bf16 v[88:91], v[164:167], v[212:215], v[88:91]
	v_mfma_f32_16x16x32_bf16 v[80:83], v[172:175], v[212:215], v[80:83]
	v_mfma_f32_16x16x32_bf16 v[72:75], v[164:167], v[224:227], v[72:75]
	v_mfma_f32_16x16x32_bf16 v[64:67], v[172:175], v[224:227], v[64:67]
	v_mfma_f32_16x16x32_bf16 v[126:129], v[176:179], v[192:195], v[126:129]
	v_mfma_f32_16x16x32_bf16 v[118:121], v[184:187], v[192:195], v[118:121]
	v_mfma_f32_16x16x32_bf16 v[110:113], v[176:179], v[200:203], v[110:113]
	v_mfma_f32_16x16x32_bf16 v[102:105], v[184:187], v[200:203], v[102:105]
	v_mfma_f32_16x16x32_bf16 v[92:95], v[176:179], v[208:211], v[92:95]
	v_mfma_f32_16x16x32_bf16 v[84:87], v[184:187], v[208:211], v[84:87]
	v_mfma_f32_16x16x32_bf16 v[76:79], v[176:179], v[220:223], v[76:79]
	v_mfma_f32_16x16x32_bf16 v[68:71], v[184:187], v[220:223], v[68:71]
	v_mfma_f32_16x16x32_bf16 v[126:129], v[180:183], v[196:199], v[126:129]
	v_mfma_f32_16x16x32_bf16 v[118:121], v[188:191], v[196:199], v[118:121]
	v_mfma_f32_16x16x32_bf16 v[110:113], v[180:183], v[204:207], v[110:113]
	v_mfma_f32_16x16x32_bf16 v[102:105], v[188:191], v[204:207], v[102:105]
	v_mfma_f32_16x16x32_bf16 v[92:95], v[180:183], v[212:215], v[92:95]
	v_mfma_f32_16x16x32_bf16 v[84:87], v[188:191], v[212:215], v[84:87]
	v_mfma_f32_16x16x32_bf16 v[76:79], v[180:183], v[224:227], v[76:79]
	v_mfma_f32_16x16x32_bf16 v[68:71], v[188:191], v[224:227], v[68:71]
	s_barrier
; #define PG8_STAGE(bufoff, gbase, voff) do { _Pragma("unroll") for (int _i = 0; _i < 2; ++_i) \
;         __builtin_amdgcn_global_load_lds((const __attribute__((address_space(1))) unsigned*)((const __attribute__((address_space(1))) char*)(gbase) + (unsigned)lnd_v((int)(voff)[_i])), (LAS unsigned*)(lds + (bufoff) + ldsw + _i * 8192), 16, 0, 0); } while (0)
; #define PG8_LDA(dst, b, h) do { _Pragma("unroll") for (int m = 0; m < 4; ++m) _Pragma("unroll") for (int k = 0; k < 2; ++k) dst[m][k] = *(const LAS bf16x8*)(lds + PG8_SA(b, h) + aoff + m * 2048 + k * 1024); } while (0)
; #define PG8_MMA(ai, bj, At, Bt) do { __builtin_amdgcn_s_setprio(1); _Pragma("unroll") for (int m = 0; m < 4; ++m) _Pragma("unroll") for (int n = 0; n < 2; ++n) _Pragma("unroll") for (int k = 0; k < 2; ++k) \
;         acc[ai][bj][m][n] = __builtin_amdgcn_mfma_f32_16x16x32_bf16(Bt[n][k], At[m][k], acc[ai][bj][m][n], 0, 0, 0); __builtin_amdgcn_s_setprio(0); } while (0)
; #define PG8_WAIT_V(n) asm volatile("s_waitcnt vmcnt(" #n ")" ::: "memory")
; #define PG8_WAIT_L(n) asm volatile("s_waitcnt lgkmcnt(" #n ")" ::: "memory")
; #define PG8_BAR __builtin_amdgcn_s_barrier()
; #define PG8_SCHED __builtin_amdgcn_sched_barrier(0)
; template <class Desc, class Epi>
; __device__ __forceinline__ void gemm_phase(const int wv_, LAS unsigned char* lds, const Desc& d, const Epi& E) {
;     ...
;             PG8_LDA(At, 1, 1); PG8_STAGE(PG8_SB(1, 0), b3, voffB); PG8_STAGE(PG8_SB(1, 1), b3 + hstepB, voffB); PG8_STAGE(PG8_SA(1, 0), a3, sA0);
;             PG8_WAIT_V(8); PG8_WAIT_L(0); PG8_BAR; PG8_MMA(1, 0, At, B0); PG8_MMA(1, 1, At, B1); PG8_BAR; PG8_SCHED;
;         }
;         if (wr == 0) PG8_BAR;
	v_mov_b32_e32 v96, v138
	ds_read_b128 v[192:195], v152 offset:49152
	ds_read_b128 v[196:199], v152 offset:50176
	ds_read_b128 v[200:203], v152 offset:51200
	ds_read_b128 v[204:207], v152 offset:52224
	ds_read_b128 v[208:211], v152 offset:53248
	ds_read_b128 v[212:215], v152 offset:54272
	ds_read_b128 v[220:223], v152 offset:55296
	ds_read_b128 v[224:227], v152 offset:56320
	s_add_i32 s2, s2, s56
	v_lshl_add_u64 v[228:229], s[22:23], 0, v[96:97]
	v_lshl_add_u64 v[228:229], v[228:229], 0, s[30:31]
	s_mov_b32 m0, s2
	v_mov_b32_e32 v96, v141
	global_load_lds_dwordx4 v[228:229], off
	s_add_i32 m0, s2, 0x2000
	s_add_u32 s2, s22, 0x40080
	v_lshl_add_u64 v[228:229], s[22:23], 0, v[96:97]
	v_lshl_add_u64 v[228:229], v[228:229], 0, s[30:31]
	s_addc_u32 s3, s23, 0
	v_mov_b32_e32 v96, v138
	s_add_i32 s22, s67, s56
	global_load_lds_dwordx4 v[228:229], off
	s_mov_b32 m0, s22
	v_mov_b32_e32 v135, v97
	global_load_lds_dwordx4 v96, s[2:3]
	v_mov_b32_e32 v96, v141
	s_add_i32 m0, s22, 0x2000
	v_mov_b32_e32 v133, v97
	global_load_lds_dwordx4 v96, s[2:3]
	s_mov_b32 m0, s61
	v_lshl_add_u64 v[134:135], s[20:21], 0, v[134:135]
	v_lshl_add_u64 v[134:135], v[134:135], 0, s[30:31]
	global_load_lds_dwordx4 v[134:135], off
	s_mov_b32 m0, s62
	v_lshl_add_u64 v[132:133], s[20:21], 0, v[132:133]
	v_lshl_add_u64 v[132:133], v[132:133], 0, s[30:31]
	global_load_lds_dwordx4 v[132:133], off
	s_waitcnt vmcnt(8)
	s_waitcnt lgkmcnt(0)
	s_barrier
	s_waitcnt lgkmcnt(0)
	v_mfma_f32_16x16x32_bf16 v[56:59], v[160:163], v[192:195], v[56:59]
	v_mfma_f32_16x16x32_bf16 v[48:51], v[168:171], v[192:195], v[48:51]
	v_mfma_f32_16x16x32_bf16 v[40:43], v[160:163], v[200:203], v[40:43]
	v_mfma_f32_16x16x32_bf16 v[32:35], v[168:171], v[200:203], v[32:35]
	v_mfma_f32_16x16x32_bf16 v[24:27], v[160:163], v[208:211], v[24:27]
	v_mfma_f32_16x16x32_bf16 v[16:19], v[168:171], v[208:211], v[16:19]
	v_mfma_f32_16x16x32_bf16 v[8:11], v[160:163], v[220:223], v[8:11]
	v_mfma_f32_16x16x32_bf16 v[4:7], v[168:171], v[220:223], v[4:7]
	v_mfma_f32_16x16x32_bf16 v[56:59], v[164:167], v[196:199], v[56:59]
	v_mfma_f32_16x16x32_bf16 v[48:51], v[172:175], v[196:199], v[48:51]
	v_mfma_f32_16x16x32_bf16 v[40:43], v[164:167], v[204:207], v[40:43]
	v_mfma_f32_16x16x32_bf16 v[32:35], v[172:175], v[204:207], v[32:35]
	v_mfma_f32_16x16x32_bf16 v[24:27], v[164:167], v[212:215], v[24:27]
	v_mfma_f32_16x16x32_bf16 v[16:19], v[172:175], v[212:215], v[16:19]
	v_mfma_f32_16x16x32_bf16 v[8:11], v[164:167], v[224:227], v[8:11]
	v_mfma_f32_16x16x32_bf16 v[4:7], v[172:175], v[224:227], v[4:7]
	v_mfma_f32_16x16x32_bf16 v[60:63], v[176:179], v[192:195], v[60:63]
	v_mfma_f32_16x16x32_bf16 v[52:55], v[184:187], v[192:195], v[52:55]
	v_mfma_f32_16x16x32_bf16 v[44:47], v[176:179], v[200:203], v[44:47]
	v_mfma_f32_16x16x32_bf16 v[36:39], v[184:187], v[200:203], v[36:39]
	v_mfma_f32_16x16x32_bf16 v[28:31], v[176:179], v[208:211], v[28:31]
	v_mfma_f32_16x16x32_bf16 v[20:23], v[184:187], v[208:211], v[20:23]
	v_mfma_f32_16x16x32_bf16 v[12:15], v[176:179], v[220:223], v[12:15]
	v_mfma_f32_16x16x32_bf16 v[0:3], v[184:187], v[220:223], v[0:3]
	v_mfma_f32_16x16x32_bf16 v[60:63], v[180:183], v[196:199], v[60:63]
	v_mfma_f32_16x16x32_bf16 v[52:55], v[188:191], v[196:199], v[52:55]
	v_mfma_f32_16x16x32_bf16 v[44:47], v[180:183], v[204:207], v[44:47]
	v_mfma_f32_16x16x32_bf16 v[36:39], v[188:191], v[204:207], v[36:39]
	v_mfma_f32_16x16x32_bf16 v[28:31], v[180:183], v[212:215], v[28:31]
	v_mfma_f32_16x16x32_bf16 v[20:23], v[188:191], v[212:215], v[20:23]
	v_mfma_f32_16x16x32_bf16 v[12:15], v[180:183], v[224:227], v[12:15]
	v_mfma_f32_16x16x32_bf16 v[0:3], v[188:191], v[224:227], v[0:3]
	s_barrier
	s_add_i32 s66, s66, 2
	s_cmp_gt_u32 s66, 13
	s_mov_b64 s[2:3], s[4:5]
	s_cbranch_scc0 .LBB0_1861
	s_and_b64 vcc, exec, s[40:41]
	s_cbranch_vccz .LBB0_1864
	s_barrier

; #define PG8_STAGE(bufoff, gbase, voff) do { _Pragma("unroll") for (int _i = 0; _i < 2; ++_i) \
;         __builtin_amdgcn_global_load_lds((const __attribute__((address_space(1))) unsigned*)((const __attribute__((address_space(1))) char*)(gbase) + (unsigned)lnd_v((int)(voff)[_i])), (LAS unsigned*)(lds + (bufoff) + ldsw + _i * 8192), 16, 0, 0); } while (0)
; #define PG8_LDA(dst, b, h) do { _Pragma("unroll") for (int m = 0; m < 4; ++m) _Pragma("unroll") for (int k = 0; k < 2; ++k) dst[m][k] = *(const LAS bf16x8*)(lds + PG8_SA(b, h) + aoff + m * 2048 + k * 1024); } while (0)
; #define PG8_LDB(dst, b, h) do { _Pragma("unroll") for (int n = 0; n < 2; ++n) _Pragma("unroll") for (int k = 0; k < 2; ++k) dst[n][k] = *(const LAS bf16x8*)(lds + PG8_SB(b, h) + boff + n * 2048 + k * 1024); } while (0)
; #define PG8_WAIT_V(n) asm volatile("s_waitcnt vmcnt(" #n ")" ::: "memory")
; #define PG8_WAIT_L(n) asm volatile("s_waitcnt lgkmcnt(" #n ")" ::: "memory")
; #define PG8_BAR __builtin_amdgcn_s_barrier()
; #define PG8_SCHED __builtin_amdgcn_sched_barrier(0)
; template <class Desc, class Epi>
; __device__ __forceinline__ void gemm_phase(const int wv_, LAS unsigned char* lds, const Desc& d, const Epi& E) {
;     ...
;         for (int t = 0; t < nt; t += 2) {
;             const bool last = (t == nt - 2);
;             unsigned sA0[2], sA1[2];
;             if constexpr (Desc::GATHER) { sA0[0] = last ? voffAn[0] : voffA[0]; sA0[1] = last ? voffAn[1] : voffA[1]; sA1[0] = last ? voffAn1[0] : voffA1[0]; sA1[1] = last ? voffAn1[1] : voffA1[1]; }
;             else { sA0[0] = voffA[0]; sA0[1] = voffA[1]; sA1[0] = voffA1[0]; sA1[1] = voffA1[1]; }
;             const char* a1 = cA + (size_t)(t + 1) * kstep;
;             const char* a2 = last ? nA : cA + (size_t)(t + 2) * kstep; const char* b2 = last ? nB : cB + (size_t)(t + 2) * kstep;
;             const char* a3 = a2 + kstep; const char* b3 = b2 + kstep;
;             PG8_LDB(B0, 0, 0); PG8_LDB(B1, 0, 1); PG8_SCHED; PG8_LDA(At, 0, 0); PG8_STAGE(PG8_SA(1, 1), a1, voffA1);
;             PG8_WAIT_V(8); PG8_WAIT_L(0); PG8_BAR; PG8_MMA(0, 0, At, B0); PG8_MMA(0, 1, At, B1); PG8_BAR; PG8_SCHED;
;             PG8_LDA(At, 0, 1); PG8_STAGE(PG8_SB(0, 0), b2, voffB); PG8_STAGE(PG8_SB(0, 1), b2 + hstepB, voffB); PG8_STAGE(PG8_SA(0, 0), a2, sA0);
.LBB0_1942:
	s_add_u32 s4, s2, 0x80
	s_addc_u32 s5, s3, 0
	s_add_i32 s63, 0, 0x10000
	s_cmp_eq_u32 s62, 28
	s_cselect_b32 s5, s47, s5
	s_cselect_b32 s4, s46, s4
	v_add_u32_e32 v96, s63, v139
	s_cselect_b32 s21, s45, s43
	s_cselect_b32 s20, s44, s29
	s_add_i32 s66, 0, 0x14000
	ds_read_b128 v[150:153], v96
	ds_read_b128 v[154:157], v96 offset:1024
	ds_read_b128 v[158:161], v96 offset:2048
	ds_read_b128 v[162:165], v96 offset:3072
	v_add_u32_e32 v96, s66, v139
	ds_read_b128 v[166:169], v96
	ds_read_b128 v[170:173], v96 offset:1024
	ds_read_b128 v[174:177], v96 offset:2048
	ds_read_b128 v[178:181], v96 offset:3072
	v_mov_b32_e32 v96, v133
	ds_read_b128 v[182:185], v149
	ds_read_b128 v[186:189], v149 offset:1024
	ds_read_b128 v[190:193], v149 offset:2048
	ds_read_b128 v[194:197], v149 offset:3072
	ds_read_b128 v[198:201], v149 offset:4096
	ds_read_b128 v[202:205], v149 offset:5120
	ds_read_b128 v[206:209], v149 offset:6144
	ds_read_b128 v[210:213], v149 offset:7168
	s_add_i32 m0, s53, 0xc000
	s_nop 0
	global_load_lds_dwordx4 v96, s[2:3]
	v_mov_b32_e32 v96, v136
	s_add_i32 m0, s53, 0xe000
	s_nop 0
	global_load_lds_dwordx4 v96, s[2:3]
	s_waitcnt vmcnt(8)
	s_waitcnt lgkmcnt(0)
	s_barrier
	s_waitcnt lgkmcnt(0)
	v_mfma_f32_16x16x32_bf16 v[126:129], v[150:153], v[182:185], v[126:129]
	v_mfma_f32_16x16x32_bf16 v[122:125], v[158:161], v[182:185], v[122:125]
	v_mfma_f32_16x16x32_bf16 v[110:113], v[150:153], v[190:193], v[110:113]
	v_mfma_f32_16x16x32_bf16 v[106:109], v[158:161], v[190:193], v[106:109]
	v_mfma_f32_16x16x32_bf16 v[92:95], v[150:153], v[198:201], v[92:95]
	v_mfma_f32_16x16x32_bf16 v[88:91], v[158:161], v[198:201], v[88:91]
	v_mfma_f32_16x16x32_bf16 v[76:79], v[150:153], v[206:209], v[76:79]
	v_mfma_f32_16x16x32_bf16 v[72:75], v[158:161], v[206:209], v[72:75]
	v_mfma_f32_16x16x32_bf16 v[126:129], v[154:157], v[186:189], v[126:129]
	v_mfma_f32_16x16x32_bf16 v[122:125], v[162:165], v[186:189], v[122:125]
	v_mfma_f32_16x16x32_bf16 v[110:113], v[154:157], v[194:197], v[110:113]
	v_mfma_f32_16x16x32_bf16 v[106:109], v[162:165], v[194:197], v[106:109]
	v_mfma_f32_16x16x32_bf16 v[92:95], v[154:157], v[202:205], v[92:95]
	v_mfma_f32_16x16x32_bf16 v[88:91], v[162:165], v[202:205], v[88:91]
	v_mfma_f32_16x16x32_bf16 v[76:79], v[154:157], v[210:213], v[76:79]
	v_mfma_f32_16x16x32_bf16 v[72:75], v[162:165], v[210:213], v[72:75]
	v_mfma_f32_16x16x32_bf16 v[118:121], v[166:169], v[182:185], v[118:121]
	v_mfma_f32_16x16x32_bf16 v[114:117], v[174:177], v[182:185], v[114:117]
	v_mfma_f32_16x16x32_bf16 v[102:105], v[166:169], v[190:193], v[102:105]
	v_mfma_f32_16x16x32_bf16 v[98:101], v[174:177], v[190:193], v[98:101]
	v_mfma_f32_16x16x32_bf16 v[84:87], v[166:169], v[198:201], v[84:87]
	v_mfma_f32_16x16x32_bf16 v[80:83], v[174:177], v[198:201], v[80:83]
	v_mfma_f32_16x16x32_bf16 v[68:71], v[166:169], v[206:209], v[68:71]
	v_mfma_f32_16x16x32_bf16 v[64:67], v[174:177], v[206:209], v[64:67]
	v_mfma_f32_16x16x32_bf16 v[118:121], v[170:173], v[186:189], v[118:121]
	v_mfma_f32_16x16x32_bf16 v[114:117], v[178:181], v[186:189], v[114:117]
	v_mfma_f32_16x16x32_bf16 v[102:105], v[170:173], v[194:197], v[102:105]
	v_mfma_f32_16x16x32_bf16 v[98:101], v[178:181], v[194:197], v[98:101]
	v_mfma_f32_16x16x32_bf16 v[84:87], v[170:173], v[202:205], v[84:87]
	v_mfma_f32_16x16x32_bf16 v[80:83], v[178:181], v[202:205], v[80:83]
	v_mfma_f32_16x16x32_bf16 v[68:71], v[170:173], v[210:213], v[68:71]
	v_mfma_f32_16x16x32_bf16 v[64:67], v[178:181], v[210:213], v[64:67]
	s_barrier
	v_mov_b32_e32 v96, v134
	s_add_i32 s63, s63, s52
	ds_read_b128 v[182:185], v149 offset:16384
	ds_read_b128 v[186:189], v149 offset:17408
	ds_read_b128 v[190:193], v149 offset:18432
	ds_read_b128 v[194:197], v149 offset:19456
	ds_read_b128 v[198:201], v149 offset:20480
	ds_read_b128 v[202:205], v149 offset:21504
	ds_read_b128 v[206:209], v149 offset:22528
	ds_read_b128 v[210:213], v149 offset:23552
	s_mov_b32 m0, s63
	s_nop 0
	global_load_lds_dwordx4 v96, s[20:21]
	v_mov_b32_e32 v96, v137
	s_add_i32 m0, s63, 0x2000
	s_add_u32 s64, s20, 0x80000
	global_load_lds_dwordx4 v96, s[20:21]
	s_addc_u32 s65, s21, 0
	v_mov_b32_e32 v96, v134
	s_add_i32 s63, s66, s52
	s_mov_b32 m0, s63
	s_nop 0
	global_load_lds_dwordx4 v96, s[64:65]
	v_mov_b32_e32 v96, v137
	s_add_i32 m0, s63, 0x2000
	s_nop 0
	global_load_lds_dwordx4 v96, s[64:65]
	v_mov_b32_e32 v96, v132
	s_mov_b32 m0, s53
	s_nop 0
	global_load_lds_dwordx4 v96, s[4:5]
	v_mov_b32_e32 v96, v135
	s_mov_b32 m0, s54
	s_nop 0
	global_load_lds_dwordx4 v96, s[4:5]
	s_waitcnt vmcnt(8)
	s_waitcnt lgkmcnt(0)
	s_barrier
; #define PG8_STAGE(bufoff, gbase, voff) do { _Pragma("unroll") for (int _i = 0; _i < 2; ++_i) \
;         __builtin_amdgcn_global_load_lds((const __attribute__((address_space(1))) unsigned*)((const __attribute__((address_space(1))) char*)(gbase) + (unsigned)lnd_v((int)(voff)[_i])), (LAS unsigned*)(lds + (bufoff) + ldsw + _i * 8192), 16, 0, 0); } while (0)
; #define PG8_LDA(dst, b, h) do { _Pragma("unroll") for (int m = 0; m < 4; ++m) _Pragma("unroll") for (int k = 0; k < 2; ++k) dst[m][k] = *(const LAS bf16x8*)(lds + PG8_SA(b, h) + aoff + m * 2048 + k * 1024); } while (0)
; #define PG8_LDB(dst, b, h) do { _Pragma("unroll") for (int n = 0; n < 2; ++n) _Pragma("unroll") for (int k = 0; k < 2; ++k) dst[n][k] = *(const LAS bf16x8*)(lds + PG8_SB(b, h) + boff + n * 2048 + k * 1024); } while (0)
; #define PG8_MMA(ai, bj, At, Bt) do { __builtin_amdgcn_s_setprio(1); _Pragma("unroll") for (int m = 0; m < 4; ++m) _Pragma("unroll") for (int n = 0; n < 2; ++n) _Pragma("unroll") for (int k = 0; k < 2; ++k) \
;         acc[ai][bj][m][n] = __builtin_amdgcn_mfma_f32_16x16x32_bf16(Bt[n][k], At[m][k], acc[ai][bj][m][n], 0, 0, 0); __builtin_amdgcn_s_setprio(0); } while (0)
; #define PG8_WAIT_V(n) asm volatile("s_waitcnt vmcnt(" #n ")" ::: "memory")
; #define PG8_WAIT_L(n) asm volatile("s_waitcnt lgkmcnt(" #n ")" ::: "memory")
; #define PG8_BAR __builtin_amdgcn_s_barrier()
; #define PG8_SCHED __builtin_amdgcn_sched_barrier(0)
; template <class Desc, class Epi>
; __device__ __forceinline__ void gemm_phase(const int wv_, LAS unsigned char* lds, const Desc& d, const Epi& E) {
;     ...
;             PG8_WAIT_V(8); PG8_WAIT_L(0); PG8_BAR; PG8_MMA(1, 0, At, B0); PG8_MMA(1, 1, At, B1); PG8_BAR; PG8_SCHED;
;             PG8_LDB(B0, 1, 0); PG8_LDB(B1, 1, 1); PG8_SCHED; PG8_LDA(At, 1, 0); PG8_STAGE(PG8_SA(0, 1), a2, sA1);
;             PG8_WAIT_V(8); PG8_WAIT_L(0); PG8_BAR; PG8_MMA(0, 0, At, B0); PG8_MMA(0, 1, At, B1); PG8_BAR; PG8_SCHED;
	s_waitcnt lgkmcnt(0)
	v_mfma_f32_16x16x32_bf16 v[60:63], v[150:153], v[182:185], v[60:63]
	v_mfma_f32_16x16x32_bf16 v[56:59], v[158:161], v[182:185], v[56:59]
	v_mfma_f32_16x16x32_bf16 v[44:47], v[150:153], v[190:193], v[44:47]
	v_mfma_f32_16x16x32_bf16 v[32:35], v[158:161], v[190:193], v[32:35]
	v_mfma_f32_16x16x32_bf16 v[16:19], v[150:153], v[198:201], v[16:19]
	v_mfma_f32_16x16x32_bf16 v[8:11], v[158:161], v[198:201], v[8:11]
	v_mfma_f32_16x16x32_bf16 v[4:7], v[150:153], v[206:209], v[4:7]
	v_mfma_f32_16x16x32_bf16 v[0:3], v[158:161], v[206:209], v[0:3]
	v_mfma_f32_16x16x32_bf16 v[60:63], v[154:157], v[186:189], v[60:63]
	v_mfma_f32_16x16x32_bf16 v[56:59], v[162:165], v[186:189], v[56:59]
	v_mfma_f32_16x16x32_bf16 v[44:47], v[154:157], v[194:197], v[44:47]
	v_mfma_f32_16x16x32_bf16 v[32:35], v[162:165], v[194:197], v[32:35]
	v_mfma_f32_16x16x32_bf16 v[16:19], v[154:157], v[202:205], v[16:19]
	v_mfma_f32_16x16x32_bf16 v[8:11], v[162:165], v[202:205], v[8:11]
	v_mfma_f32_16x16x32_bf16 v[4:7], v[154:157], v[210:213], v[4:7]
	v_mfma_f32_16x16x32_bf16 v[0:3], v[162:165], v[210:213], v[0:3]
	v_mfma_f32_16x16x32_bf16 v[52:55], v[166:169], v[182:185], v[52:55]
	v_mfma_f32_16x16x32_bf16 v[48:51], v[174:177], v[182:185], v[48:51]
	v_mfma_f32_16x16x32_bf16 v[28:31], v[166:169], v[190:193], v[28:31]
	v_mfma_f32_16x16x32_bf16 v[12:15], v[174:177], v[190:193], v[12:15]
	v_mfma_f32_16x16x32_bf16 v[36:39], v[166:169], v[198:201], v[36:39]
	v_mfma_f32_16x16x32_bf16 v[40:43], v[174:177], v[198:201], v[40:43]
	v_mfma_f32_16x16x32_bf16 v[20:23], v[166:169], v[206:209], v[20:23]
	v_mfma_f32_16x16x32_bf16 v[24:27], v[174:177], v[206:209], v[24:27]
	v_mfma_f32_16x16x32_bf16 v[52:55], v[170:173], v[186:189], v[52:55]
	v_mfma_f32_16x16x32_bf16 v[48:51], v[178:181], v[186:189], v[48:51]
	v_mfma_f32_16x16x32_bf16 v[28:31], v[170:173], v[194:197], v[28:31]
	v_mfma_f32_16x16x32_bf16 v[12:15], v[178:181], v[194:197], v[12:15]
	v_mfma_f32_16x16x32_bf16 v[36:39], v[170:173], v[202:205], v[36:39]
	v_mfma_f32_16x16x32_bf16 v[40:43], v[178:181], v[202:205], v[40:43]
	v_mfma_f32_16x16x32_bf16 v[20:23], v[170:173], v[210:213], v[20:23]
	v_mfma_f32_16x16x32_bf16 v[24:27], v[178:181], v[210:213], v[24:27]
	s_barrier
	s_add_i32 s63, 0, 0x18000
	v_add_u32_e32 v96, s63, v139
	s_add_i32 s64, 0, 0x1c000
	ds_read_b128 v[150:153], v96
	ds_read_b128 v[154:157], v96 offset:1024
	ds_read_b128 v[158:161], v96 offset:2048
	ds_read_b128 v[162:165], v96 offset:3072
	v_add_u32_e32 v96, s64, v139
	ds_read_b128 v[166:169], v96
	ds_read_b128 v[170:173], v96 offset:1024
	ds_read_b128 v[174:177], v96 offset:2048
	ds_read_b128 v[178:181], v96 offset:3072
	v_mov_b32_e32 v96, v133
	s_mov_b32 m0, s55
	ds_read_b128 v[182:185], v149 offset:32768
	ds_read_b128 v[186:189], v149 offset:33792
	ds_read_b128 v[190:193], v149 offset:34816
	ds_read_b128 v[194:197], v149 offset:35840
	ds_read_b128 v[198:201], v149 offset:36864
	ds_read_b128 v[202:205], v149 offset:37888
	ds_read_b128 v[206:209], v149 offset:38912
	ds_read_b128 v[210:213], v149 offset:39936
	s_nop 0
	global_load_lds_dwordx4 v96, s[4:5]
	v_mov_b32_e32 v96, v136
	s_mov_b32 m0, s56
	s_nop 0
	global_load_lds_dwordx4 v96, s[4:5]
	s_waitcnt vmcnt(8)
	s_waitcnt lgkmcnt(0)
	s_barrier
	s_waitcnt lgkmcnt(0)
	v_mfma_f32_16x16x32_bf16 v[126:129], v[150:153], v[182:185], v[126:129]
	v_mfma_f32_16x16x32_bf16 v[122:125], v[158:161], v[182:185], v[122:125]
	v_mfma_f32_16x16x32_bf16 v[110:113], v[150:153], v[190:193], v[110:113]
	v_mfma_f32_16x16x32_bf16 v[106:109], v[158:161], v[190:193], v[106:109]
	v_mfma_f32_16x16x32_bf16 v[92:95], v[150:153], v[198:201], v[92:95]
	v_mfma_f32_16x16x32_bf16 v[88:91], v[158:161], v[198:201], v[88:91]
	v_mfma_f32_16x16x32_bf16 v[76:79], v[150:153], v[206:209], v[76:79]
	v_mfma_f32_16x16x32_bf16 v[72:75], v[158:161], v[206:209], v[72:75]
	v_mfma_f32_16x16x32_bf16 v[126:129], v[154:157], v[186:189], v[126:129]
	v_mfma_f32_16x16x32_bf16 v[122:125], v[162:165], v[186:189], v[122:125]
	v_mfma_f32_16x16x32_bf16 v[110:113], v[154:157], v[194:197], v[110:113]
	v_mfma_f32_16x16x32_bf16 v[106:109], v[162:165], v[194:197], v[106:109]
	v_mfma_f32_16x16x32_bf16 v[92:95], v[154:157], v[202:205], v[92:95]
	v_mfma_f32_16x16x32_bf16 v[88:91], v[162:165], v[202:205], v[88:91]
	v_mfma_f32_16x16x32_bf16 v[76:79], v[154:157], v[210:213], v[76:79]
	v_mfma_f32_16x16x32_bf16 v[72:75], v[162:165], v[210:213], v[72:75]
	v_mfma_f32_16x16x32_bf16 v[118:121], v[166:169], v[182:185], v[118:121]
	v_mfma_f32_16x16x32_bf16 v[114:117], v[174:177], v[182:185], v[114:117]
	v_mfma_f32_16x16x32_bf16 v[102:105], v[166:169], v[190:193], v[102:105]
	v_mfma_f32_16x16x32_bf16 v[98:101], v[174:177], v[190:193], v[98:101]
	v_mfma_f32_16x16x32_bf16 v[84:87], v[166:169], v[198:201], v[84:87]
	v_mfma_f32_16x16x32_bf16 v[80:83], v[174:177], v[198:201], v[80:83]
	v_mfma_f32_16x16x32_bf16 v[68:71], v[166:169], v[206:209], v[68:71]
	v_mfma_f32_16x16x32_bf16 v[64:67], v[174:177], v[206:209], v[64:67]
	v_mfma_f32_16x16x32_bf16 v[118:121], v[170:173], v[186:189], v[118:121]
	v_mfma_f32_16x16x32_bf16 v[114:117], v[178:181], v[186:189], v[114:117]
	v_mfma_f32_16x16x32_bf16 v[102:105], v[170:173], v[194:197], v[102:105]
	v_mfma_f32_16x16x32_bf16 v[98:101], v[178:181], v[194:197], v[98:101]
	v_mfma_f32_16x16x32_bf16 v[84:87], v[170:173], v[202:205], v[84:87]
	v_mfma_f32_16x16x32_bf16 v[80:83], v[178:181], v[202:205], v[80:83]
	v_mfma_f32_16x16x32_bf16 v[68:71], v[170:173], v[210:213], v[68:71]
	v_mfma_f32_16x16x32_bf16 v[64:67], v[178:181], v[210:213], v[64:67]
	s_barrier
; #define PG8_STAGE(bufoff, gbase, voff) do { _Pragma("unroll") for (int _i = 0; _i < 2; ++_i) \
;         __builtin_amdgcn_global_load_lds((const __attribute__((address_space(1))) unsigned*)((const __attribute__((address_space(1))) char*)(gbase) + (unsigned)lnd_v((int)(voff)[_i])), (LAS unsigned*)(lds + (bufoff) + ldsw + _i * 8192), 16, 0, 0); } while (0)
; #define PG8_LDA(dst, b, h) do { _Pragma("unroll") for (int m = 0; m < 4; ++m) _Pragma("unroll") for (int k = 0; k < 2; ++k) dst[m][k] = *(const LAS bf16x8*)(lds + PG8_SA(b, h) + aoff + m * 2048 + k * 1024); } while (0)
; #define PG8_MMA(ai, bj, At, Bt) do { __builtin_amdgcn_s_setprio(1); _Pragma("unroll") for (int m = 0; m < 4; ++m) _Pragma("unroll") for (int n = 0; n < 2; ++n) _Pragma("unroll") for (int k = 0; k < 2; ++k) \
;         acc[ai][bj][m][n] = __builtin_amdgcn_mfma_f32_16x16x32_bf16(Bt[n][k], At[m][k], acc[ai][bj][m][n], 0, 0, 0); __builtin_amdgcn_s_setprio(0); } while (0)
; #define PG8_WAIT_V(n) asm volatile("s_waitcnt vmcnt(" #n ")" ::: "memory")
; #define PG8_WAIT_L(n) asm volatile("s_waitcnt lgkmcnt(" #n ")" ::: "memory")
; #define PG8_BAR __builtin_amdgcn_s_barrier()
; #define PG8_SCHED __builtin_amdgcn_sched_barrier(0)
; template <class Desc, class Epi>
; __device__ __forceinline__ void gemm_phase(const int wv_, LAS unsigned char* lds, const Desc& d, const Epi& E) {
;     ...
;             PG8_LDA(At, 1, 1); PG8_STAGE(PG8_SB(1, 0), b3, voffB); PG8_STAGE(PG8_SB(1, 1), b3 + hstepB, voffB); PG8_STAGE(PG8_SA(1, 0), a3, sA0);
;             PG8_WAIT_V(8); PG8_WAIT_L(0); PG8_BAR; PG8_MMA(1, 0, At, B0); PG8_MMA(1, 1, At, B1); PG8_BAR; PG8_SCHED;
;         }
;         if (wr == 0) PG8_BAR;
	v_mov_b32_e32 v96, v134
	ds_read_b128 v[182:185], v149 offset:49152
	ds_read_b128 v[186:189], v149 offset:50176
	ds_read_b128 v[190:193], v149 offset:51200
	ds_read_b128 v[194:197], v149 offset:52224
	ds_read_b128 v[198:201], v149 offset:53248
	ds_read_b128 v[202:205], v149 offset:54272
	ds_read_b128 v[206:209], v149 offset:55296
	ds_read_b128 v[210:213], v149 offset:56320
	s_add_i32 s63, s63, s52
	v_lshl_add_u64 v[130:131], s[20:21], 0, v[96:97]
	v_lshl_add_u64 v[130:131], v[130:131], 0, s[30:31]
	s_mov_b32 m0, s63
	v_mov_b32_e32 v96, v137
	global_load_lds_dwordx4 v[130:131], off
	s_add_i32 m0, s63, 0x2000
	s_nop 0
	v_lshl_add_u64 v[130:131], s[20:21], 0, v[96:97]
	s_add_u32 s20, s20, 0x80080
	v_lshl_add_u64 v[130:131], v[130:131], 0, s[30:31]
	s_addc_u32 s21, s21, 0
	v_mov_b32_e32 v96, v134
	s_add_i32 s63, s64, s52
	global_load_lds_dwordx4 v[130:131], off
	s_mov_b32 m0, s63
	s_nop 0
	global_load_lds_dwordx4 v96, s[20:21]
	v_mov_b32_e32 v96, v137
	s_add_i32 m0, s63, 0x2000
	s_nop 0
	global_load_lds_dwordx4 v96, s[20:21]
	v_mov_b32_e32 v96, v132
	s_mov_b32 m0, s57
	v_lshl_add_u64 v[130:131], s[4:5], 0, v[96:97]
	v_lshl_add_u64 v[130:131], v[130:131], 0, s[30:31]
	v_mov_b32_e32 v96, v135
	global_load_lds_dwordx4 v[130:131], off
	s_mov_b32 m0, s58
	v_lshl_add_u64 v[130:131], s[4:5], 0, v[96:97]
	v_lshl_add_u64 v[130:131], v[130:131], 0, s[30:31]
	global_load_lds_dwordx4 v[130:131], off
	s_waitcnt vmcnt(8)
	s_waitcnt lgkmcnt(0)
	s_barrier
	s_waitcnt lgkmcnt(0)
	v_mfma_f32_16x16x32_bf16 v[60:63], v[150:153], v[182:185], v[60:63]
	v_mfma_f32_16x16x32_bf16 v[56:59], v[158:161], v[182:185], v[56:59]
	v_mfma_f32_16x16x32_bf16 v[44:47], v[150:153], v[190:193], v[44:47]
	v_mfma_f32_16x16x32_bf16 v[32:35], v[158:161], v[190:193], v[32:35]
	v_mfma_f32_16x16x32_bf16 v[16:19], v[150:153], v[198:201], v[16:19]
	v_mfma_f32_16x16x32_bf16 v[8:11], v[158:161], v[198:201], v[8:11]
	v_mfma_f32_16x16x32_bf16 v[4:7], v[150:153], v[206:209], v[4:7]
	v_mfma_f32_16x16x32_bf16 v[0:3], v[158:161], v[206:209], v[0:3]
	v_mfma_f32_16x16x32_bf16 v[60:63], v[154:157], v[186:189], v[60:63]
	v_mfma_f32_16x16x32_bf16 v[56:59], v[162:165], v[186:189], v[56:59]
	v_mfma_f32_16x16x32_bf16 v[44:47], v[154:157], v[194:197], v[44:47]
	v_mfma_f32_16x16x32_bf16 v[32:35], v[162:165], v[194:197], v[32:35]
	v_mfma_f32_16x16x32_bf16 v[16:19], v[154:157], v[202:205], v[16:19]
	v_mfma_f32_16x16x32_bf16 v[8:11], v[162:165], v[202:205], v[8:11]
	v_mfma_f32_16x16x32_bf16 v[4:7], v[154:157], v[210:213], v[4:7]
	v_mfma_f32_16x16x32_bf16 v[0:3], v[162:165], v[210:213], v[0:3]
	v_mfma_f32_16x16x32_bf16 v[52:55], v[166:169], v[182:185], v[52:55]
	v_mfma_f32_16x16x32_bf16 v[48:51], v[174:177], v[182:185], v[48:51]
	v_mfma_f32_16x16x32_bf16 v[28:31], v[166:169], v[190:193], v[28:31]
	v_mfma_f32_16x16x32_bf16 v[12:15], v[174:177], v[190:193], v[12:15]
	v_mfma_f32_16x16x32_bf16 v[36:39], v[166:169], v[198:201], v[36:39]
	v_mfma_f32_16x16x32_bf16 v[40:43], v[174:177], v[198:201], v[40:43]
	v_mfma_f32_16x16x32_bf16 v[20:23], v[166:169], v[206:209], v[20:23]
	v_mfma_f32_16x16x32_bf16 v[24:27], v[174:177], v[206:209], v[24:27]
	v_mfma_f32_16x16x32_bf16 v[52:55], v[170:173], v[186:189], v[52:55]
	v_mfma_f32_16x16x32_bf16 v[48:51], v[178:181], v[186:189], v[48:51]
	v_mfma_f32_16x16x32_bf16 v[28:31], v[170:173], v[194:197], v[28:31]
	v_mfma_f32_16x16x32_bf16 v[12:15], v[178:181], v[194:197], v[12:15]
	v_mfma_f32_16x16x32_bf16 v[36:39], v[170:173], v[202:205], v[36:39]
	v_mfma_f32_16x16x32_bf16 v[40:43], v[178:181], v[202:205], v[40:43]
	v_mfma_f32_16x16x32_bf16 v[20:23], v[170:173], v[210:213], v[20:23]
	v_mfma_f32_16x16x32_bf16 v[24:27], v[178:181], v[210:213], v[24:27]
	s_barrier
	s_add_i32 s62, s62, 2
	s_add_u32 s2, s2, 0x100
	s_addc_u32 s3, s3, 0
	s_add_u32 s29, s29, 0x100
	s_addc_u32 s43, s43, 0
	s_cmp_gt_u32 s62, 29
	s_cbranch_scc0 .LBB0_1942
	s_and_b64 vcc, exec, s[40:41]
	s_cbranch_vccz .LBB0_1945
	s_barrier
